# GEMM_OUT epilogues: residual-stream rows prefetched several loads ahead into spare fragment registers (was one load-wait round trip per row group)
# speedup vs baseline: 1.0158x; 1.0158x over previous
.LBB0_565:
	s_lshl_b64 s[34:35], s[36:37], 11
	s_lshl_b64 s[8:9], s[8:9], 2
	v_bfe_u32 v152, v88, 6, 2
	v_bfe_u32 v193, v88, 4, 2
	s_add_u32 s8, s10, s8
	v_and_b32_e32 v192, 15, v88
	s_addc_u32 s9, s11, s9
	v_ashrrev_i32_e32 v92, 2, v88
	s_lshl_b32 s1, s0, 8
	v_lshlrev_b32_e32 v88, 5, v152
	v_lshlrev_b32_e32 v89, 3, v193
	v_or3_b32 v158, v88, s1, v89
	v_ashrrev_i32_e32 v159, 31, v158
	v_lshl_add_u64 v[88:89], v[158:159], 2, s[8:9]
	s_movk_i32 s1, 0x6000
	v_add_co_u32_e32 v90, vcc, s1, v88
	s_movk_i32 s1, 0xffc0
	v_and_or_b32 v160, v92, s1, v192
	v_addc_co_u32_e32 v91, vcc, 0, v89, vcc
	v_ashrrev_i32_e32 v161, 31, v160
	global_load_dwordx4 v[104:107], v[90:91], off
	v_lshlrev_b64 v[90:91], 10, v[160:161]
	v_lshl_add_u64 v[90:91], v[90:91], 0, v[158:159]
	s_mov_b64 s[8:9], 0x6000
	v_lshl_add_u64 v[188:189], v[90:91], 2, s[2:3]
	v_lshl_add_u64 v[92:93], v[88:89], 0, s[8:9]
	v_mov_b32_e32 v194, v188
	v_mov_b32_e32 v195, v189
	global_load_dwordx4 v[196:199], v[194:195], off offset:16
	global_load_dwordx4 v[200:203], v[194:195], off
	global_load_dwordx4 v[204:207], v[194:195], off offset:512
	global_load_dwordx4 v[212:215], v[194:195], off offset:528
	s_mov_b32 s98, 0x10000
	s_mov_b32 s99, 0
	v_lshl_add_u64 v[210:211], v[194:195], 0, s[98:99]
	global_load_dwordx4 v[216:219], v[210:211], off
	s_mov_b32 s98, 0x10000
	s_mov_b32 s99, 0
	v_lshl_add_u64 v[210:211], v[194:195], 0, s[98:99]
	global_load_dwordx4 v[220:223], v[210:211], off offset:16
	s_mov_b32 s98, 0x10000
	s_mov_b32 s99, 0
	v_lshl_add_u64 v[210:211], v[194:195], 0, s[98:99]
	global_load_dwordx4 v[244:247], v[210:211], off offset:512
	global_load_dwordx4 v[108:111], v[92:93], off offset:16
	s_add_u32 s34, s59, s34
	s_addc_u32 s35, s60, s35
	v_lshl_add_u64 v[190:191], v[90:91], 1, s[34:35]
	global_load_dwordx4 v[88:91], v[92:93], off offset:528
	s_nop 0
	global_load_dwordx4 v[92:95], v[92:93], off offset:512
	s_movk_i32 s1, 0x80
	s_lshl_b32 s0, s0, 2
	v_cmp_eq_u32_e64 s[8:9], 0, v193
	s_and_b32 s25, s0, 12
	v_lshlrev_b32_e32 v152, 2, v152
	s_waitcnt vmcnt(10)
	s_waitcnt vmcnt(8)
	v_pk_fma_f32 v[142:143], v[142:143], v[106:107], v[202:203]
	v_pk_fma_f32 v[140:141], v[140:141], v[104:105], v[200:201]
	s_waitcnt vmcnt(2)
	v_pk_fma_f32 v[182:183], v[138:139], v[110:111], v[198:199]
	v_pk_fma_f32 v[136:137], v[136:137], v[108:109], v[196:197]
	v_cvt_pk_bf16_f32 v138, v140, v141
	v_cvt_pk_bf16_f32 v139, v142, v143
	v_cvt_pk_bf16_f32 v140, v136, v137
	v_cvt_pk_bf16_f32 v141, v182, v183
	global_store_dwordx4 v[190:191], v[138:141], off
	s_mov_b32 s98, 0x10000
	s_mov_b32 s99, 0
	v_lshl_add_u64 v[210:211], v[194:195], 0, s[98:99]
	global_load_dwordx4 v[196:199], v[210:211], off offset:528
	s_mov_b32 s98, 0x20000
	s_mov_b32 s99, 0
	v_lshl_add_u64 v[210:211], v[194:195], 0, s[98:99]
	global_load_dwordx4 v[200:203], v[210:211], off
	v_lshlrev_b32_e32 v143, 16, v138
	v_and_b32_e32 v138, 0xffff0000, v138
	v_lshlrev_b32_e32 v188, 16, v139
	v_and_b32_e32 v139, 0xffff0000, v139
	v_lshlrev_b32_e32 v189, 16, v140
	v_and_b32_e32 v140, 0xffff0000, v140
	v_mul_f32_e32 v138, v138, v138
	v_mul_f32_e32 v139, v139, v139
	v_lshlrev_b32_e32 v142, 2, v192
	v_lshlrev_b32_e32 v192, 16, v141
	v_and_b32_e32 v141, 0xffff0000, v141
	v_mul_f32_e32 v140, v140, v140
	v_fmac_f32_e32 v138, v143, v143
	v_fmac_f32_e32 v139, v188, v188
	v_mul_f32_e32 v141, v141, v141
	v_fmac_f32_e32 v140, v189, v189
	v_add_f32_e32 v138, v138, v139
	v_fmac_f32_e32 v141, v192, v192
	v_add_f32_e32 v138, v138, v140
	v_add_f32_e32 v143, v141, v138
	v_lshlrev_b32_e32 v137, 6, v193
	v_bitop3_b32 v136, v137, 64, v142 bitop3:0x36
	s_waitcnt vmcnt(3)
	v_pk_fma_f32 v[132:133], v[132:133], v[92:93], v[204:205]
	v_pk_fma_f32 v[134:135], v[134:135], v[94:95], v[206:207]
	v_pk_fma_f32 v[128:129], v[128:129], v[88:89], v[212:213]
	v_cvt_pk_bf16_f32 v138, v132, v133
	v_pk_fma_f32 v[130:131], v[130:131], v[90:91], v[214:215]
	v_cvt_pk_bf16_f32 v139, v134, v135
	v_cvt_pk_bf16_f32 v140, v128, v129
	v_and_b32_e32 v129, 0xffff0000, v138
	v_cvt_pk_bf16_f32 v141, v130, v131
	v_lshlrev_b32_e32 v128, 16, v138
	v_and_b32_e32 v131, 0xffff0000, v139
	v_mul_f32_e32 v129, v129, v129
	v_lshlrev_b32_e32 v130, 16, v139
	v_and_b32_e32 v133, 0xffff0000, v140
	v_mul_f32_e32 v131, v131, v131
	v_fmac_f32_e32 v129, v128, v128
	v_lshlrev_b32_e32 v132, 16, v140
	v_and_b32_e32 v135, 0xffff0000, v141
	v_mul_f32_e32 v133, v133, v133
	v_fmac_f32_e32 v131, v130, v130
	v_add_f32_e32 v128, v143, v129
	v_lshlrev_b32_e32 v134, 16, v141
	v_mul_f32_e32 v135, v135, v135
	v_fmac_f32_e32 v133, v132, v132
	v_add_f32_e32 v128, v131, v128
	v_fmac_f32_e32 v135, v134, v134
	v_add_f32_e32 v128, v133, v128
	v_add_f32_e32 v129, v135, v128
	ds_bpermute_b32 v131, v136, v129
	v_bitop3_b32 v130, v137, s1, v142 bitop3:0x36
	v_add_u32_e32 v128, s36, v160
	global_store_dwordx4 v[190:191], v[138:141], off offset:256
	s_waitcnt lgkmcnt(0)
	v_add_f32_e32 v131, v129, v131
	ds_bpermute_b32 v132, v130, v131
	v_ashrrev_i32_e32 v129, 31, v128
	s_and_saveexec_b64 s[0:1], s[8:9]
	s_cbranch_execz .LBB0_567
	s_waitcnt lgkmcnt(0)
	v_add_f32_e32 v131, v131, v132
	v_lshlrev_b64 v[132:133], 6, v[128:129]
	v_lshl_add_u64 v[132:133], s[22:23], 0, v[132:133]
	s_lshl_b32 s20, s25, 2
	v_lshl_add_u64 v[132:133], v[132:133], 0, s[20:21]
	v_lshl_add_u64 v[132:133], v[132:133], 0, v[152:153]
	global_store_dword v[132:133], v131, off
.LBB0_567:
	s_or_b64 exec, exec, s[0:1]
	s_waitcnt lgkmcnt(0)
	v_or_b32_e32 v132, 16, v160
	v_ashrrev_i32_e32 v133, 31, v132
	v_lshlrev_b64 v[132:133], 10, v[132:133]
	v_lshl_add_u64 v[142:143], v[132:133], 0, v[158:159]
	v_lshl_add_u64 v[180:181], v[142:143], 2, s[2:3]
	s_mov_b32 s98, 0x20000
	s_mov_b32 s99, 0
	v_lshl_add_u64 v[210:211], v[194:195], 0, s[98:99]
	global_load_dwordx4 v[204:207], v[210:211], off offset:16
	s_mov_b32 s98, 0x20000
	s_mov_b32 s99, 0
	v_lshl_add_u64 v[210:211], v[194:195], 0, s[98:99]
	global_load_dwordx4 v[212:215], v[210:211], off offset:512
	v_lshl_add_u64 v[142:143], v[142:143], 1, s[34:35]
	s_waitcnt vmcnt(11)
	v_pk_fma_f32 v[126:127], v[126:127], v[106:107], v[218:219]
	v_pk_fma_f32 v[124:125], v[124:125], v[104:105], v[216:217]
	s_waitcnt vmcnt(10)
	v_pk_fma_f32 v[132:133], v[122:123], v[110:111], v[222:223]
	v_pk_fma_f32 v[122:123], v[120:121], v[108:109], v[220:221]
	v_cvt_pk_bf16_f32 v120, v124, v125
	v_cvt_pk_bf16_f32 v121, v126, v127
	v_cvt_pk_bf16_f32 v122, v122, v123
	v_cvt_pk_bf16_f32 v123, v132, v133
	global_store_dwordx4 v[142:143], v[120:123], off
	s_mov_b32 s98, 0x20000
	s_mov_b32 s99, 0
	v_lshl_add_u64 v[210:211], v[194:195], 0, s[98:99]
	global_load_dwordx4 v[216:219], v[210:211], off offset:528
	s_mov_b32 s98, 0x30000
	s_mov_b32 s99, 0
	v_lshl_add_u64 v[210:211], v[194:195], 0, s[98:99]
	global_load_dwordx4 v[220:223], v[210:211], off
	v_lshlrev_b32_e32 v131, 16, v120
	v_and_b32_e32 v120, 0xffff0000, v120
	v_lshlrev_b32_e32 v137, 16, v121
	v_and_b32_e32 v121, 0xffff0000, v121
	v_lshlrev_b32_e32 v138, 16, v122
	v_and_b32_e32 v122, 0xffff0000, v122
	v_mul_f32_e32 v120, v120, v120
	v_mul_f32_e32 v121, v121, v121
	v_lshlrev_b32_e32 v139, 16, v123
	v_and_b32_e32 v123, 0xffff0000, v123
	v_mul_f32_e32 v122, v122, v122
	v_fmac_f32_e32 v120, v131, v131
	v_fmac_f32_e32 v121, v137, v137
	v_mul_f32_e32 v123, v123, v123
	v_fmac_f32_e32 v122, v138, v138
	v_add_f32_e32 v120, v120, v121
	v_fmac_f32_e32 v123, v139, v139
	v_add_f32_e32 v120, v120, v122
	v_add_f32_e32 v122, v123, v120
	s_waitcnt vmcnt(12)
	v_pk_fma_f32 v[116:117], v[116:117], v[92:93], v[244:245]
	v_pk_fma_f32 v[118:119], v[118:119], v[94:95], v[246:247]
	s_waitcnt vmcnt(7)
	v_pk_fma_f32 v[120:121], v[114:115], v[90:91], v[198:199]
	v_pk_fma_f32 v[112:113], v[112:113], v[88:89], v[196:197]
	v_cvt_pk_bf16_f32 v114, v116, v117
	v_cvt_pk_bf16_f32 v115, v118, v119
	v_cvt_pk_bf16_f32 v116, v112, v113
	v_and_b32_e32 v113, 0xffff0000, v114
	v_lshlrev_b32_e32 v112, 16, v114
	v_and_b32_e32 v119, 0xffff0000, v115
	v_mul_f32_e32 v113, v113, v113
	v_cvt_pk_bf16_f32 v117, v120, v121
	v_lshlrev_b32_e32 v118, 16, v115
	v_and_b32_e32 v121, 0xffff0000, v116
	v_mul_f32_e32 v119, v119, v119
	v_fmac_f32_e32 v113, v112, v112
	v_lshlrev_b32_e32 v120, 16, v116
	v_and_b32_e32 v124, 0xffff0000, v117
	v_mul_f32_e32 v121, v121, v121
	v_fmac_f32_e32 v119, v118, v118
	v_add_f32_e32 v112, v122, v113
	v_lshlrev_b32_e32 v123, 16, v117
	v_mul_f32_e32 v124, v124, v124
	v_fmac_f32_e32 v121, v120, v120
	v_add_f32_e32 v112, v119, v112
	v_add_f32_e32 v112, v121, v112
	v_fmac_f32_e32 v124, v123, v123
	v_add_f32_e32 v112, v124, v112
	ds_bpermute_b32 v113, v136, v112
	global_store_dwordx4 v[142:143], v[114:117], off offset:256
	s_waitcnt lgkmcnt(0)
	v_add_f32_e32 v112, v112, v113
	ds_bpermute_b32 v113, v130, v112
	s_and_saveexec_b64 s[0:1], s[8:9]
	s_cbranch_execz .LBB0_569
	s_waitcnt lgkmcnt(0)
	v_add_f32_e32 v114, v112, v113
	v_or_b32_e32 v112, 16, v128
	v_ashrrev_i32_e32 v113, 31, v112
	v_lshlrev_b64 v[112:113], 6, v[112:113]
	v_lshl_add_u64 v[112:113], s[22:23], 0, v[112:113]
	s_lshl_b32 s20, s25, 2
	v_lshl_add_u64 v[112:113], v[112:113], 0, s[20:21]
	v_lshl_add_u64 v[112:113], v[112:113], 0, v[152:153]
	global_store_dword v[112:113], v114, off
.LBB0_569:
	s_or_b64 exec, exec, s[0:1]
	v_or_b32_e32 v112, 32, v160
	s_waitcnt lgkmcnt(0)
	v_ashrrev_i32_e32 v113, 31, v112
	v_lshlrev_b64 v[112:113], 10, v[112:113]
	v_lshl_add_u64 v[120:121], v[112:113], 0, v[158:159]
	v_lshl_add_u64 v[122:123], v[120:121], 2, s[2:3]
	s_mov_b32 s98, 0x30000
	s_mov_b32 s99, 0
	v_lshl_add_u64 v[210:211], v[194:195], 0, s[98:99]
	global_load_dwordx4 v[244:247], v[210:211], off offset:16
	s_mov_b32 s98, 0x30000
	s_mov_b32 s99, 0
	v_lshl_add_u64 v[210:211], v[194:195], 0, s[98:99]
	global_load_dwordx4 v[196:199], v[210:211], off offset:512
	v_lshl_add_u64 v[120:121], v[120:121], 1, s[34:35]
	s_waitcnt vmcnt(9)
	v_pk_fma_f32 v[102:103], v[102:103], v[106:107], v[202:203]
	v_pk_fma_f32 v[100:101], v[100:101], v[104:105], v[200:201]
	s_waitcnt vmcnt(7)
	v_pk_fma_f32 v[112:113], v[98:99], v[110:111], v[206:207]
	v_pk_fma_f32 v[98:99], v[96:97], v[108:109], v[204:205]
	v_cvt_pk_bf16_f32 v96, v100, v101
	v_cvt_pk_bf16_f32 v97, v102, v103
	v_cvt_pk_bf16_f32 v98, v98, v99
	v_cvt_pk_bf16_f32 v99, v112, v113
	global_store_dwordx4 v[120:121], v[96:99], off
	s_mov_b32 s98, 0x30000
	s_mov_b32 s99, 0
	v_lshl_add_u64 v[210:211], v[194:195], 0, s[98:99]
	global_load_dwordx4 v[200:203], v[210:211], off offset:528
	s_mov_b32 s98, 0x80000
	s_mov_b32 s99, 0
	v_lshl_add_u64 v[210:211], v[194:195], 0, s[98:99]
	global_load_dwordx4 v[204:207], v[210:211], off
	v_lshlrev_b32_e32 v116, 16, v96
	v_and_b32_e32 v96, 0xffff0000, v96
	v_lshlrev_b32_e32 v117, 16, v97
	v_and_b32_e32 v97, 0xffff0000, v97
	v_lshlrev_b32_e32 v118, 16, v98
	v_and_b32_e32 v98, 0xffff0000, v98
	v_mul_f32_e32 v96, v96, v96
	v_mul_f32_e32 v97, v97, v97
	v_lshlrev_b32_e32 v119, 16, v99
	v_and_b32_e32 v99, 0xffff0000, v99
	v_mul_f32_e32 v98, v98, v98
	v_fmac_f32_e32 v96, v116, v116
	v_fmac_f32_e32 v97, v117, v117
	v_mul_f32_e32 v99, v99, v99
	v_fmac_f32_e32 v98, v118, v118
	v_add_f32_e32 v96, v96, v97
	v_fmac_f32_e32 v99, v119, v119
	v_add_f32_e32 v96, v96, v98
	v_add_f32_e32 v98, v99, v96
	s_waitcnt vmcnt(9)
	v_pk_fma_f32 v[84:85], v[84:85], v[92:93], v[212:213]
	v_pk_fma_f32 v[86:87], v[86:87], v[94:95], v[214:215]
	s_waitcnt vmcnt(7)
	v_pk_fma_f32 v[96:97], v[82:83], v[90:91], v[218:219]
	v_pk_fma_f32 v[80:81], v[80:81], v[88:89], v[216:217]
	v_cvt_pk_bf16_f32 v82, v84, v85
	v_cvt_pk_bf16_f32 v83, v86, v87
	v_cvt_pk_bf16_f32 v84, v80, v81
	v_and_b32_e32 v81, 0xffff0000, v82
	v_lshlrev_b32_e32 v80, 16, v82
	v_and_b32_e32 v87, 0xffff0000, v83
	v_mul_f32_e32 v81, v81, v81
	v_cvt_pk_bf16_f32 v85, v96, v97
	v_lshlrev_b32_e32 v86, 16, v83
	v_and_b32_e32 v97, 0xffff0000, v84
	v_mul_f32_e32 v87, v87, v87
	v_fmac_f32_e32 v81, v80, v80
	v_lshlrev_b32_e32 v96, 16, v84
	v_and_b32_e32 v100, 0xffff0000, v85
	v_mul_f32_e32 v97, v97, v97
	v_fmac_f32_e32 v87, v86, v86
	v_add_f32_e32 v80, v98, v81
	v_lshlrev_b32_e32 v99, 16, v85
	v_mul_f32_e32 v100, v100, v100
	v_fmac_f32_e32 v97, v96, v96
	v_add_f32_e32 v80, v87, v80
	v_add_f32_e32 v80, v97, v80
	v_fmac_f32_e32 v100, v99, v99
	v_add_f32_e32 v80, v100, v80
	ds_bpermute_b32 v81, v136, v80
	global_store_dwordx4 v[120:121], v[82:85], off offset:256
	s_waitcnt lgkmcnt(0)
	v_add_f32_e32 v80, v80, v81
	ds_bpermute_b32 v81, v130, v80
	s_and_saveexec_b64 s[0:1], s[8:9]
	s_cbranch_execz .LBB0_571
	s_waitcnt lgkmcnt(0)
	v_add_f32_e32 v82, v80, v81
	v_or_b32_e32 v80, 32, v128
	v_ashrrev_i32_e32 v81, 31, v80
	v_lshlrev_b64 v[80:81], 6, v[80:81]
	v_lshl_add_u64 v[80:81], s[22:23], 0, v[80:81]
	s_lshl_b32 s20, s25, 2
	v_lshl_add_u64 v[80:81], v[80:81], 0, s[20:21]
	v_lshl_add_u64 v[80:81], v[80:81], 0, v[152:153]
	global_store_dword v[80:81], v82, off
.LBB0_571:
	s_or_b64 exec, exec, s[0:1]
	v_or_b32_e32 v80, 48, v160
	s_waitcnt lgkmcnt(0)
	v_ashrrev_i32_e32 v81, 31, v80
	v_lshlrev_b64 v[80:81], 10, v[80:81]
	v_lshl_add_u64 v[96:97], v[80:81], 0, v[158:159]
	v_lshl_add_u64 v[98:99], v[96:97], 2, s[2:3]
	s_mov_b32 s98, 0x80000
	s_mov_b32 s99, 0
	v_lshl_add_u64 v[210:211], v[194:195], 0, s[98:99]
	global_load_dwordx4 v[212:215], v[210:211], off offset:16
	s_mov_b32 s98, 0x80000
	s_mov_b32 s99, 0
	v_lshl_add_u64 v[210:211], v[194:195], 0, s[98:99]
	global_load_dwordx4 v[216:219], v[210:211], off offset:512
	v_lshl_add_u64 v[96:97], v[96:97], 1, s[34:35]
	s_waitcnt vmcnt(9)
	v_pk_fma_f32 v[78:79], v[78:79], v[106:107], v[222:223]
	v_pk_fma_f32 v[76:77], v[76:77], v[104:105], v[220:221]
	s_waitcnt vmcnt(7)
	v_pk_fma_f32 v[80:81], v[74:75], v[110:111], v[246:247]
	v_pk_fma_f32 v[74:75], v[72:73], v[108:109], v[244:245]
	v_cvt_pk_bf16_f32 v72, v76, v77
	v_cvt_pk_bf16_f32 v73, v78, v79
	v_cvt_pk_bf16_f32 v74, v74, v75
	v_cvt_pk_bf16_f32 v75, v80, v81
	global_store_dwordx4 v[96:97], v[72:75], off
	s_mov_b32 s98, 0x80000
	s_mov_b32 s99, 0
	v_lshl_add_u64 v[210:211], v[194:195], 0, s[98:99]
	global_load_dwordx4 v[220:223], v[210:211], off offset:528
	s_mov_b32 s98, 0x90000
	s_mov_b32 s99, 0
	v_lshl_add_u64 v[210:211], v[194:195], 0, s[98:99]
	global_load_dwordx4 v[244:247], v[210:211], off
	v_lshlrev_b32_e32 v84, 16, v72
	v_and_b32_e32 v72, 0xffff0000, v72
	v_lshlrev_b32_e32 v85, 16, v73
	v_and_b32_e32 v73, 0xffff0000, v73
	v_lshlrev_b32_e32 v86, 16, v74
	v_and_b32_e32 v74, 0xffff0000, v74
	v_mul_f32_e32 v72, v72, v72
	v_mul_f32_e32 v73, v73, v73
	v_lshlrev_b32_e32 v87, 16, v75
	v_and_b32_e32 v75, 0xffff0000, v75
	v_mul_f32_e32 v74, v74, v74
	v_fmac_f32_e32 v72, v84, v84
	v_fmac_f32_e32 v73, v85, v85
	v_mul_f32_e32 v75, v75, v75
	v_fmac_f32_e32 v74, v86, v86
	v_add_f32_e32 v72, v72, v73
	v_fmac_f32_e32 v75, v87, v87
	v_add_f32_e32 v72, v72, v74
	v_add_f32_e32 v74, v75, v72
	s_waitcnt vmcnt(9)
	v_pk_fma_f32 v[68:69], v[68:69], v[92:93], v[196:197]
	v_pk_fma_f32 v[70:71], v[70:71], v[94:95], v[198:199]
	s_waitcnt vmcnt(7)
	v_pk_fma_f32 v[72:73], v[66:67], v[90:91], v[202:203]
	v_pk_fma_f32 v[64:65], v[64:65], v[88:89], v[200:201]
	v_cvt_pk_bf16_f32 v66, v68, v69
	v_cvt_pk_bf16_f32 v67, v70, v71
	v_cvt_pk_bf16_f32 v68, v64, v65
	v_and_b32_e32 v65, 0xffff0000, v66
	v_lshlrev_b32_e32 v64, 16, v66
	v_and_b32_e32 v71, 0xffff0000, v67
	v_mul_f32_e32 v65, v65, v65
	v_cvt_pk_bf16_f32 v69, v72, v73
	v_lshlrev_b32_e32 v70, 16, v67
	v_and_b32_e32 v73, 0xffff0000, v68
	v_mul_f32_e32 v71, v71, v71
	v_fmac_f32_e32 v65, v64, v64
	v_lshlrev_b32_e32 v72, 16, v68
	v_and_b32_e32 v76, 0xffff0000, v69
	v_mul_f32_e32 v73, v73, v73
	v_fmac_f32_e32 v71, v70, v70
	v_add_f32_e32 v64, v74, v65
	v_lshlrev_b32_e32 v75, 16, v69
	v_mul_f32_e32 v76, v76, v76
	v_fmac_f32_e32 v73, v72, v72
	v_add_f32_e32 v64, v71, v64
	v_add_f32_e32 v64, v73, v64
	v_fmac_f32_e32 v76, v75, v75
	v_add_f32_e32 v64, v76, v64
	ds_bpermute_b32 v65, v136, v64
	global_store_dwordx4 v[96:97], v[66:69], off offset:256
	s_waitcnt lgkmcnt(0)
	v_add_f32_e32 v64, v64, v65
	ds_bpermute_b32 v65, v130, v64
	s_and_saveexec_b64 s[0:1], s[8:9]
	s_cbranch_execz .LBB0_573
	s_waitcnt lgkmcnt(0)
	v_add_f32_e32 v66, v64, v65
	v_or_b32_e32 v64, 48, v128
	v_ashrrev_i32_e32 v65, 31, v64
	v_lshlrev_b64 v[64:65], 6, v[64:65]
	v_lshl_add_u64 v[64:65], s[22:23], 0, v[64:65]
	s_lshl_b32 s20, s25, 2
	v_lshl_add_u64 v[64:65], v[64:65], 0, s[20:21]
	v_lshl_add_u64 v[64:65], v[64:65], 0, v[152:153]
	global_store_dword v[64:65], v66, off
.LBB0_573:
	s_or_b64 exec, exec, s[0:1]
	s_waitcnt lgkmcnt(0)
	v_lshlrev_b64 v[64:65], 10, v[160:161]
	v_lshl_add_u64 v[64:65], v[64:65], 0, v[158:159]
	s_mov_b64 s[0:1], 0x20000
	v_lshl_add_u64 v[74:75], v[64:65], 0, s[0:1]
	v_lshl_add_u64 v[76:77], v[74:75], 2, s[2:3]
	s_mov_b32 s98, 0x90000
	s_mov_b32 s99, 0
	v_lshl_add_u64 v[210:211], v[194:195], 0, s[98:99]
	global_load_dwordx4 v[196:199], v[210:211], off offset:16
	s_mov_b32 s98, 0x90000
	s_mov_b32 s99, 0
	v_lshl_add_u64 v[210:211], v[194:195], 0, s[98:99]
	global_load_dwordx4 v[200:203], v[210:211], off offset:512
	v_lshl_add_u64 v[74:75], v[74:75], 1, s[34:35]
	s_waitcnt vmcnt(9)
	v_pk_fma_f32 v[62:63], v[62:63], v[106:107], v[206:207]
	v_pk_fma_f32 v[60:61], v[60:61], v[104:105], v[204:205]
	s_waitcnt vmcnt(7)
	v_pk_fma_f32 v[66:67], v[58:59], v[110:111], v[214:215]
	v_pk_fma_f32 v[58:59], v[56:57], v[108:109], v[212:213]
	v_cvt_pk_bf16_f32 v56, v60, v61
	v_cvt_pk_bf16_f32 v57, v62, v63
	v_cvt_pk_bf16_f32 v58, v58, v59
	v_cvt_pk_bf16_f32 v59, v66, v67
	global_store_dwordx4 v[74:75], v[56:59], off
	s_mov_b32 s98, 0x90000
	s_mov_b32 s99, 0
	v_lshl_add_u64 v[210:211], v[194:195], 0, s[98:99]
	global_load_dwordx4 v[204:207], v[210:211], off offset:528
	s_mov_b32 s98, 0xa0000
	s_mov_b32 s99, 0
	v_lshl_add_u64 v[210:211], v[194:195], 0, s[98:99]
	global_load_dwordx4 v[212:215], v[210:211], off
	v_lshlrev_b32_e32 v70, 16, v56
	v_and_b32_e32 v56, 0xffff0000, v56
	v_lshlrev_b32_e32 v71, 16, v57
	v_and_b32_e32 v57, 0xffff0000, v57
	v_lshlrev_b32_e32 v72, 16, v58
	v_and_b32_e32 v58, 0xffff0000, v58
	v_mul_f32_e32 v56, v56, v56
	v_mul_f32_e32 v57, v57, v57
	v_lshlrev_b32_e32 v73, 16, v59
	v_and_b32_e32 v59, 0xffff0000, v59
	v_mul_f32_e32 v58, v58, v58
	v_fmac_f32_e32 v56, v70, v70
	v_fmac_f32_e32 v57, v71, v71
	v_mul_f32_e32 v59, v59, v59
	v_fmac_f32_e32 v58, v72, v72
	v_add_f32_e32 v56, v56, v57
	v_fmac_f32_e32 v59, v73, v73
	v_add_f32_e32 v56, v56, v58
	v_add_f32_e32 v58, v59, v56
	s_waitcnt vmcnt(9)
	v_pk_fma_f32 v[52:53], v[52:53], v[92:93], v[216:217]
	v_pk_fma_f32 v[54:55], v[54:55], v[94:95], v[218:219]
	s_waitcnt vmcnt(7)
	v_pk_fma_f32 v[56:57], v[50:51], v[90:91], v[222:223]
	v_pk_fma_f32 v[48:49], v[48:49], v[88:89], v[220:221]
	v_cvt_pk_bf16_f32 v50, v52, v53
	v_cvt_pk_bf16_f32 v51, v54, v55
	v_cvt_pk_bf16_f32 v52, v48, v49
	v_and_b32_e32 v49, 0xffff0000, v50
	v_lshlrev_b32_e32 v48, 16, v50
	v_and_b32_e32 v55, 0xffff0000, v51
	v_mul_f32_e32 v49, v49, v49
	v_cvt_pk_bf16_f32 v53, v56, v57
	v_lshlrev_b32_e32 v54, 16, v51
	v_and_b32_e32 v57, 0xffff0000, v52
	v_mul_f32_e32 v55, v55, v55
	v_fmac_f32_e32 v49, v48, v48
	v_lshlrev_b32_e32 v56, 16, v52
	v_and_b32_e32 v60, 0xffff0000, v53
	v_mul_f32_e32 v57, v57, v57
	v_fmac_f32_e32 v55, v54, v54
	v_add_f32_e32 v48, v58, v49
	v_lshlrev_b32_e32 v59, 16, v53
	v_mul_f32_e32 v60, v60, v60
	v_fmac_f32_e32 v57, v56, v56
	v_add_f32_e32 v48, v55, v48
	v_add_f32_e32 v48, v57, v48
	v_fmac_f32_e32 v60, v59, v59
	v_add_f32_e32 v48, v60, v48
	ds_bpermute_b32 v49, v136, v48
	global_store_dwordx4 v[74:75], v[50:53], off offset:256
	s_waitcnt lgkmcnt(0)
	v_add_f32_e32 v48, v48, v49
	ds_bpermute_b32 v49, v130, v48
	s_and_saveexec_b64 s[0:1], s[8:9]
	s_cbranch_execz .LBB0_575
	s_waitcnt lgkmcnt(0)
	v_add_f32_e32 v50, v48, v49
	v_lshlrev_b64 v[48:49], 6, v[128:129]
	v_lshl_add_u64 v[48:49], s[22:23], 0, v[48:49]
	s_lshl_b32 s20, s25, 2
	v_lshl_add_u64 v[48:49], v[48:49], 0, s[20:21]
	v_lshl_add_u64 v[48:49], v[48:49], 0, v[152:153]
	v_add_co_u32_e32 v48, vcc, 0x2000, v48
	s_nop 1
	v_addc_co_u32_e32 v49, vcc, 0, v49, vcc
	global_store_dword v[48:49], v50, off
.LBB0_575:
	s_or_b64 exec, exec, s[0:1]
	s_mov_b64 s[0:1], 0x24000
	v_lshl_add_u64 v[56:57], v[64:65], 0, s[0:1]
	v_lshl_add_u64 v[58:59], v[56:57], 2, s[2:3]
	s_waitcnt lgkmcnt(0)
	s_mov_b32 s98, 0xa0000
	s_mov_b32 s99, 0
	v_lshl_add_u64 v[210:211], v[194:195], 0, s[98:99]
	global_load_dwordx4 v[216:219], v[210:211], off offset:16
	s_mov_b32 s98, 0xa0000
	s_mov_b32 s99, 0
	v_lshl_add_u64 v[210:211], v[194:195], 0, s[98:99]
	global_load_dwordx4 v[220:223], v[210:211], off offset:512
	v_lshl_add_u64 v[56:57], v[56:57], 1, s[34:35]
	s_waitcnt vmcnt(9)
	v_pk_fma_f32 v[46:47], v[46:47], v[106:107], v[246:247]
	v_pk_fma_f32 v[44:45], v[44:45], v[104:105], v[244:245]
	s_waitcnt vmcnt(7)
	v_pk_fma_f32 v[48:49], v[42:43], v[110:111], v[198:199]
	v_pk_fma_f32 v[42:43], v[40:41], v[108:109], v[196:197]
	v_cvt_pk_bf16_f32 v40, v44, v45
	v_cvt_pk_bf16_f32 v41, v46, v47
	v_cvt_pk_bf16_f32 v42, v42, v43
	v_cvt_pk_bf16_f32 v43, v48, v49
	global_store_dwordx4 v[56:57], v[40:43], off
	s_mov_b32 s98, 0xa0000
	s_mov_b32 s99, 0
	v_lshl_add_u64 v[210:211], v[194:195], 0, s[98:99]
	global_load_dwordx4 v[244:247], v[210:211], off offset:528
	s_mov_b32 s98, 0xb0000
	s_mov_b32 s99, 0
	v_lshl_add_u64 v[210:211], v[194:195], 0, s[98:99]
	global_load_dwordx4 v[196:199], v[210:211], off
	v_lshlrev_b32_e32 v52, 16, v40
	v_and_b32_e32 v40, 0xffff0000, v40
	v_lshlrev_b32_e32 v53, 16, v41
	v_and_b32_e32 v41, 0xffff0000, v41
	v_lshlrev_b32_e32 v54, 16, v42
	v_and_b32_e32 v42, 0xffff0000, v42
	v_mul_f32_e32 v40, v40, v40
	v_mul_f32_e32 v41, v41, v41
	v_lshlrev_b32_e32 v55, 16, v43
	v_and_b32_e32 v43, 0xffff0000, v43
	v_mul_f32_e32 v42, v42, v42
	v_fmac_f32_e32 v40, v52, v52
	v_fmac_f32_e32 v41, v53, v53
	v_mul_f32_e32 v43, v43, v43
	v_fmac_f32_e32 v42, v54, v54
	v_add_f32_e32 v40, v40, v41
	v_fmac_f32_e32 v43, v55, v55
	v_add_f32_e32 v40, v40, v42
	v_add_f32_e32 v42, v43, v40
	s_waitcnt vmcnt(9)
	v_pk_fma_f32 v[36:37], v[36:37], v[92:93], v[200:201]
	v_pk_fma_f32 v[38:39], v[38:39], v[94:95], v[202:203]
	s_waitcnt vmcnt(7)
	v_pk_fma_f32 v[40:41], v[34:35], v[90:91], v[206:207]
	v_pk_fma_f32 v[32:33], v[32:33], v[88:89], v[204:205]
	v_cvt_pk_bf16_f32 v34, v36, v37
	v_cvt_pk_bf16_f32 v35, v38, v39
	v_cvt_pk_bf16_f32 v36, v32, v33
	v_and_b32_e32 v33, 0xffff0000, v34
	v_lshlrev_b32_e32 v32, 16, v34
	v_and_b32_e32 v39, 0xffff0000, v35
	v_mul_f32_e32 v33, v33, v33
	v_cvt_pk_bf16_f32 v37, v40, v41
	v_lshlrev_b32_e32 v38, 16, v35
	v_and_b32_e32 v41, 0xffff0000, v36
	v_mul_f32_e32 v39, v39, v39
	v_fmac_f32_e32 v33, v32, v32
	v_lshlrev_b32_e32 v40, 16, v36
	v_and_b32_e32 v44, 0xffff0000, v37
	v_mul_f32_e32 v41, v41, v41
	v_fmac_f32_e32 v39, v38, v38
	v_add_f32_e32 v32, v42, v33
	v_lshlrev_b32_e32 v43, 16, v37
	v_mul_f32_e32 v44, v44, v44
	v_fmac_f32_e32 v41, v40, v40
	v_add_f32_e32 v32, v39, v32
	v_add_f32_e32 v32, v41, v32
	v_fmac_f32_e32 v44, v43, v43
	v_add_f32_e32 v32, v44, v32
	ds_bpermute_b32 v33, v136, v32
	global_store_dwordx4 v[56:57], v[34:37], off offset:256
	s_waitcnt lgkmcnt(0)
	v_add_f32_e32 v32, v32, v33
	ds_bpermute_b32 v33, v130, v32
	s_and_saveexec_b64 s[0:1], s[8:9]
	s_cbranch_execz .LBB0_577
	s_waitcnt lgkmcnt(0)
	v_add_f32_e32 v34, v32, v33
	v_lshlrev_b64 v[32:33], 6, v[128:129]
	v_lshl_add_u64 v[32:33], s[22:23], 0, v[32:33]
	s_lshl_b32 s20, s25, 2
	v_lshl_add_u64 v[32:33], v[32:33], 0, s[20:21]
	v_lshl_add_u64 v[32:33], v[32:33], 0, v[152:153]
	v_add_co_u32_e32 v32, vcc, 0x2000, v32
	s_nop 1
	v_addc_co_u32_e32 v33, vcc, 0, v33, vcc
	global_store_dword v[32:33], v34, off offset:1024
.LBB0_577:
	s_or_b64 exec, exec, s[0:1]
	s_waitcnt lgkmcnt(0)
	v_lshlrev_b64 v[32:33], 10, v[160:161]
	v_lshl_add_u64 v[32:33], v[32:33], 0, v[158:159]
	s_mov_b64 s[0:1], 0x28000
	v_lshl_add_u64 v[42:43], v[32:33], 0, s[0:1]
	v_lshl_add_u64 v[44:45], v[42:43], 2, s[2:3]
	s_mov_b32 s98, 0xb0000
	s_mov_b32 s99, 0
	v_lshl_add_u64 v[210:211], v[194:195], 0, s[98:99]
	global_load_dwordx4 v[200:203], v[210:211], off offset:16
	s_mov_b32 s98, 0xb0000
	s_mov_b32 s99, 0
	v_lshl_add_u64 v[210:211], v[194:195], 0, s[98:99]
	global_load_dwordx4 v[204:207], v[210:211], off offset:512
	v_lshl_add_u64 v[42:43], v[42:43], 1, s[34:35]
	s_waitcnt vmcnt(9)
	v_pk_fma_f32 v[30:31], v[30:31], v[106:107], v[214:215]
	v_pk_fma_f32 v[28:29], v[28:29], v[104:105], v[212:213]
	s_waitcnt vmcnt(7)
	v_pk_fma_f32 v[34:35], v[26:27], v[110:111], v[218:219]
	v_pk_fma_f32 v[26:27], v[24:25], v[108:109], v[216:217]
	v_cvt_pk_bf16_f32 v24, v28, v29
	v_cvt_pk_bf16_f32 v25, v30, v31
	v_cvt_pk_bf16_f32 v26, v26, v27
	v_cvt_pk_bf16_f32 v27, v34, v35
	global_store_dwordx4 v[42:43], v[24:27], off
	s_mov_b32 s98, 0xb0000
	s_mov_b32 s99, 0
	v_lshl_add_u64 v[210:211], v[194:195], 0, s[98:99]
	global_load_dwordx4 v[212:215], v[210:211], off offset:528
	v_lshlrev_b32_e32 v38, 16, v24
	v_and_b32_e32 v24, 0xffff0000, v24
	v_lshlrev_b32_e32 v39, 16, v25
	v_and_b32_e32 v25, 0xffff0000, v25
	v_lshlrev_b32_e32 v40, 16, v26
	v_and_b32_e32 v26, 0xffff0000, v26
	v_mul_f32_e32 v24, v24, v24
	v_mul_f32_e32 v25, v25, v25
	v_lshlrev_b32_e32 v41, 16, v27
	v_and_b32_e32 v27, 0xffff0000, v27
	v_mul_f32_e32 v26, v26, v26
	v_fmac_f32_e32 v24, v38, v38
	v_fmac_f32_e32 v25, v39, v39
	v_mul_f32_e32 v27, v27, v27
	v_fmac_f32_e32 v26, v40, v40
	v_add_f32_e32 v24, v24, v25
	v_fmac_f32_e32 v27, v41, v41
	v_add_f32_e32 v24, v24, v26
	v_add_f32_e32 v26, v27, v24
	s_waitcnt vmcnt(8)
	v_pk_fma_f32 v[20:21], v[20:21], v[92:93], v[220:221]
	v_pk_fma_f32 v[22:23], v[22:23], v[94:95], v[222:223]
	s_waitcnt vmcnt(6)
	v_pk_fma_f32 v[24:25], v[18:19], v[90:91], v[246:247]
	v_pk_fma_f32 v[16:17], v[16:17], v[88:89], v[244:245]
	v_cvt_pk_bf16_f32 v18, v20, v21
	v_cvt_pk_bf16_f32 v19, v22, v23
	v_cvt_pk_bf16_f32 v20, v16, v17
	v_and_b32_e32 v17, 0xffff0000, v18
	v_lshlrev_b32_e32 v16, 16, v18
	v_and_b32_e32 v23, 0xffff0000, v19
	v_mul_f32_e32 v17, v17, v17
	v_cvt_pk_bf16_f32 v21, v24, v25
	v_lshlrev_b32_e32 v22, 16, v19
	v_and_b32_e32 v25, 0xffff0000, v20
	v_mul_f32_e32 v23, v23, v23
	v_fmac_f32_e32 v17, v16, v16
	v_lshlrev_b32_e32 v24, 16, v20
	v_and_b32_e32 v28, 0xffff0000, v21
	v_mul_f32_e32 v25, v25, v25
	v_fmac_f32_e32 v23, v22, v22
	v_add_f32_e32 v16, v26, v17
	v_lshlrev_b32_e32 v27, 16, v21
	v_mul_f32_e32 v28, v28, v28
	v_fmac_f32_e32 v25, v24, v24
	v_add_f32_e32 v16, v23, v16
	v_add_f32_e32 v16, v25, v16
	v_fmac_f32_e32 v28, v27, v27
	v_add_f32_e32 v16, v28, v16
	ds_bpermute_b32 v17, v136, v16
	global_store_dwordx4 v[42:43], v[18:21], off offset:256
	s_waitcnt lgkmcnt(0)
	v_add_f32_e32 v16, v16, v17
	ds_bpermute_b32 v17, v130, v16
	s_and_saveexec_b64 s[0:1], s[8:9]
	s_cbranch_execz .LBB0_579
	s_waitcnt lgkmcnt(0)
	v_add_f32_e32 v18, v16, v17
	v_lshlrev_b64 v[16:17], 6, v[128:129]
	v_lshl_add_u64 v[16:17], s[22:23], 0, v[16:17]
	s_lshl_b32 s20, s25, 2
	v_lshl_add_u64 v[16:17], v[16:17], 0, s[20:21]
	v_lshl_add_u64 v[16:17], v[16:17], 0, v[152:153]
	v_add_co_u32_e32 v16, vcc, 0x2000, v16
	s_nop 1
	v_addc_co_u32_e32 v17, vcc, 0, v17, vcc
	global_store_dword v[16:17], v18, off offset:2048
.LBB0_579:
	s_or_b64 exec, exec, s[0:1]
	s_mov_b64 s[0:1], 0x2c000
	v_lshl_add_u64 v[24:25], v[32:33], 0, s[0:1]
	v_lshl_add_u64 v[26:27], v[24:25], 2, s[2:3]
	s_waitcnt lgkmcnt(0)
	v_lshl_add_u64 v[24:25], v[24:25], 1, s[34:35]
	s_waitcnt vmcnt(6)
	v_pk_fma_f32 v[14:15], v[14:15], v[106:107], v[198:199]
	v_pk_fma_f32 v[12:13], v[12:13], v[104:105], v[196:197]
	s_waitcnt vmcnt(4)
	v_pk_fma_f32 v[16:17], v[10:11], v[110:111], v[202:203]
	v_pk_fma_f32 v[10:11], v[8:9], v[108:109], v[200:201]
	v_cvt_pk_bf16_f32 v8, v12, v13
	v_cvt_pk_bf16_f32 v9, v14, v15
	v_cvt_pk_bf16_f32 v10, v10, v11
	v_cvt_pk_bf16_f32 v11, v16, v17
	global_store_dwordx4 v[24:25], v[8:11], off
	v_lshlrev_b32_e32 v20, 16, v8
	v_and_b32_e32 v8, 0xffff0000, v8
	v_lshlrev_b32_e32 v21, 16, v9
	v_and_b32_e32 v9, 0xffff0000, v9
	v_lshlrev_b32_e32 v22, 16, v10
	v_and_b32_e32 v10, 0xffff0000, v10
	v_mul_f32_e32 v8, v8, v8
	v_mul_f32_e32 v9, v9, v9
	v_lshlrev_b32_e32 v23, 16, v11
	v_and_b32_e32 v11, 0xffff0000, v11
	v_mul_f32_e32 v10, v10, v10
	v_fmac_f32_e32 v8, v20, v20
	v_fmac_f32_e32 v9, v21, v21
	v_mul_f32_e32 v11, v11, v11
	v_fmac_f32_e32 v10, v22, v22
	v_add_f32_e32 v8, v8, v9
	v_fmac_f32_e32 v11, v23, v23
	v_add_f32_e32 v8, v8, v10
	v_add_f32_e32 v10, v11, v8
	s_waitcnt vmcnt(4)
	v_pk_fma_f32 v[4:5], v[4:5], v[92:93], v[204:205]
	v_pk_fma_f32 v[6:7], v[6:7], v[94:95], v[206:207]
	s_waitcnt vmcnt(2)
	v_pk_fma_f32 v[8:9], v[2:3], v[90:91], v[214:215]
	v_pk_fma_f32 v[0:1], v[0:1], v[88:89], v[212:213]
	v_cvt_pk_bf16_f32 v2, v4, v5
	v_cvt_pk_bf16_f32 v3, v6, v7
	v_cvt_pk_bf16_f32 v4, v0, v1
	v_and_b32_e32 v1, 0xffff0000, v2
	v_lshlrev_b32_e32 v0, 16, v2
	v_and_b32_e32 v7, 0xffff0000, v3
	v_mul_f32_e32 v1, v1, v1
	v_cvt_pk_bf16_f32 v5, v8, v9
	v_lshlrev_b32_e32 v6, 16, v3
	v_and_b32_e32 v9, 0xffff0000, v4
	v_mul_f32_e32 v7, v7, v7
	v_fmac_f32_e32 v1, v0, v0
	v_lshlrev_b32_e32 v8, 16, v4
	v_and_b32_e32 v12, 0xffff0000, v5
	v_mul_f32_e32 v9, v9, v9
	v_fmac_f32_e32 v7, v6, v6
	v_add_f32_e32 v0, v10, v1
	v_lshlrev_b32_e32 v11, 16, v5
	v_mul_f32_e32 v12, v12, v12
	v_fmac_f32_e32 v9, v8, v8
	v_add_f32_e32 v0, v7, v0
	v_add_f32_e32 v0, v9, v0
	v_fmac_f32_e32 v12, v11, v11
	v_add_f32_e32 v0, v12, v0
	ds_bpermute_b32 v1, v136, v0
	global_store_dwordx4 v[24:25], v[2:5], off offset:256
	s_waitcnt lgkmcnt(0)
	v_add_f32_e32 v0, v0, v1
	ds_bpermute_b32 v1, v130, v0
	s_and_saveexec_b64 s[0:1], s[8:9]
	s_cbranch_execz .LBB0_554
	s_waitcnt lgkmcnt(0)
	v_add_f32_e32 v2, v0, v1
	v_lshlrev_b64 v[0:1], 6, v[128:129]
	v_lshl_add_u64 v[0:1], s[22:23], 0, v[0:1]
	s_lshl_b32 s20, s25, 2
	v_lshl_add_u64 v[0:1], v[0:1], 0, s[20:21]
	v_lshl_add_u64 v[0:1], v[0:1], 0, v[152:153]
	v_add_co_u32_e32 v0, vcc, 0x2000, v0
	s_nop 1
	v_addc_co_u32_e32 v1, vcc, 0, v1, vcc
	global_store_dword v[0:1], v2, off offset:3072
	s_branch .LBB0_554

.LBB0_1561:
	s_lshl_b32 s30, s2, 8
	s_ashr_i32 s31, s30, 31
	s_lshl_b64 s[14:15], s[30:31], 11
	s_lshl_b64 s[4:5], s[4:5], 2
	v_bfe_u32 v152, v32, 6, 2
	v_bfe_u32 v164, v32, 4, 2
	s_add_u32 s4, s8, s4
	v_and_b32_e32 v163, 15, v32
	s_addc_u32 s5, s9, s5
	v_ashrrev_i32_e32 v160, 2, v32
	s_lshl_b32 s1, s0, 8
	v_lshlrev_b32_e32 v32, 5, v152
	v_lshlrev_b32_e32 v33, 3, v164
	v_or3_b32 v158, v32, s1, v33
	v_ashrrev_i32_e32 v159, 31, v158
	v_lshl_add_u64 v[32:33], v[158:159], 2, s[4:5]
	s_mov_b64 s[4:5], 0x3c000
	s_mov_b32 s1, 0x3c000
	v_lshl_add_u64 v[36:37], v[32:33], 0, s[4:5]
	v_add_co_u32_e32 v32, vcc, s1, v32
	s_add_u32 s4, s54, s14
	s_movk_i32 s1, 0xffc0
	s_addc_u32 s5, s55, s15
	v_and_or_b32 v162, v160, s1, v163
	v_lshl_add_u64 v[160:161], v[158:159], 1, s[4:5]
	v_lshlrev_b32_e32 v159, 2, v163
	v_ashrrev_i32_e32 v163, 31, v162
	v_lshlrev_b32_e32 v158, 6, v164
	v_cmp_eq_u32_e64 s[14:15], 0, v164
	v_lshlrev_b64 v[164:165], 11, v[162:163]
	v_addc_co_u32_e32 v33, vcc, 0, v33, vcc
	v_lshl_add_u64 v[164:165], v[160:161], 0, v[164:165]
	global_load_dwordx4 v[52:55], v[32:33], off
	global_load_dwordx4 v[48:51], v[36:37], off offset:16
	s_nop 0
	global_load_dwordx4 v[32:35], v[36:37], off offset:528
	s_nop 0
	global_load_dwordx4 v[36:39], v[36:37], off offset:512
	s_movk_i32 s1, 0x80
	v_mov_b32_e32 v194, v164
	v_mov_b32_e32 v195, v165
	global_load_dwordx4 v[196:199], v[194:195], off
	global_load_dwordx4 v[200:203], v[194:195], off offset:256
	s_mov_b32 s98, 0x8000
	s_mov_b32 s99, 0
	v_lshl_add_u64 v[210:211], v[194:195], 0, s[98:99]
	global_load_dwordx4 v[204:207], v[210:211], off
	s_mov_b32 s98, 0x8000
	s_mov_b32 s99, 0
	v_lshl_add_u64 v[210:211], v[194:195], 0, s[98:99]
	global_load_dwordx4 v[212:215], v[210:211], off offset:256
	s_mov_b32 s98, 0x10000
	s_mov_b32 s99, 0
	v_lshl_add_u64 v[210:211], v[194:195], 0, s[98:99]
	global_load_dwordx4 v[216:219], v[210:211], off
	s_mov_b32 s98, 0x10000
	s_mov_b32 s99, 0
	v_lshl_add_u64 v[210:211], v[194:195], 0, s[98:99]
	global_load_dwordx4 v[220:223], v[210:211], off offset:256
	v_bitop3_b32 v184, v158, 64, v159 bitop3:0x36
	v_bitop3_b32 v185, v158, s1, v159 bitop3:0x36
	v_add_u32_e32 v158, s30, v162
	s_lshl_b32 s0, s0, 2
	s_and_b32 s2, s0, 12
	v_lshlrev_b32_e32 v152, 2, v152
	s_waitcnt vmcnt(5)
	v_lshlrev_b32_e32 v190, 16, v196
	v_and_b32_e32 v191, 0xffff0000, v196
	v_lshlrev_b32_e32 v186, 16, v197
	v_and_b32_e32 v187, 0xffff0000, v197
	v_lshlrev_b32_e32 v192, 16, v198
	v_and_b32_e32 v193, 0xffff0000, v198
	v_lshlrev_b32_e32 v188, 16, v199
	v_and_b32_e32 v189, 0xffff0000, v199
	v_pk_fma_f32 v[142:143], v[142:143], v[54:55], v[186:187]
	v_pk_fma_f32 v[140:141], v[140:141], v[52:53], v[190:191]
	v_pk_fma_f32 v[186:187], v[138:139], v[50:51], v[188:189]
	v_pk_fma_f32 v[138:139], v[136:137], v[48:49], v[192:193]
	v_cvt_pk_bf16_f32 v136, v140, v141
	v_cvt_pk_bf16_f32 v137, v142, v143
	v_cvt_pk_bf16_f32 v138, v138, v139
	v_cvt_pk_bf16_f32 v139, v186, v187
	global_store_dwordx4 v[164:165], v[136:139], off
	v_lshlrev_b32_e32 v140, 16, v136
	s_nop 0
	v_and_b32_e32 v136, 0xffff0000, v136
	v_mul_f32_e32 v136, v136, v136
	v_fmac_f32_e32 v136, v140, v140
	v_lshlrev_b32_e32 v140, 16, v137
	v_and_b32_e32 v137, 0xffff0000, v137
	v_mul_f32_e32 v137, v137, v137
	v_fmac_f32_e32 v137, v140, v140
	v_add_f32_e32 v136, v136, v137
	v_lshlrev_b32_e32 v137, 16, v138
	v_and_b32_e32 v138, 0xffff0000, v138
	v_mul_f32_e32 v138, v138, v138
	v_fmac_f32_e32 v138, v137, v137
	v_add_f32_e32 v136, v138, v136
	v_and_b32_e32 v138, 0xffff0000, v139
	v_lshlrev_b32_e32 v137, 16, v139
	v_mul_f32_e32 v138, v138, v138
	v_fmac_f32_e32 v138, v137, v137
	v_add_f32_e32 v159, v138, v136
	s_mov_b32 s98, 0x18000
	s_mov_b32 s99, 0
	v_lshl_add_u64 v[210:211], v[194:195], 0, s[98:99]
	global_load_dwordx4 v[244:247], v[210:211], off
	s_waitcnt vmcnt(6)
	v_lshlrev_b32_e32 v140, 16, v200
	v_and_b32_e32 v141, 0xffff0000, v200
	v_lshlrev_b32_e32 v136, 16, v201
	v_and_b32_e32 v137, 0xffff0000, v201
	v_lshlrev_b32_e32 v142, 16, v202
	v_and_b32_e32 v143, 0xffff0000, v202
	v_lshlrev_b32_e32 v138, 16, v203
	v_and_b32_e32 v139, 0xffff0000, v203
	v_pk_fma_f32 v[134:135], v[134:135], v[38:39], v[136:137]
	v_pk_fma_f32 v[132:133], v[132:133], v[36:37], v[140:141]
	v_pk_fma_f32 v[136:137], v[130:131], v[34:35], v[138:139]
	v_pk_fma_f32 v[130:131], v[128:129], v[32:33], v[142:143]
	v_cvt_pk_bf16_f32 v128, v132, v133
	v_cvt_pk_bf16_f32 v129, v134, v135
	v_cvt_pk_bf16_f32 v130, v130, v131
	v_cvt_pk_bf16_f32 v131, v136, v137
	global_store_dwordx4 v[164:165], v[128:131], off offset:256
	v_lshlrev_b32_e32 v132, 16, v128
	s_nop 0
	v_and_b32_e32 v128, 0xffff0000, v128
	v_mul_f32_e32 v128, v128, v128
	v_fmac_f32_e32 v128, v132, v132
	v_lshlrev_b32_e32 v132, 16, v129
	v_and_b32_e32 v129, 0xffff0000, v129
	v_mul_f32_e32 v129, v129, v129
	v_add_f32_e32 v128, v128, v159
	v_fmac_f32_e32 v129, v132, v132
	v_add_f32_e32 v128, v129, v128
	v_lshlrev_b32_e32 v129, 16, v130
	v_and_b32_e32 v130, 0xffff0000, v130
	v_mul_f32_e32 v130, v130, v130
	v_fmac_f32_e32 v130, v129, v129
	v_add_f32_e32 v128, v130, v128
	v_and_b32_e32 v130, 0xffff0000, v131
	v_lshlrev_b32_e32 v129, 16, v131
	v_mul_f32_e32 v130, v130, v130
	v_fmac_f32_e32 v130, v129, v129
	v_add_f32_e32 v128, v130, v128
	ds_bpermute_b32 v129, v184, v128
	v_ashrrev_i32_e32 v159, 31, v158
	s_waitcnt lgkmcnt(0)
	v_add_f32_e32 v128, v128, v129
	ds_bpermute_b32 v129, v185, v128
	s_and_saveexec_b64 s[0:1], s[14:15]
	s_cbranch_execz .LBB0_1563
	s_waitcnt lgkmcnt(0)
	v_add_f32_e32 v130, v128, v129
	v_lshlrev_b64 v[128:129], 6, v[158:159]
	v_lshl_add_u64 v[128:129], s[20:21], 0, v[128:129]
	s_lshl_b32 s10, s2, 2
	v_lshl_add_u64 v[128:129], v[128:129], 0, s[10:11]
	v_lshl_add_u64 v[128:129], v[128:129], 0, v[152:153]
	global_store_dword v[128:129], v130, off
.LBB0_1563:
	s_or_b64 exec, exec, s[0:1]
	v_or_b32_e32 v128, 16, v162
	s_waitcnt lgkmcnt(0)
	v_ashrrev_i32_e32 v129, 31, v128
	v_lshlrev_b64 v[128:129], 11, v[128:129]
	v_lshl_add_u64 v[128:129], v[160:161], 0, v[128:129]
	s_mov_b32 s98, 0x18000
	s_mov_b32 s99, 0
	v_lshl_add_u64 v[210:211], v[194:195], 0, s[98:99]
	global_load_dwordx4 v[196:199], v[210:211], off offset:256
	s_mov_b32 s98, 0x40000
	s_mov_b32 s99, 0
	v_lshl_add_u64 v[210:211], v[194:195], 0, s[98:99]
	global_load_dwordx4 v[200:203], v[210:211], off
	s_waitcnt vmcnt(8)
	v_lshlrev_b32_e32 v138, 16, v204
	v_and_b32_e32 v139, 0xffff0000, v204
	v_lshlrev_b32_e32 v130, 16, v205
	v_and_b32_e32 v131, 0xffff0000, v205
	v_lshlrev_b32_e32 v140, 16, v206
	v_and_b32_e32 v141, 0xffff0000, v206
	v_lshlrev_b32_e32 v132, 16, v207
	v_and_b32_e32 v133, 0xffff0000, v207
	s_waitcnt vmcnt(7)
	v_lshlrev_b32_e32 v164, 16, v214
	v_and_b32_e32 v165, 0xffff0000, v214
	v_lshlrev_b32_e32 v136, 16, v215
	v_and_b32_e32 v137, 0xffff0000, v215
	v_pk_fma_f32 v[126:127], v[126:127], v[54:55], v[130:131]
	v_pk_fma_f32 v[124:125], v[124:125], v[52:53], v[138:139]
	v_lshlrev_b32_e32 v142, 16, v212
	v_and_b32_e32 v143, 0xffff0000, v212
	v_lshlrev_b32_e32 v134, 16, v213
	v_and_b32_e32 v135, 0xffff0000, v213
	v_pk_fma_f32 v[122:123], v[122:123], v[50:51], v[132:133]
	v_pk_fma_f32 v[120:121], v[120:121], v[48:49], v[140:141]
	v_pk_fma_f32 v[132:133], v[114:115], v[34:35], v[136:137]
	v_pk_fma_f32 v[112:113], v[112:113], v[32:33], v[164:165]
	v_cvt_pk_bf16_f32 v114, v124, v125
	v_cvt_pk_bf16_f32 v115, v126, v127
	v_pk_fma_f32 v[130:131], v[118:119], v[38:39], v[134:135]
	v_pk_fma_f32 v[118:119], v[116:117], v[36:37], v[142:143]
	v_cvt_pk_bf16_f32 v116, v120, v121
	v_cvt_pk_bf16_f32 v117, v122, v123
	v_cvt_pk_bf16_f32 v120, v112, v113
	v_and_b32_e32 v113, 0xffff0000, v114
	v_and_b32_e32 v123, 0xffff0000, v115
	v_lshlrev_b32_e32 v112, 16, v114
	v_lshlrev_b32_e32 v122, 16, v115
	v_and_b32_e32 v125, 0xffff0000, v116
	v_mul_f32_e32 v113, v113, v113
	v_mul_f32_e32 v123, v123, v123
	v_cvt_pk_bf16_f32 v118, v118, v119
	v_lshlrev_b32_e32 v124, 16, v116
	v_and_b32_e32 v127, 0xffff0000, v117
	v_mul_f32_e32 v125, v125, v125
	v_fmac_f32_e32 v113, v112, v112
	v_fmac_f32_e32 v123, v122, v122
	v_cvt_pk_bf16_f32 v119, v130, v131
	v_lshlrev_b32_e32 v126, 16, v117
	v_and_b32_e32 v131, 0xffff0000, v118
	v_mul_f32_e32 v127, v127, v127
	v_fmac_f32_e32 v125, v124, v124
	v_add_f32_e32 v112, v113, v123
	v_cvt_pk_bf16_f32 v121, v132, v133
	v_lshlrev_b32_e32 v130, 16, v118
	v_and_b32_e32 v133, 0xffff0000, v119
	v_mul_f32_e32 v131, v131, v131
	v_fmac_f32_e32 v127, v126, v126
	v_add_f32_e32 v112, v125, v112
	v_lshlrev_b32_e32 v132, 16, v119
	v_and_b32_e32 v135, 0xffff0000, v120
	v_mul_f32_e32 v133, v133, v133
	v_fmac_f32_e32 v131, v130, v130
	v_add_f32_e32 v112, v127, v112
	v_lshlrev_b32_e32 v134, 16, v120
	v_and_b32_e32 v137, 0xffff0000, v121
	v_mul_f32_e32 v135, v135, v135
	v_fmac_f32_e32 v133, v132, v132
	v_add_f32_e32 v112, v131, v112
	v_lshlrev_b32_e32 v136, 16, v121
	v_mul_f32_e32 v137, v137, v137
	v_fmac_f32_e32 v135, v134, v134
	v_add_f32_e32 v112, v133, v112
	v_add_f32_e32 v112, v135, v112
	v_fmac_f32_e32 v137, v136, v136
	v_add_f32_e32 v112, v137, v112
	ds_bpermute_b32 v113, v184, v112
	global_store_dwordx4 v[128:129], v[114:117], off
	global_store_dwordx4 v[128:129], v[118:121], off offset:256
	s_waitcnt lgkmcnt(0)
	v_add_f32_e32 v112, v112, v113
	ds_bpermute_b32 v113, v185, v112
	s_and_saveexec_b64 s[0:1], s[14:15]
	s_cbranch_execz .LBB0_1565
	s_waitcnt lgkmcnt(0)
	v_add_f32_e32 v114, v112, v113
	v_or_b32_e32 v112, 16, v158
	v_ashrrev_i32_e32 v113, 31, v112
	v_lshlrev_b64 v[112:113], 6, v[112:113]
	v_lshl_add_u64 v[112:113], s[20:21], 0, v[112:113]
	s_lshl_b32 s10, s2, 2
	v_lshl_add_u64 v[112:113], v[112:113], 0, s[10:11]
	v_lshl_add_u64 v[112:113], v[112:113], 0, v[152:153]
	global_store_dword v[112:113], v114, off
.LBB0_1565:
	s_or_b64 exec, exec, s[0:1]
	v_or_b32_e32 v112, 32, v162
	s_waitcnt lgkmcnt(0)
	v_ashrrev_i32_e32 v113, 31, v112
	v_lshlrev_b64 v[112:113], 11, v[112:113]
	v_lshl_add_u64 v[112:113], v[160:161], 0, v[112:113]
	s_mov_b32 s98, 0x40000
	s_mov_b32 s99, 0
	v_lshl_add_u64 v[210:211], v[194:195], 0, s[98:99]
	global_load_dwordx4 v[204:207], v[210:211], off offset:256
	s_mov_b32 s98, 0x48000
	s_mov_b32 s99, 0
	v_lshl_add_u64 v[210:211], v[194:195], 0, s[98:99]
	global_load_dwordx4 v[212:215], v[210:211], off
	s_waitcnt vmcnt(10)
	v_lshlrev_b32_e32 v122, 16, v216
	v_and_b32_e32 v123, 0xffff0000, v216
	v_lshlrev_b32_e32 v114, 16, v217
	v_and_b32_e32 v115, 0xffff0000, v217
	v_lshlrev_b32_e32 v124, 16, v218
	v_and_b32_e32 v125, 0xffff0000, v218
	v_lshlrev_b32_e32 v116, 16, v219
	v_and_b32_e32 v117, 0xffff0000, v219
	s_waitcnt vmcnt(9)
	v_lshlrev_b32_e32 v128, 16, v222
	v_and_b32_e32 v129, 0xffff0000, v222
	v_lshlrev_b32_e32 v120, 16, v223
	v_and_b32_e32 v121, 0xffff0000, v223
	v_pk_fma_f32 v[110:111], v[110:111], v[54:55], v[114:115]
	v_pk_fma_f32 v[108:109], v[108:109], v[52:53], v[122:123]
	v_lshlrev_b32_e32 v126, 16, v220
	v_and_b32_e32 v127, 0xffff0000, v220
	v_lshlrev_b32_e32 v118, 16, v221
	v_and_b32_e32 v119, 0xffff0000, v221
	v_pk_fma_f32 v[106:107], v[106:107], v[50:51], v[116:117]
	v_pk_fma_f32 v[104:105], v[104:105], v[48:49], v[124:125]
	v_pk_fma_f32 v[116:117], v[98:99], v[34:35], v[120:121]
	v_pk_fma_f32 v[96:97], v[96:97], v[32:33], v[128:129]
	v_cvt_pk_bf16_f32 v98, v108, v109
	v_cvt_pk_bf16_f32 v99, v110, v111
	v_pk_fma_f32 v[114:115], v[102:103], v[38:39], v[118:119]
	v_pk_fma_f32 v[102:103], v[100:101], v[36:37], v[126:127]
	v_cvt_pk_bf16_f32 v100, v104, v105
	v_cvt_pk_bf16_f32 v101, v106, v107
	v_cvt_pk_bf16_f32 v104, v96, v97
	v_and_b32_e32 v97, 0xffff0000, v98
	v_and_b32_e32 v107, 0xffff0000, v99
	v_lshlrev_b32_e32 v96, 16, v98
	v_lshlrev_b32_e32 v106, 16, v99
	v_and_b32_e32 v109, 0xffff0000, v100
	v_mul_f32_e32 v97, v97, v97
	v_mul_f32_e32 v107, v107, v107
	v_cvt_pk_bf16_f32 v102, v102, v103
	v_lshlrev_b32_e32 v108, 16, v100
	v_and_b32_e32 v111, 0xffff0000, v101
	v_mul_f32_e32 v109, v109, v109
	v_fmac_f32_e32 v97, v96, v96
	v_fmac_f32_e32 v107, v106, v106
	v_cvt_pk_bf16_f32 v103, v114, v115
	v_lshlrev_b32_e32 v110, 16, v101
	v_and_b32_e32 v115, 0xffff0000, v102
	v_mul_f32_e32 v111, v111, v111
	v_fmac_f32_e32 v109, v108, v108
	v_add_f32_e32 v96, v97, v107
	v_cvt_pk_bf16_f32 v105, v116, v117
	v_lshlrev_b32_e32 v114, 16, v102
	v_and_b32_e32 v117, 0xffff0000, v103
	v_mul_f32_e32 v115, v115, v115
	v_fmac_f32_e32 v111, v110, v110
	v_add_f32_e32 v96, v109, v96
	v_lshlrev_b32_e32 v116, 16, v103
	v_and_b32_e32 v119, 0xffff0000, v104
	v_mul_f32_e32 v117, v117, v117
	v_fmac_f32_e32 v115, v114, v114
	v_add_f32_e32 v96, v111, v96
	v_lshlrev_b32_e32 v118, 16, v104
	v_and_b32_e32 v121, 0xffff0000, v105
	v_mul_f32_e32 v119, v119, v119
	v_fmac_f32_e32 v117, v116, v116
	v_add_f32_e32 v96, v115, v96
	v_lshlrev_b32_e32 v120, 16, v105
	v_mul_f32_e32 v121, v121, v121
	v_fmac_f32_e32 v119, v118, v118
	v_add_f32_e32 v96, v117, v96
	v_add_f32_e32 v96, v119, v96
	v_fmac_f32_e32 v121, v120, v120
	v_add_f32_e32 v96, v121, v96
	ds_bpermute_b32 v97, v184, v96
	global_store_dwordx4 v[112:113], v[98:101], off
	global_store_dwordx4 v[112:113], v[102:105], off offset:256
	s_waitcnt lgkmcnt(0)
	v_add_f32_e32 v96, v96, v97
	ds_bpermute_b32 v97, v185, v96
	s_and_saveexec_b64 s[0:1], s[14:15]
	s_cbranch_execz .LBB0_1567
	s_waitcnt lgkmcnt(0)
	v_add_f32_e32 v98, v96, v97
	v_or_b32_e32 v96, 32, v158
	v_ashrrev_i32_e32 v97, 31, v96
	v_lshlrev_b64 v[96:97], 6, v[96:97]
	v_lshl_add_u64 v[96:97], s[20:21], 0, v[96:97]
	s_lshl_b32 s10, s2, 2
	v_lshl_add_u64 v[96:97], v[96:97], 0, s[10:11]
	v_lshl_add_u64 v[96:97], v[96:97], 0, v[152:153]
	global_store_dword v[96:97], v98, off
.LBB0_1567:
	s_or_b64 exec, exec, s[0:1]
	v_or_b32_e32 v96, 48, v162
	s_waitcnt lgkmcnt(0)
	v_ashrrev_i32_e32 v97, 31, v96
	v_lshlrev_b64 v[96:97], 11, v[96:97]
	v_lshl_add_u64 v[96:97], v[160:161], 0, v[96:97]
	s_mov_b32 s98, 0x48000
	s_mov_b32 s99, 0
	v_lshl_add_u64 v[210:211], v[194:195], 0, s[98:99]
	global_load_dwordx4 v[216:219], v[210:211], off offset:256
	s_mov_b32 s98, 0x50000
	s_mov_b32 s99, 0
	v_lshl_add_u64 v[210:211], v[194:195], 0, s[98:99]
	global_load_dwordx4 v[220:223], v[210:211], off
	s_waitcnt vmcnt(11)
	v_lshlrev_b32_e32 v106, 16, v244
	v_and_b32_e32 v107, 0xffff0000, v244
	v_lshlrev_b32_e32 v98, 16, v245
	v_and_b32_e32 v99, 0xffff0000, v245
	v_lshlrev_b32_e32 v108, 16, v246
	v_and_b32_e32 v109, 0xffff0000, v246
	v_lshlrev_b32_e32 v100, 16, v247
	v_and_b32_e32 v101, 0xffff0000, v247
	s_waitcnt vmcnt(9)
	v_lshlrev_b32_e32 v112, 16, v198
	v_and_b32_e32 v113, 0xffff0000, v198
	v_lshlrev_b32_e32 v104, 16, v199
	v_and_b32_e32 v105, 0xffff0000, v199
	v_pk_fma_f32 v[94:95], v[94:95], v[54:55], v[98:99]
	v_pk_fma_f32 v[92:93], v[92:93], v[52:53], v[106:107]
	v_lshlrev_b32_e32 v110, 16, v196
	v_and_b32_e32 v111, 0xffff0000, v196
	v_lshlrev_b32_e32 v102, 16, v197
	v_and_b32_e32 v103, 0xffff0000, v197
	v_pk_fma_f32 v[90:91], v[90:91], v[50:51], v[100:101]
	v_pk_fma_f32 v[88:89], v[88:89], v[48:49], v[108:109]
	v_pk_fma_f32 v[100:101], v[82:83], v[34:35], v[104:105]
	v_pk_fma_f32 v[80:81], v[80:81], v[32:33], v[112:113]
	v_cvt_pk_bf16_f32 v82, v92, v93
	v_cvt_pk_bf16_f32 v83, v94, v95
	v_pk_fma_f32 v[98:99], v[86:87], v[38:39], v[102:103]
	v_pk_fma_f32 v[86:87], v[84:85], v[36:37], v[110:111]
	v_cvt_pk_bf16_f32 v84, v88, v89
	v_cvt_pk_bf16_f32 v85, v90, v91
	v_cvt_pk_bf16_f32 v88, v80, v81
	v_and_b32_e32 v81, 0xffff0000, v82
	v_and_b32_e32 v91, 0xffff0000, v83
	v_lshlrev_b32_e32 v80, 16, v82
	v_lshlrev_b32_e32 v90, 16, v83
	v_and_b32_e32 v93, 0xffff0000, v84
	v_mul_f32_e32 v81, v81, v81
	v_mul_f32_e32 v91, v91, v91
	v_cvt_pk_bf16_f32 v86, v86, v87
	v_lshlrev_b32_e32 v92, 16, v84
	v_and_b32_e32 v95, 0xffff0000, v85
	v_mul_f32_e32 v93, v93, v93
	v_fmac_f32_e32 v81, v80, v80
	v_fmac_f32_e32 v91, v90, v90
	v_cvt_pk_bf16_f32 v87, v98, v99
	v_lshlrev_b32_e32 v94, 16, v85
	v_and_b32_e32 v99, 0xffff0000, v86
	v_mul_f32_e32 v95, v95, v95
	v_fmac_f32_e32 v93, v92, v92
	v_add_f32_e32 v80, v81, v91
	v_cvt_pk_bf16_f32 v89, v100, v101
	v_lshlrev_b32_e32 v98, 16, v86
	v_and_b32_e32 v101, 0xffff0000, v87
	v_mul_f32_e32 v99, v99, v99
	v_fmac_f32_e32 v95, v94, v94
	v_add_f32_e32 v80, v93, v80
	v_lshlrev_b32_e32 v100, 16, v87
	v_and_b32_e32 v103, 0xffff0000, v88
	v_mul_f32_e32 v101, v101, v101
	v_fmac_f32_e32 v99, v98, v98
	v_add_f32_e32 v80, v95, v80
	v_lshlrev_b32_e32 v102, 16, v88
	v_and_b32_e32 v105, 0xffff0000, v89
	v_mul_f32_e32 v103, v103, v103
	v_fmac_f32_e32 v101, v100, v100
	v_add_f32_e32 v80, v99, v80
	v_lshlrev_b32_e32 v104, 16, v89
	v_mul_f32_e32 v105, v105, v105
	v_fmac_f32_e32 v103, v102, v102
	v_add_f32_e32 v80, v101, v80
	v_add_f32_e32 v80, v103, v80
	v_fmac_f32_e32 v105, v104, v104
	v_add_f32_e32 v80, v105, v80
	ds_bpermute_b32 v81, v184, v80
	global_store_dwordx4 v[96:97], v[82:85], off
	global_store_dwordx4 v[96:97], v[86:89], off offset:256
	s_waitcnt lgkmcnt(0)
	v_add_f32_e32 v80, v80, v81
	ds_bpermute_b32 v81, v185, v80
	s_and_saveexec_b64 s[0:1], s[14:15]
	s_cbranch_execz .LBB0_1569
	s_waitcnt lgkmcnt(0)
	v_add_f32_e32 v82, v80, v81
	v_or_b32_e32 v80, 48, v158
	v_ashrrev_i32_e32 v81, 31, v80
	v_lshlrev_b64 v[80:81], 6, v[80:81]
	v_lshl_add_u64 v[80:81], s[20:21], 0, v[80:81]
	s_lshl_b32 s10, s2, 2
	v_lshl_add_u64 v[80:81], v[80:81], 0, s[10:11]
	v_lshl_add_u64 v[80:81], v[80:81], 0, v[152:153]
	global_store_dword v[80:81], v82, off
.LBB0_1569:
	s_or_b64 exec, exec, s[0:1]
	s_waitcnt lgkmcnt(0)
	v_lshlrev_b64 v[80:81], 11, v[162:163]
	v_lshl_add_u64 v[80:81], v[160:161], 0, v[80:81]
	v_add_co_u32_e32 v88, vcc, 0x40000, v80
	s_mov_b64 s[0:1], 0x40000
	s_nop 0
	v_addc_co_u32_e32 v89, vcc, 0, v81, vcc
	s_mov_b32 s98, 0x50000
	s_mov_b32 s99, 0
	v_lshl_add_u64 v[210:211], v[194:195], 0, s[98:99]
	global_load_dwordx4 v[244:247], v[210:211], off offset:256
	v_lshl_add_u64 v[82:83], v[80:81], 0, s[0:1]
	s_waitcnt vmcnt(11)
	v_lshlrev_b32_e32 v90, 16, v200
	v_and_b32_e32 v91, 0xffff0000, v200
	v_lshlrev_b32_e32 v84, 16, v201
	v_and_b32_e32 v85, 0xffff0000, v201
	v_lshlrev_b32_e32 v92, 16, v202
	v_and_b32_e32 v93, 0xffff0000, v202
	v_lshlrev_b32_e32 v86, 16, v203
	v_and_b32_e32 v87, 0xffff0000, v203
	v_pk_fma_f32 v[78:79], v[78:79], v[54:55], v[84:85]
	v_pk_fma_f32 v[76:77], v[76:77], v[52:53], v[90:91]
	v_pk_fma_f32 v[84:85], v[74:75], v[50:51], v[86:87]
	v_pk_fma_f32 v[74:75], v[72:73], v[48:49], v[92:93]
	v_cvt_pk_bf16_f32 v72, v76, v77
	v_cvt_pk_bf16_f32 v73, v78, v79
	v_cvt_pk_bf16_f32 v74, v74, v75
	v_cvt_pk_bf16_f32 v75, v84, v85
	global_store_dwordx4 v[88:89], v[72:75], off
	v_lshlrev_b32_e32 v76, 16, v72
	s_nop 0
	v_and_b32_e32 v72, 0xffff0000, v72
	v_mul_f32_e32 v72, v72, v72
	v_fmac_f32_e32 v72, v76, v76
	v_lshlrev_b32_e32 v76, 16, v73
	v_and_b32_e32 v73, 0xffff0000, v73
	v_mul_f32_e32 v73, v73, v73
	v_fmac_f32_e32 v73, v76, v76
	v_add_f32_e32 v72, v72, v73
	v_lshlrev_b32_e32 v73, 16, v74
	v_and_b32_e32 v74, 0xffff0000, v74
	v_mul_f32_e32 v74, v74, v74
	v_fmac_f32_e32 v74, v73, v73
	v_add_f32_e32 v72, v74, v72
	v_and_b32_e32 v74, 0xffff0000, v75
	v_lshlrev_b32_e32 v73, 16, v75
	v_mul_f32_e32 v74, v74, v74
	v_fmac_f32_e32 v74, v73, v73
	v_add_f32_e32 v84, v74, v72
	s_mov_b32 s98, 0x58000
	s_mov_b32 s99, 0
	v_lshl_add_u64 v[210:211], v[194:195], 0, s[98:99]
	global_load_dwordx4 v[196:199], v[210:211], off
	s_waitcnt vmcnt(10)
	v_lshlrev_b32_e32 v76, 16, v204
	v_and_b32_e32 v77, 0xffff0000, v204
	v_lshlrev_b32_e32 v72, 16, v205
	v_and_b32_e32 v73, 0xffff0000, v205
	v_lshlrev_b32_e32 v78, 16, v206
	v_and_b32_e32 v79, 0xffff0000, v206
	v_lshlrev_b32_e32 v74, 16, v207
	v_and_b32_e32 v75, 0xffff0000, v207
	v_pk_fma_f32 v[70:71], v[70:71], v[38:39], v[72:73]
	v_pk_fma_f32 v[68:69], v[68:69], v[36:37], v[76:77]
	v_pk_fma_f32 v[72:73], v[66:67], v[34:35], v[74:75]
	v_pk_fma_f32 v[66:67], v[64:65], v[32:33], v[78:79]
	v_cvt_pk_bf16_f32 v64, v68, v69
	v_cvt_pk_bf16_f32 v65, v70, v71
	v_cvt_pk_bf16_f32 v66, v66, v67
	v_cvt_pk_bf16_f32 v67, v72, v73
	global_store_dwordx4 v[82:83], v[64:67], off offset:256
	v_lshlrev_b32_e32 v68, 16, v64
	s_nop 0
	v_and_b32_e32 v64, 0xffff0000, v64
	v_mul_f32_e32 v64, v64, v64
	v_fmac_f32_e32 v64, v68, v68
	v_lshlrev_b32_e32 v68, 16, v65
	v_and_b32_e32 v65, 0xffff0000, v65
	v_mul_f32_e32 v65, v65, v65
	v_add_f32_e32 v64, v64, v84
	v_fmac_f32_e32 v65, v68, v68
	v_add_f32_e32 v64, v65, v64
	v_lshlrev_b32_e32 v65, 16, v66
	v_and_b32_e32 v66, 0xffff0000, v66
	v_mul_f32_e32 v66, v66, v66
	v_fmac_f32_e32 v66, v65, v65
	v_add_f32_e32 v64, v66, v64
	v_and_b32_e32 v66, 0xffff0000, v67
	v_lshlrev_b32_e32 v65, 16, v67
	v_mul_f32_e32 v66, v66, v66
	v_fmac_f32_e32 v66, v65, v65
	v_add_f32_e32 v64, v66, v64
	ds_bpermute_b32 v65, v184, v64
	s_waitcnt lgkmcnt(0)
	v_add_f32_e32 v64, v64, v65
	ds_bpermute_b32 v65, v185, v64
	s_and_saveexec_b64 s[0:1], s[14:15]
	s_cbranch_execz .LBB0_1571
	s_waitcnt lgkmcnt(0)
	v_add_f32_e32 v66, v64, v65
	v_lshlrev_b64 v[64:65], 6, v[158:159]
	v_lshl_add_u64 v[64:65], s[20:21], 0, v[64:65]
	s_lshl_b32 s10, s2, 2
	v_lshl_add_u64 v[64:65], v[64:65], 0, s[10:11]
	v_lshl_add_u64 v[64:65], v[64:65], 0, v[152:153]
	v_add_co_u32_e32 v64, vcc, 0x2000, v64
	s_nop 1
	v_addc_co_u32_e32 v65, vcc, 0, v65, vcc
	global_store_dword v[64:65], v66, off
.LBB0_1571:
	s_or_b64 exec, exec, s[0:1]
	v_add_co_u32_e32 v70, vcc, 0x48000, v80
	s_mov_b64 s[0:1], 0x48000
	s_nop 0
	v_addc_co_u32_e32 v71, vcc, 0, v81, vcc
	s_mov_b32 s98, 0x58000
	s_mov_b32 s99, 0
	v_lshl_add_u64 v[210:211], v[194:195], 0, s[98:99]
	global_load_dwordx4 v[200:203], v[210:211], off offset:256
	s_waitcnt lgkmcnt(0)
	v_lshl_add_u64 v[64:65], v[80:81], 0, s[0:1]
	s_waitcnt vmcnt(11)
	v_lshlrev_b32_e32 v72, 16, v212
	v_and_b32_e32 v73, 0xffff0000, v212
	v_lshlrev_b32_e32 v66, 16, v213
	v_and_b32_e32 v67, 0xffff0000, v213
	v_lshlrev_b32_e32 v74, 16, v214
	v_and_b32_e32 v75, 0xffff0000, v214
	v_lshlrev_b32_e32 v68, 16, v215
	v_and_b32_e32 v69, 0xffff0000, v215
	v_pk_fma_f32 v[62:63], v[62:63], v[54:55], v[66:67]
	v_pk_fma_f32 v[60:61], v[60:61], v[52:53], v[72:73]
	v_pk_fma_f32 v[66:67], v[58:59], v[50:51], v[68:69]
	v_pk_fma_f32 v[58:59], v[56:57], v[48:49], v[74:75]
	v_cvt_pk_bf16_f32 v56, v60, v61
	v_cvt_pk_bf16_f32 v57, v62, v63
	v_cvt_pk_bf16_f32 v58, v58, v59
	v_cvt_pk_bf16_f32 v59, v66, v67
	global_store_dwordx4 v[70:71], v[56:59], off
	v_lshlrev_b32_e32 v60, 16, v56
	s_nop 0
	v_and_b32_e32 v56, 0xffff0000, v56
	v_mul_f32_e32 v56, v56, v56
	v_fmac_f32_e32 v56, v60, v60
	v_lshlrev_b32_e32 v60, 16, v57
	v_and_b32_e32 v57, 0xffff0000, v57
	v_mul_f32_e32 v57, v57, v57
	v_fmac_f32_e32 v57, v60, v60
	v_add_f32_e32 v56, v56, v57
	v_lshlrev_b32_e32 v57, 16, v58
	v_and_b32_e32 v58, 0xffff0000, v58
	v_mul_f32_e32 v58, v58, v58
	v_fmac_f32_e32 v58, v57, v57
	v_add_f32_e32 v56, v58, v56
	v_and_b32_e32 v58, 0xffff0000, v59
	v_lshlrev_b32_e32 v57, 16, v59
	v_mul_f32_e32 v58, v58, v58
	v_fmac_f32_e32 v58, v57, v57
	v_add_f32_e32 v66, v58, v56
	s_waitcnt vmcnt(9)
	v_lshlrev_b32_e32 v60, 16, v216
	v_and_b32_e32 v61, 0xffff0000, v216
	v_lshlrev_b32_e32 v56, 16, v217
	v_and_b32_e32 v57, 0xffff0000, v217
	v_lshlrev_b32_e32 v62, 16, v218
	v_and_b32_e32 v63, 0xffff0000, v218
	v_lshlrev_b32_e32 v58, 16, v219
	v_and_b32_e32 v59, 0xffff0000, v219
	v_pk_fma_f32 v[46:47], v[46:47], v[38:39], v[56:57]
	v_pk_fma_f32 v[44:45], v[44:45], v[36:37], v[60:61]
	v_pk_fma_f32 v[56:57], v[42:43], v[34:35], v[58:59]
	v_pk_fma_f32 v[42:43], v[40:41], v[32:33], v[62:63]
	v_cvt_pk_bf16_f32 v40, v44, v45
	v_cvt_pk_bf16_f32 v41, v46, v47
	v_cvt_pk_bf16_f32 v42, v42, v43
	v_cvt_pk_bf16_f32 v43, v56, v57
	global_store_dwordx4 v[64:65], v[40:43], off offset:256
	v_lshlrev_b32_e32 v44, 16, v40
	s_nop 0
	v_and_b32_e32 v40, 0xffff0000, v40
	v_mul_f32_e32 v40, v40, v40
	v_fmac_f32_e32 v40, v44, v44
	v_lshlrev_b32_e32 v44, 16, v41
	v_and_b32_e32 v41, 0xffff0000, v41
	v_mul_f32_e32 v41, v41, v41
	v_add_f32_e32 v40, v40, v66
	v_fmac_f32_e32 v41, v44, v44
	v_add_f32_e32 v40, v41, v40
	v_lshlrev_b32_e32 v41, 16, v42
	v_and_b32_e32 v42, 0xffff0000, v42
	v_mul_f32_e32 v42, v42, v42
	v_fmac_f32_e32 v42, v41, v41
	v_add_f32_e32 v40, v42, v40
	v_and_b32_e32 v42, 0xffff0000, v43
	v_lshlrev_b32_e32 v41, 16, v43
	v_mul_f32_e32 v42, v42, v42
	v_fmac_f32_e32 v42, v41, v41
	v_add_f32_e32 v40, v42, v40
	ds_bpermute_b32 v41, v184, v40
	s_waitcnt lgkmcnt(0)
	v_add_f32_e32 v40, v40, v41
	ds_bpermute_b32 v41, v185, v40
	s_and_saveexec_b64 s[0:1], s[14:15]
	s_cbranch_execz .LBB0_1573
	s_waitcnt lgkmcnt(0)
	v_add_f32_e32 v42, v40, v41
	v_lshlrev_b64 v[40:41], 6, v[158:159]
	v_lshl_add_u64 v[40:41], s[20:21], 0, v[40:41]
	s_lshl_b32 s10, s2, 2
	v_lshl_add_u64 v[40:41], v[40:41], 0, s[10:11]
	v_lshl_add_u64 v[40:41], v[40:41], 0, v[152:153]
	v_add_co_u32_e32 v40, vcc, 0x2000, v40
	s_nop 1
	v_addc_co_u32_e32 v41, vcc, 0, v41, vcc
	global_store_dword v[40:41], v42, off offset:1024
.LBB0_1573:
	s_or_b64 exec, exec, s[0:1]
	s_waitcnt lgkmcnt(0)
	v_lshlrev_b64 v[40:41], 11, v[162:163]
	v_lshl_add_u64 v[40:41], v[160:161], 0, v[40:41]
	v_add_co_u32_e32 v56, vcc, 0x50000, v40
	s_mov_b64 s[0:1], 0x50000
	s_nop 0
	v_addc_co_u32_e32 v57, vcc, 0, v41, vcc
	v_lshl_add_u64 v[42:43], v[40:41], 0, s[0:1]
	s_waitcnt vmcnt(9)
	v_lshlrev_b32_e32 v58, 16, v220
	v_and_b32_e32 v59, 0xffff0000, v220
	v_lshlrev_b32_e32 v44, 16, v221
	v_and_b32_e32 v45, 0xffff0000, v221
	v_lshlrev_b32_e32 v60, 16, v222
	v_and_b32_e32 v61, 0xffff0000, v222
	v_lshlrev_b32_e32 v46, 16, v223
	v_and_b32_e32 v47, 0xffff0000, v223
	v_pk_fma_f32 v[30:31], v[30:31], v[54:55], v[44:45]
	v_pk_fma_f32 v[28:29], v[28:29], v[52:53], v[58:59]
	v_pk_fma_f32 v[44:45], v[26:27], v[50:51], v[46:47]
	v_pk_fma_f32 v[26:27], v[24:25], v[48:49], v[60:61]
	v_cvt_pk_bf16_f32 v24, v28, v29
	v_cvt_pk_bf16_f32 v25, v30, v31
	v_cvt_pk_bf16_f32 v26, v26, v27
	v_cvt_pk_bf16_f32 v27, v44, v45
	global_store_dwordx4 v[56:57], v[24:27], off
	v_lshlrev_b32_e32 v28, 16, v24
	s_nop 0
	v_and_b32_e32 v24, 0xffff0000, v24
	v_mul_f32_e32 v24, v24, v24
	v_fmac_f32_e32 v24, v28, v28
	v_lshlrev_b32_e32 v28, 16, v25
	v_and_b32_e32 v25, 0xffff0000, v25
	v_mul_f32_e32 v25, v25, v25
	v_fmac_f32_e32 v25, v28, v28
	v_add_f32_e32 v24, v24, v25
	v_lshlrev_b32_e32 v25, 16, v26
	v_and_b32_e32 v26, 0xffff0000, v26
	v_mul_f32_e32 v26, v26, v26
	v_fmac_f32_e32 v26, v25, v25
	v_add_f32_e32 v24, v26, v24
	v_and_b32_e32 v26, 0xffff0000, v27
	v_lshlrev_b32_e32 v25, 16, v27
	v_mul_f32_e32 v26, v26, v26
	v_fmac_f32_e32 v26, v25, v25
	v_add_f32_e32 v44, v26, v24
	s_waitcnt vmcnt(7)
	v_lshlrev_b32_e32 v28, 16, v244
	v_and_b32_e32 v29, 0xffff0000, v244
	v_lshlrev_b32_e32 v24, 16, v245
	v_and_b32_e32 v25, 0xffff0000, v245
	v_lshlrev_b32_e32 v30, 16, v246
	v_and_b32_e32 v31, 0xffff0000, v246
	v_lshlrev_b32_e32 v26, 16, v247
	v_and_b32_e32 v27, 0xffff0000, v247
	v_pk_fma_f32 v[22:23], v[22:23], v[38:39], v[24:25]
	v_pk_fma_f32 v[20:21], v[20:21], v[36:37], v[28:29]
	v_pk_fma_f32 v[24:25], v[18:19], v[34:35], v[26:27]
	v_pk_fma_f32 v[18:19], v[16:17], v[32:33], v[30:31]
	v_cvt_pk_bf16_f32 v16, v20, v21
	v_cvt_pk_bf16_f32 v17, v22, v23
	v_cvt_pk_bf16_f32 v18, v18, v19
	v_cvt_pk_bf16_f32 v19, v24, v25
	global_store_dwordx4 v[42:43], v[16:19], off offset:256
	v_lshlrev_b32_e32 v20, 16, v16
	s_nop 0
	v_and_b32_e32 v16, 0xffff0000, v16
	v_mul_f32_e32 v16, v16, v16
	v_fmac_f32_e32 v16, v20, v20
	v_lshlrev_b32_e32 v20, 16, v17
	v_and_b32_e32 v17, 0xffff0000, v17
	v_mul_f32_e32 v17, v17, v17
	v_add_f32_e32 v16, v16, v44
	v_fmac_f32_e32 v17, v20, v20
	v_add_f32_e32 v16, v17, v16
	v_lshlrev_b32_e32 v17, 16, v18
	v_and_b32_e32 v18, 0xffff0000, v18
	v_mul_f32_e32 v18, v18, v18
	v_fmac_f32_e32 v18, v17, v17
	v_add_f32_e32 v16, v18, v16
	v_and_b32_e32 v18, 0xffff0000, v19
	v_lshlrev_b32_e32 v17, 16, v19
	v_mul_f32_e32 v18, v18, v18
	v_fmac_f32_e32 v18, v17, v17
	v_add_f32_e32 v16, v18, v16
	ds_bpermute_b32 v17, v184, v16
	s_waitcnt lgkmcnt(0)
	v_add_f32_e32 v16, v16, v17
	ds_bpermute_b32 v17, v185, v16
	s_and_saveexec_b64 s[0:1], s[14:15]
	s_cbranch_execz .LBB0_1575
	s_waitcnt lgkmcnt(0)
	v_add_f32_e32 v18, v16, v17
	v_lshlrev_b64 v[16:17], 6, v[158:159]
	v_lshl_add_u64 v[16:17], s[20:21], 0, v[16:17]
	s_lshl_b32 s10, s2, 2
	v_lshl_add_u64 v[16:17], v[16:17], 0, s[10:11]
	v_lshl_add_u64 v[16:17], v[16:17], 0, v[152:153]
	v_add_co_u32_e32 v16, vcc, 0x2000, v16
	s_nop 1
	v_addc_co_u32_e32 v17, vcc, 0, v17, vcc
	global_store_dword v[16:17], v18, off offset:2048
.LBB0_1575:
	s_or_b64 exec, exec, s[0:1]
	v_add_co_u32_e32 v22, vcc, 0x58000, v40
	s_mov_b64 s[0:1], 0x58000
	s_nop 0
	v_addc_co_u32_e32 v23, vcc, 0, v41, vcc
	s_waitcnt lgkmcnt(0)
	v_lshl_add_u64 v[16:17], v[40:41], 0, s[0:1]
	s_waitcnt vmcnt(6)
	v_lshlrev_b32_e32 v24, 16, v196
	v_and_b32_e32 v25, 0xffff0000, v196
	v_lshlrev_b32_e32 v18, 16, v197
	v_and_b32_e32 v19, 0xffff0000, v197
	v_lshlrev_b32_e32 v26, 16, v198
	v_and_b32_e32 v27, 0xffff0000, v198
	v_lshlrev_b32_e32 v20, 16, v199
	v_and_b32_e32 v21, 0xffff0000, v199
	v_pk_fma_f32 v[14:15], v[14:15], v[54:55], v[18:19]
	v_pk_fma_f32 v[12:13], v[12:13], v[52:53], v[24:25]
	v_pk_fma_f32 v[18:19], v[10:11], v[50:51], v[20:21]
	v_pk_fma_f32 v[10:11], v[8:9], v[48:49], v[26:27]
	v_cvt_pk_bf16_f32 v8, v12, v13
	v_cvt_pk_bf16_f32 v9, v14, v15
	v_cvt_pk_bf16_f32 v10, v10, v11
	v_cvt_pk_bf16_f32 v11, v18, v19
	global_store_dwordx4 v[22:23], v[8:11], off
	v_lshlrev_b32_e32 v12, 16, v8
	s_nop 0
	v_and_b32_e32 v8, 0xffff0000, v8
	v_mul_f32_e32 v8, v8, v8
	v_fmac_f32_e32 v8, v12, v12
	v_lshlrev_b32_e32 v12, 16, v9
	v_and_b32_e32 v9, 0xffff0000, v9
	v_mul_f32_e32 v9, v9, v9
	v_fmac_f32_e32 v9, v12, v12
	v_add_f32_e32 v8, v8, v9
	v_lshlrev_b32_e32 v9, 16, v10
	v_and_b32_e32 v10, 0xffff0000, v10
	v_mul_f32_e32 v10, v10, v10
	v_fmac_f32_e32 v10, v9, v9
	v_add_f32_e32 v8, v10, v8
	v_and_b32_e32 v10, 0xffff0000, v11
	v_lshlrev_b32_e32 v9, 16, v11
	v_mul_f32_e32 v10, v10, v10
	v_fmac_f32_e32 v10, v9, v9
	v_add_f32_e32 v18, v10, v8
	s_waitcnt vmcnt(5)
	v_lshlrev_b32_e32 v12, 16, v200
	v_and_b32_e32 v13, 0xffff0000, v200
	v_lshlrev_b32_e32 v8, 16, v201
	v_and_b32_e32 v9, 0xffff0000, v201
	v_lshlrev_b32_e32 v14, 16, v202
	v_and_b32_e32 v15, 0xffff0000, v202
	v_lshlrev_b32_e32 v10, 16, v203
	v_and_b32_e32 v11, 0xffff0000, v203
	v_pk_fma_f32 v[6:7], v[6:7], v[38:39], v[8:9]
	v_pk_fma_f32 v[4:5], v[4:5], v[36:37], v[12:13]
	v_pk_fma_f32 v[8:9], v[2:3], v[34:35], v[10:11]
	v_pk_fma_f32 v[2:3], v[0:1], v[32:33], v[14:15]
	v_cvt_pk_bf16_f32 v0, v4, v5
	v_cvt_pk_bf16_f32 v1, v6, v7
	v_cvt_pk_bf16_f32 v2, v2, v3
	v_cvt_pk_bf16_f32 v3, v8, v9
	global_store_dwordx4 v[16:17], v[0:3], off offset:256
	v_lshlrev_b32_e32 v4, 16, v0
	s_nop 0
	v_and_b32_e32 v0, 0xffff0000, v0
	v_mul_f32_e32 v0, v0, v0
	v_fmac_f32_e32 v0, v4, v4
	v_lshlrev_b32_e32 v4, 16, v1
	v_and_b32_e32 v1, 0xffff0000, v1
	v_mul_f32_e32 v1, v1, v1
	v_add_f32_e32 v0, v0, v18
	v_fmac_f32_e32 v1, v4, v4
	v_add_f32_e32 v0, v1, v0
	v_lshlrev_b32_e32 v1, 16, v2
	v_and_b32_e32 v2, 0xffff0000, v2
	v_mul_f32_e32 v2, v2, v2
	v_fmac_f32_e32 v2, v1, v1
	v_add_f32_e32 v0, v2, v0
	v_and_b32_e32 v2, 0xffff0000, v3
	v_lshlrev_b32_e32 v1, 16, v3
	v_mul_f32_e32 v2, v2, v2
	v_fmac_f32_e32 v2, v1, v1
	v_add_f32_e32 v0, v2, v0
	ds_bpermute_b32 v1, v184, v0
	s_waitcnt lgkmcnt(0)
	v_add_f32_e32 v0, v0, v1
	ds_bpermute_b32 v1, v185, v0
	s_and_saveexec_b64 s[0:1], s[14:15]
	s_cbranch_execz .LBB0_1554
	s_waitcnt lgkmcnt(0)
	v_add_f32_e32 v2, v0, v1
	v_lshlrev_b64 v[0:1], 6, v[158:159]
	v_lshl_add_u64 v[0:1], s[20:21], 0, v[0:1]
	s_lshl_b32 s10, s2, 2
	v_lshl_add_u64 v[0:1], v[0:1], 0, s[10:11]
	v_lshl_add_u64 v[0:1], v[0:1], 0, v[152:153]
	v_add_co_u32_e32 v0, vcc, 0x2000, v0
	s_nop 1
	v_addc_co_u32_e32 v1, vcc, 0, v1, vcc
	global_store_dword v[0:1], v2, off offset:3072
	s_branch .LBB0_1554

.LBB0_2529:
	s_lshl_b32 s0, s0, 8
	s_ashr_i32 s1, s0, 31
	s_lshl_b64 s[4:5], s[0:1], 11
	s_lshl_b64 s[2:3], s[2:3], 2
	v_bfe_u32 v152, v92, 6, 2
	v_bfe_u32 v184, v92, 4, 2
	s_add_u32 s2, s8, s2
	v_and_b32_e32 v182, 15, v92
	s_addc_u32 s3, s9, s3
	v_ashrrev_i32_e32 v94, 2, v92
	s_lshl_b32 s1, s12, 8
	v_lshlrev_b32_e32 v92, 5, v152
	v_lshlrev_b32_e32 v93, 3, v184
	v_or3_b32 v92, v92, s1, v93
	s_movk_i32 s1, 0xffc0
	s_add_u32 s4, s54, s4
	v_and_or_b32 v160, v94, s1, v182
	v_ashrrev_i32_e32 v93, 31, v92
	s_addc_u32 s5, s55, s5
	v_ashrrev_i32_e32 v161, 31, v160
	v_lshl_add_u64 v[158:159], v[92:93], 1, s[4:5]
	v_lshlrev_b64 v[94:95], 11, v[160:161]
	v_lshl_add_u64 v[92:93], v[92:93], 2, s[2:3]
	s_mov_b32 s1, 0x72000
	v_lshl_add_u64 v[162:163], v[158:159], 0, v[94:95]
	v_add_co_u32_e32 v94, vcc, s1, v92
	v_mov_b32_e32 v202, v162
	v_mov_b32_e32 v203, v163
	global_load_dwordx4 v[212:215], v[202:203], off
	global_load_dwordx4 v[216:219], v[202:203], off offset:256
	s_mov_b32 s98, 0x8000
	s_mov_b32 s99, 0
	v_lshl_add_u64 v[204:205], v[202:203], 0, s[98:99]
	global_load_dwordx4 v[220:223], v[204:205], off
	s_mov_b32 s98, 0x8000
	s_mov_b32 s99, 0
	v_lshl_add_u64 v[204:205], v[202:203], 0, s[98:99]
	global_load_dwordx4 v[224:227], v[204:205], off offset:256
	s_mov_b64 s[2:3], 0x72000
	v_addc_co_u32_e32 v95, vcc, 0, v93, vcc
	s_mov_b32 s98, 0x10000
	s_mov_b32 s99, 0
	v_lshl_add_u64 v[204:205], v[202:203], 0, s[98:99]
	global_load_dwordx4 v[244:247], v[204:205], off
	global_load_dwordx4 v[108:111], v[94:95], off
	v_lshl_add_u64 v[92:93], v[92:93], 0, s[2:3]
	global_load_dwordx4 v[104:107], v[92:93], off offset:16
	global_load_dwordx4 v[100:103], v[92:93], off offset:512
	s_nop 0
	global_load_dwordx4 v[92:95], v[92:93], off offset:528
	s_movk_i32 s1, 0x80
	v_lshlrev_b32_e32 v185, 6, v184
	v_lshlrev_b32_e32 v182, 2, v182
	v_bitop3_b32 v183, v185, 64, v182 bitop3:0x36
	v_bitop3_b32 v182, v185, s1, v182 bitop3:0x36
	v_cmp_eq_u32_e64 s[14:15], 0, v184
	v_lshlrev_b32_e32 v152, 2, v152
	s_waitcnt vmcnt(8)
	v_lshlrev_b32_e32 v194, 16, v212
	v_and_b32_e32 v195, 0xffff0000, v212
	v_lshlrev_b32_e32 v186, 16, v213
	v_and_b32_e32 v187, 0xffff0000, v213
	v_lshlrev_b32_e32 v196, 16, v214
	v_and_b32_e32 v197, 0xffff0000, v214
	v_lshlrev_b32_e32 v188, 16, v215
	v_and_b32_e32 v189, 0xffff0000, v215
	s_waitcnt vmcnt(7)
	v_lshlrev_b32_e32 v198, 16, v216
	v_and_b32_e32 v199, 0xffff0000, v216
	v_lshlrev_b32_e32 v200, 16, v218
	v_and_b32_e32 v201, 0xffff0000, v218
	v_lshlrev_b32_e32 v192, 16, v219
	v_and_b32_e32 v193, 0xffff0000, v219
	s_waitcnt vmcnt(3)
	v_pk_fma_f32 v[142:143], v[142:143], v[110:111], v[186:187]
	v_pk_fma_f32 v[140:141], v[140:141], v[108:109], v[194:195]
	v_lshlrev_b32_e32 v190, 16, v217
	v_and_b32_e32 v191, 0xffff0000, v217
	s_waitcnt vmcnt(2)
	v_pk_fma_f32 v[138:139], v[138:139], v[106:107], v[188:189]
	v_pk_fma_f32 v[136:137], v[136:137], v[104:105], v[196:197]
	s_waitcnt vmcnt(1)
	v_pk_fma_f32 v[188:189], v[132:133], v[100:101], v[198:199]
	s_waitcnt vmcnt(0)
	v_pk_fma_f32 v[130:131], v[130:131], v[94:95], v[192:193]
	v_pk_fma_f32 v[128:129], v[128:129], v[92:93], v[200:201]
	v_cvt_pk_bf16_f32 v132, v140, v141
	v_cvt_pk_bf16_f32 v133, v142, v143
	v_pk_fma_f32 v[186:187], v[134:135], v[102:103], v[190:191]
	v_cvt_pk_bf16_f32 v134, v136, v137
	v_cvt_pk_bf16_f32 v135, v138, v139
	v_cvt_pk_bf16_f32 v138, v128, v129
	v_cvt_pk_bf16_f32 v139, v130, v131
	v_and_b32_e32 v129, 0xffff0000, v132
	v_and_b32_e32 v131, 0xffff0000, v133
	v_lshlrev_b32_e32 v128, 16, v132
	v_lshlrev_b32_e32 v130, 16, v133
	v_and_b32_e32 v141, 0xffff0000, v134
	v_mul_f32_e32 v129, v129, v129
	v_mul_f32_e32 v131, v131, v131
	v_cvt_pk_bf16_f32 v136, v188, v189
	v_lshlrev_b32_e32 v140, 16, v134
	v_and_b32_e32 v143, 0xffff0000, v135
	v_mul_f32_e32 v141, v141, v141
	v_fmac_f32_e32 v129, v128, v128
	v_fmac_f32_e32 v131, v130, v130
	v_cvt_pk_bf16_f32 v137, v186, v187
	v_lshlrev_b32_e32 v142, 16, v135
	v_and_b32_e32 v186, 0xffff0000, v136
	v_mul_f32_e32 v143, v143, v143
	v_fmac_f32_e32 v141, v140, v140
	v_add_f32_e32 v128, v129, v131
	v_lshlrev_b32_e32 v185, 16, v136
	v_mul_f32_e32 v186, v186, v186
	v_fmac_f32_e32 v143, v142, v142
	v_add_f32_e32 v128, v141, v128
	v_and_b32_e32 v130, 0xffff0000, v137
	v_fmac_f32_e32 v186, v185, v185
	v_add_f32_e32 v128, v143, v128
	v_lshlrev_b32_e32 v129, 16, v137
	v_mul_f32_e32 v130, v130, v130
	v_add_f32_e32 v128, v186, v128
	v_fmac_f32_e32 v130, v129, v129
	v_add_f32_e32 v128, v130, v128
	v_and_b32_e32 v130, 0xffff0000, v138
	v_lshlrev_b32_e32 v129, 16, v138
	v_mul_f32_e32 v130, v130, v130
	v_fmac_f32_e32 v130, v129, v129
	v_add_f32_e32 v128, v130, v128
	v_and_b32_e32 v130, 0xffff0000, v139
	v_lshlrev_b32_e32 v129, 16, v139
	v_mul_f32_e32 v130, v130, v130
	v_fmac_f32_e32 v130, v129, v129
	v_add_f32_e32 v129, v130, v128
	ds_bpermute_b32 v130, v183, v129
	v_add_u32_e32 v128, s0, v160
	s_lshl_b32 s0, s12, 2
	s_and_b32 s2, s0, 12
	global_store_dwordx4 v[162:163], v[132:135], off
	global_store_dwordx4 v[162:163], v[136:139], off offset:256
	s_waitcnt lgkmcnt(0)
	v_add_f32_e32 v130, v129, v130
	ds_bpermute_b32 v131, v182, v130
	v_ashrrev_i32_e32 v129, 31, v128
	s_and_saveexec_b64 s[0:1], s[14:15]
	s_cbranch_execz .LBB0_2531
	s_waitcnt lgkmcnt(0)
	v_add_f32_e32 v132, v130, v131
	v_lshlrev_b64 v[130:131], 6, v[128:129]
	v_lshl_add_u64 v[130:131], s[22:23], 0, v[130:131]
	s_lshl_b32 s20, s2, 2
	v_lshl_add_u64 v[130:131], v[130:131], 0, s[20:21]
	v_lshl_add_u64 v[130:131], v[130:131], 0, v[152:153]
	global_store_dword v[130:131], v132, off
.LBB0_2531:
	s_or_b64 exec, exec, s[0:1]
	v_or_b32_e32 v130, 16, v160
	s_waitcnt lgkmcnt(0)
	v_ashrrev_i32_e32 v131, 31, v130
	v_lshlrev_b64 v[130:131], 11, v[130:131]
	v_lshl_add_u64 v[138:139], v[158:159], 0, v[130:131]
	s_mov_b32 s98, 0x10000
	s_mov_b32 s99, 0
	v_lshl_add_u64 v[204:205], v[202:203], 0, s[98:99]
	global_load_dwordx4 v[212:215], v[204:205], off offset:256
	s_mov_b32 s98, 0x18000
	s_mov_b32 s99, 0
	v_lshl_add_u64 v[204:205], v[202:203], 0, s[98:99]
	global_load_dwordx4 v[216:219], v[204:205], off
	s_waitcnt vmcnt(10)
	v_lshlrev_b32_e32 v140, 16, v220
	v_and_b32_e32 v141, 0xffff0000, v220
	v_lshlrev_b32_e32 v130, 16, v221
	v_and_b32_e32 v131, 0xffff0000, v221
	v_lshlrev_b32_e32 v142, 16, v222
	v_and_b32_e32 v143, 0xffff0000, v222
	v_lshlrev_b32_e32 v132, 16, v223
	v_and_b32_e32 v133, 0xffff0000, v223
	s_waitcnt vmcnt(9)
	v_lshlrev_b32_e32 v184, 16, v226
	v_and_b32_e32 v185, 0xffff0000, v226
	v_lshlrev_b32_e32 v136, 16, v227
	v_and_b32_e32 v137, 0xffff0000, v227
	v_pk_fma_f32 v[126:127], v[126:127], v[110:111], v[130:131]
	v_pk_fma_f32 v[124:125], v[124:125], v[108:109], v[140:141]
	v_lshlrev_b32_e32 v162, 16, v224
	v_and_b32_e32 v163, 0xffff0000, v224
	v_lshlrev_b32_e32 v134, 16, v225
	v_and_b32_e32 v135, 0xffff0000, v225
	v_pk_fma_f32 v[122:123], v[122:123], v[106:107], v[132:133]
	v_pk_fma_f32 v[120:121], v[120:121], v[104:105], v[142:143]
	v_pk_fma_f32 v[132:133], v[114:115], v[94:95], v[136:137]
	v_pk_fma_f32 v[112:113], v[112:113], v[92:93], v[184:185]
	v_cvt_pk_bf16_f32 v114, v124, v125
	v_cvt_pk_bf16_f32 v115, v126, v127
	v_pk_fma_f32 v[130:131], v[118:119], v[102:103], v[134:135]
	v_pk_fma_f32 v[118:119], v[116:117], v[100:101], v[162:163]
	v_cvt_pk_bf16_f32 v116, v120, v121
	v_cvt_pk_bf16_f32 v117, v122, v123
	v_cvt_pk_bf16_f32 v120, v112, v113
	v_and_b32_e32 v113, 0xffff0000, v114
	v_and_b32_e32 v123, 0xffff0000, v115
	v_lshlrev_b32_e32 v112, 16, v114
	v_lshlrev_b32_e32 v122, 16, v115
	v_and_b32_e32 v125, 0xffff0000, v116
	v_mul_f32_e32 v113, v113, v113
	v_mul_f32_e32 v123, v123, v123
	v_cvt_pk_bf16_f32 v118, v118, v119
	v_lshlrev_b32_e32 v124, 16, v116
	v_and_b32_e32 v127, 0xffff0000, v117
	v_mul_f32_e32 v125, v125, v125
	v_fmac_f32_e32 v113, v112, v112
	v_fmac_f32_e32 v123, v122, v122
	v_cvt_pk_bf16_f32 v119, v130, v131
	v_lshlrev_b32_e32 v126, 16, v117
	v_and_b32_e32 v131, 0xffff0000, v118
	v_mul_f32_e32 v127, v127, v127
	v_fmac_f32_e32 v125, v124, v124
	v_add_f32_e32 v112, v113, v123
	v_cvt_pk_bf16_f32 v121, v132, v133
	v_lshlrev_b32_e32 v130, 16, v118
	v_and_b32_e32 v133, 0xffff0000, v119
	v_mul_f32_e32 v131, v131, v131
	v_fmac_f32_e32 v127, v126, v126
	v_add_f32_e32 v112, v125, v112
	v_lshlrev_b32_e32 v132, 16, v119
	v_and_b32_e32 v135, 0xffff0000, v120
	v_mul_f32_e32 v133, v133, v133
	v_fmac_f32_e32 v131, v130, v130
	v_add_f32_e32 v112, v127, v112
	v_lshlrev_b32_e32 v134, 16, v120
	v_and_b32_e32 v137, 0xffff0000, v121
	v_mul_f32_e32 v135, v135, v135
	v_fmac_f32_e32 v133, v132, v132
	v_add_f32_e32 v112, v131, v112
	v_lshlrev_b32_e32 v136, 16, v121
	v_mul_f32_e32 v137, v137, v137
	v_fmac_f32_e32 v135, v134, v134
	v_add_f32_e32 v112, v133, v112
	v_add_f32_e32 v112, v135, v112
	v_fmac_f32_e32 v137, v136, v136
	v_add_f32_e32 v112, v137, v112
	ds_bpermute_b32 v113, v183, v112
	global_store_dwordx4 v[138:139], v[114:117], off
	global_store_dwordx4 v[138:139], v[118:121], off offset:256
	s_waitcnt lgkmcnt(0)
	v_add_f32_e32 v112, v112, v113
	ds_bpermute_b32 v113, v182, v112
	s_and_saveexec_b64 s[0:1], s[14:15]
	s_cbranch_execz .LBB0_2533
	s_waitcnt lgkmcnt(0)
	v_add_f32_e32 v114, v112, v113
	v_or_b32_e32 v112, 16, v128
	v_ashrrev_i32_e32 v113, 31, v112
	v_lshlrev_b64 v[112:113], 6, v[112:113]
	v_lshl_add_u64 v[112:113], s[22:23], 0, v[112:113]
	s_lshl_b32 s20, s2, 2
	v_lshl_add_u64 v[112:113], v[112:113], 0, s[20:21]
	v_lshl_add_u64 v[112:113], v[112:113], 0, v[152:153]
	global_store_dword v[112:113], v114, off
.LBB0_2533:
	s_or_b64 exec, exec, s[0:1]
	v_or_b32_e32 v112, 32, v160
	s_waitcnt lgkmcnt(0)
	v_ashrrev_i32_e32 v113, 31, v112
	v_lshlrev_b64 v[112:113], 11, v[112:113]
	v_lshl_add_u64 v[120:121], v[158:159], 0, v[112:113]
	s_mov_b32 s98, 0x18000
	s_mov_b32 s99, 0
	v_lshl_add_u64 v[204:205], v[202:203], 0, s[98:99]
	global_load_dwordx4 v[220:223], v[204:205], off offset:256
	s_mov_b32 s98, 0x40000
	s_mov_b32 s99, 0
	v_lshl_add_u64 v[204:205], v[202:203], 0, s[98:99]
	global_load_dwordx4 v[224:227], v[204:205], off
	s_waitcnt vmcnt(12)
	v_lshlrev_b32_e32 v122, 16, v244
	v_and_b32_e32 v123, 0xffff0000, v244
	v_lshlrev_b32_e32 v112, 16, v245
	v_and_b32_e32 v113, 0xffff0000, v245
	v_lshlrev_b32_e32 v124, 16, v246
	v_and_b32_e32 v125, 0xffff0000, v246
	v_lshlrev_b32_e32 v114, 16, v247
	v_and_b32_e32 v115, 0xffff0000, v247
	s_waitcnt vmcnt(5)
	v_lshlrev_b32_e32 v130, 16, v214
	v_and_b32_e32 v131, 0xffff0000, v214
	v_lshlrev_b32_e32 v118, 16, v215
	v_and_b32_e32 v119, 0xffff0000, v215
	v_pk_fma_f32 v[98:99], v[98:99], v[110:111], v[112:113]
	v_pk_fma_f32 v[96:97], v[96:97], v[108:109], v[122:123]
	v_lshlrev_b32_e32 v126, 16, v212
	v_and_b32_e32 v127, 0xffff0000, v212
	v_lshlrev_b32_e32 v116, 16, v213
	v_and_b32_e32 v117, 0xffff0000, v213
	v_pk_fma_f32 v[90:91], v[90:91], v[106:107], v[114:115]
	v_pk_fma_f32 v[88:89], v[88:89], v[104:105], v[124:125]
	v_pk_fma_f32 v[114:115], v[82:83], v[94:95], v[118:119]
	v_pk_fma_f32 v[80:81], v[80:81], v[92:93], v[130:131]
	v_cvt_pk_bf16_f32 v82, v96, v97
	v_cvt_pk_bf16_f32 v83, v98, v99
	v_pk_fma_f32 v[112:113], v[86:87], v[102:103], v[116:117]
	v_pk_fma_f32 v[86:87], v[84:85], v[100:101], v[126:127]
	v_cvt_pk_bf16_f32 v84, v88, v89
	v_cvt_pk_bf16_f32 v85, v90, v91
	v_cvt_pk_bf16_f32 v88, v80, v81
	v_and_b32_e32 v81, 0xffff0000, v82
	v_and_b32_e32 v91, 0xffff0000, v83
	v_lshlrev_b32_e32 v80, 16, v82
	v_lshlrev_b32_e32 v90, 16, v83
	v_and_b32_e32 v97, 0xffff0000, v84
	v_mul_f32_e32 v81, v81, v81
	v_mul_f32_e32 v91, v91, v91
	v_cvt_pk_bf16_f32 v86, v86, v87
	v_lshlrev_b32_e32 v96, 16, v84
	v_and_b32_e32 v99, 0xffff0000, v85
	v_mul_f32_e32 v97, v97, v97
	v_fmac_f32_e32 v81, v80, v80
	v_fmac_f32_e32 v91, v90, v90
	v_cvt_pk_bf16_f32 v87, v112, v113
	v_lshlrev_b32_e32 v98, 16, v85
	v_and_b32_e32 v113, 0xffff0000, v86
	v_mul_f32_e32 v99, v99, v99
	v_fmac_f32_e32 v97, v96, v96
	v_add_f32_e32 v80, v81, v91
	v_cvt_pk_bf16_f32 v89, v114, v115
	v_lshlrev_b32_e32 v112, 16, v86
	v_and_b32_e32 v115, 0xffff0000, v87
	v_mul_f32_e32 v113, v113, v113
	v_fmac_f32_e32 v99, v98, v98
	v_add_f32_e32 v80, v97, v80
	v_lshlrev_b32_e32 v114, 16, v87
	v_and_b32_e32 v117, 0xffff0000, v88
	v_mul_f32_e32 v115, v115, v115
	v_fmac_f32_e32 v113, v112, v112
	v_add_f32_e32 v80, v99, v80
	v_lshlrev_b32_e32 v116, 16, v88
	v_and_b32_e32 v119, 0xffff0000, v89
	v_mul_f32_e32 v117, v117, v117
	v_fmac_f32_e32 v115, v114, v114
	v_add_f32_e32 v80, v113, v80
	v_lshlrev_b32_e32 v118, 16, v89
	v_mul_f32_e32 v119, v119, v119
	v_fmac_f32_e32 v117, v116, v116
	v_add_f32_e32 v80, v115, v80
	v_add_f32_e32 v80, v117, v80
	v_fmac_f32_e32 v119, v118, v118
	v_add_f32_e32 v80, v119, v80
	ds_bpermute_b32 v81, v183, v80
	global_store_dwordx4 v[120:121], v[82:85], off
	global_store_dwordx4 v[120:121], v[86:89], off offset:256
	s_waitcnt lgkmcnt(0)
	v_add_f32_e32 v80, v80, v81
	ds_bpermute_b32 v81, v182, v80
	s_and_saveexec_b64 s[0:1], s[14:15]
	s_cbranch_execz .LBB0_2535
	s_waitcnt lgkmcnt(0)
	v_add_f32_e32 v82, v80, v81
	v_or_b32_e32 v80, 32, v128
	v_ashrrev_i32_e32 v81, 31, v80
	v_lshlrev_b64 v[80:81], 6, v[80:81]
	v_lshl_add_u64 v[80:81], s[22:23], 0, v[80:81]
	s_lshl_b32 s20, s2, 2
	v_lshl_add_u64 v[80:81], v[80:81], 0, s[20:21]
	v_lshl_add_u64 v[80:81], v[80:81], 0, v[152:153]
	global_store_dword v[80:81], v82, off
.LBB0_2535:
	s_or_b64 exec, exec, s[0:1]
	v_or_b32_e32 v80, 48, v160
	s_waitcnt lgkmcnt(0)
	v_ashrrev_i32_e32 v81, 31, v80
	v_lshlrev_b64 v[80:81], 11, v[80:81]
	v_lshl_add_u64 v[88:89], v[158:159], 0, v[80:81]
	s_mov_b32 s98, 0x40000
	s_mov_b32 s99, 0
	v_lshl_add_u64 v[204:205], v[202:203], 0, s[98:99]
	global_load_dwordx4 v[244:247], v[204:205], off offset:256
	s_mov_b32 s98, 0x48000
	s_mov_b32 s99, 0
	v_lshl_add_u64 v[204:205], v[202:203], 0, s[98:99]
	global_load_dwordx4 v[212:215], v[204:205], off
	s_waitcnt vmcnt(8)
	v_lshlrev_b32_e32 v90, 16, v216
	v_and_b32_e32 v91, 0xffff0000, v216
	v_lshlrev_b32_e32 v80, 16, v217
	v_and_b32_e32 v81, 0xffff0000, v217
	v_lshlrev_b32_e32 v96, 16, v218
	v_and_b32_e32 v97, 0xffff0000, v218
	v_lshlrev_b32_e32 v82, 16, v219
	v_and_b32_e32 v83, 0xffff0000, v219
	s_waitcnt vmcnt(5)
	v_lshlrev_b32_e32 v112, 16, v222
	v_and_b32_e32 v113, 0xffff0000, v222
	v_lshlrev_b32_e32 v86, 16, v223
	v_and_b32_e32 v87, 0xffff0000, v223
	v_pk_fma_f32 v[78:79], v[78:79], v[110:111], v[80:81]
	v_pk_fma_f32 v[76:77], v[76:77], v[108:109], v[90:91]
	v_lshlrev_b32_e32 v98, 16, v220
	v_and_b32_e32 v99, 0xffff0000, v220
	v_lshlrev_b32_e32 v84, 16, v221
	v_and_b32_e32 v85, 0xffff0000, v221
	v_pk_fma_f32 v[74:75], v[74:75], v[106:107], v[82:83]
	v_pk_fma_f32 v[72:73], v[72:73], v[104:105], v[96:97]
	v_pk_fma_f32 v[82:83], v[66:67], v[94:95], v[86:87]
	v_pk_fma_f32 v[64:65], v[64:65], v[92:93], v[112:113]
	v_cvt_pk_bf16_f32 v66, v76, v77
	v_cvt_pk_bf16_f32 v67, v78, v79
	v_pk_fma_f32 v[80:81], v[70:71], v[102:103], v[84:85]
	v_pk_fma_f32 v[70:71], v[68:69], v[100:101], v[98:99]
	v_cvt_pk_bf16_f32 v68, v72, v73
	v_cvt_pk_bf16_f32 v69, v74, v75
	v_cvt_pk_bf16_f32 v72, v64, v65
	v_and_b32_e32 v65, 0xffff0000, v66
	v_and_b32_e32 v75, 0xffff0000, v67
	v_lshlrev_b32_e32 v64, 16, v66
	v_lshlrev_b32_e32 v74, 16, v67
	v_and_b32_e32 v77, 0xffff0000, v68
	v_mul_f32_e32 v65, v65, v65
	v_mul_f32_e32 v75, v75, v75
	v_cvt_pk_bf16_f32 v70, v70, v71
	v_lshlrev_b32_e32 v76, 16, v68
	v_and_b32_e32 v79, 0xffff0000, v69
	v_mul_f32_e32 v77, v77, v77
	v_fmac_f32_e32 v65, v64, v64
	v_fmac_f32_e32 v75, v74, v74
	v_cvt_pk_bf16_f32 v71, v80, v81
	v_lshlrev_b32_e32 v78, 16, v69
	v_and_b32_e32 v81, 0xffff0000, v70
	v_mul_f32_e32 v79, v79, v79
	v_fmac_f32_e32 v77, v76, v76
	v_add_f32_e32 v64, v65, v75
	v_cvt_pk_bf16_f32 v73, v82, v83
	v_lshlrev_b32_e32 v80, 16, v70
	v_and_b32_e32 v83, 0xffff0000, v71
	v_mul_f32_e32 v81, v81, v81
	v_fmac_f32_e32 v79, v78, v78
	v_add_f32_e32 v64, v77, v64
	v_lshlrev_b32_e32 v82, 16, v71
	v_and_b32_e32 v85, 0xffff0000, v72
	v_mul_f32_e32 v83, v83, v83
	v_fmac_f32_e32 v81, v80, v80
	v_add_f32_e32 v64, v79, v64
	v_lshlrev_b32_e32 v84, 16, v72
	v_and_b32_e32 v87, 0xffff0000, v73
	v_mul_f32_e32 v85, v85, v85
	v_fmac_f32_e32 v83, v82, v82
	v_add_f32_e32 v64, v81, v64
	v_lshlrev_b32_e32 v86, 16, v73
	v_mul_f32_e32 v87, v87, v87
	v_fmac_f32_e32 v85, v84, v84
	v_add_f32_e32 v64, v83, v64
	v_add_f32_e32 v64, v85, v64
	v_fmac_f32_e32 v87, v86, v86
	v_add_f32_e32 v64, v87, v64
	ds_bpermute_b32 v65, v183, v64
	global_store_dwordx4 v[88:89], v[66:69], off
	global_store_dwordx4 v[88:89], v[70:73], off offset:256
	s_waitcnt lgkmcnt(0)
	v_add_f32_e32 v64, v64, v65
	ds_bpermute_b32 v65, v182, v64
	s_and_saveexec_b64 s[0:1], s[14:15]
	s_cbranch_execz .LBB0_2537
	s_waitcnt lgkmcnt(0)
	v_add_f32_e32 v66, v64, v65
	v_or_b32_e32 v64, 48, v128
	v_ashrrev_i32_e32 v65, 31, v64
	v_lshlrev_b64 v[64:65], 6, v[64:65]
	v_lshl_add_u64 v[64:65], s[22:23], 0, v[64:65]
	s_lshl_b32 s20, s2, 2
	v_lshl_add_u64 v[64:65], v[64:65], 0, s[20:21]
	v_lshl_add_u64 v[64:65], v[64:65], 0, v[152:153]
	global_store_dword v[64:65], v66, off
.LBB0_2537:
	s_or_b64 exec, exec, s[0:1]
	s_waitcnt lgkmcnt(0)
	v_lshlrev_b64 v[64:65], 11, v[160:161]
	v_lshl_add_u64 v[64:65], v[158:159], 0, v[64:65]
	v_add_co_u32_e32 v74, vcc, 0x40000, v64
	s_mov_b64 s[0:1], 0x40000
	s_nop 0
	v_addc_co_u32_e32 v75, vcc, 0, v65, vcc
	s_mov_b32 s98, 0x48000
	s_mov_b32 s99, 0
	v_lshl_add_u64 v[204:205], v[202:203], 0, s[98:99]
	global_load_dwordx4 v[216:219], v[204:205], off offset:256
	v_lshl_add_u64 v[76:77], v[64:65], 0, s[0:1]
	s_mov_b32 s98, 0x50000
	s_mov_b32 s99, 0
	v_lshl_add_u64 v[204:205], v[202:203], 0, s[98:99]
	global_load_dwordx4 v[220:223], v[204:205], off
	s_waitcnt vmcnt(8)
	v_lshlrev_b32_e32 v78, 16, v224
	v_and_b32_e32 v79, 0xffff0000, v224
	v_lshlrev_b32_e32 v66, 16, v225
	v_and_b32_e32 v67, 0xffff0000, v225
	v_lshlrev_b32_e32 v80, 16, v226
	v_and_b32_e32 v81, 0xffff0000, v226
	v_lshlrev_b32_e32 v68, 16, v227
	v_and_b32_e32 v69, 0xffff0000, v227
	s_waitcnt vmcnt(5)
	v_lshlrev_b32_e32 v84, 16, v246
	v_and_b32_e32 v85, 0xffff0000, v246
	v_lshlrev_b32_e32 v72, 16, v247
	v_and_b32_e32 v73, 0xffff0000, v247
	v_pk_fma_f32 v[62:63], v[62:63], v[110:111], v[66:67]
	v_pk_fma_f32 v[60:61], v[60:61], v[108:109], v[78:79]
	v_lshlrev_b32_e32 v82, 16, v244
	v_and_b32_e32 v83, 0xffff0000, v244
	v_lshlrev_b32_e32 v70, 16, v245
	v_and_b32_e32 v71, 0xffff0000, v245
	v_pk_fma_f32 v[58:59], v[58:59], v[106:107], v[68:69]
	v_pk_fma_f32 v[56:57], v[56:57], v[104:105], v[80:81]
	v_pk_fma_f32 v[68:69], v[50:51], v[94:95], v[72:73]
	v_pk_fma_f32 v[48:49], v[48:49], v[92:93], v[84:85]
	v_cvt_pk_bf16_f32 v50, v60, v61
	v_cvt_pk_bf16_f32 v51, v62, v63
	v_pk_fma_f32 v[66:67], v[54:55], v[102:103], v[70:71]
	v_pk_fma_f32 v[54:55], v[52:53], v[100:101], v[82:83]
	v_cvt_pk_bf16_f32 v52, v56, v57
	v_cvt_pk_bf16_f32 v53, v58, v59
	v_cvt_pk_bf16_f32 v56, v48, v49
	v_and_b32_e32 v49, 0xffff0000, v50
	v_and_b32_e32 v59, 0xffff0000, v51
	v_lshlrev_b32_e32 v48, 16, v50
	v_lshlrev_b32_e32 v58, 16, v51
	v_and_b32_e32 v61, 0xffff0000, v52
	v_mul_f32_e32 v49, v49, v49
	v_mul_f32_e32 v59, v59, v59
	v_cvt_pk_bf16_f32 v54, v54, v55
	v_lshlrev_b32_e32 v60, 16, v52
	v_and_b32_e32 v63, 0xffff0000, v53
	v_mul_f32_e32 v61, v61, v61
	v_fmac_f32_e32 v49, v48, v48
	v_fmac_f32_e32 v59, v58, v58
	v_cvt_pk_bf16_f32 v55, v66, v67
	v_lshlrev_b32_e32 v62, 16, v53
	v_and_b32_e32 v67, 0xffff0000, v54
	v_mul_f32_e32 v63, v63, v63
	v_fmac_f32_e32 v61, v60, v60
	v_add_f32_e32 v48, v49, v59
	v_cvt_pk_bf16_f32 v57, v68, v69
	v_lshlrev_b32_e32 v66, 16, v54
	v_and_b32_e32 v69, 0xffff0000, v55
	v_mul_f32_e32 v67, v67, v67
	v_fmac_f32_e32 v63, v62, v62
	v_add_f32_e32 v48, v61, v48
	v_lshlrev_b32_e32 v68, 16, v55
	v_and_b32_e32 v71, 0xffff0000, v56
	v_mul_f32_e32 v69, v69, v69
	v_fmac_f32_e32 v67, v66, v66
	v_add_f32_e32 v48, v63, v48
	v_lshlrev_b32_e32 v70, 16, v56
	v_and_b32_e32 v73, 0xffff0000, v57
	v_mul_f32_e32 v71, v71, v71
	v_fmac_f32_e32 v69, v68, v68
	v_add_f32_e32 v48, v67, v48
	v_lshlrev_b32_e32 v72, 16, v57
	v_mul_f32_e32 v73, v73, v73
	v_fmac_f32_e32 v71, v70, v70
	v_add_f32_e32 v48, v69, v48
	v_add_f32_e32 v48, v71, v48
	v_fmac_f32_e32 v73, v72, v72
	v_add_f32_e32 v48, v73, v48
	ds_bpermute_b32 v49, v183, v48
	global_store_dwordx4 v[74:75], v[50:53], off
	global_store_dwordx4 v[76:77], v[54:57], off offset:256
	s_waitcnt lgkmcnt(0)
	v_add_f32_e32 v48, v48, v49
	ds_bpermute_b32 v49, v182, v48
	s_and_saveexec_b64 s[0:1], s[14:15]
	s_cbranch_execz .LBB0_2539
	s_waitcnt lgkmcnt(0)
	v_add_f32_e32 v50, v48, v49
	v_lshlrev_b64 v[48:49], 6, v[128:129]
	v_lshl_add_u64 v[48:49], s[22:23], 0, v[48:49]
	s_lshl_b32 s20, s2, 2
	v_lshl_add_u64 v[48:49], v[48:49], 0, s[20:21]
	v_lshl_add_u64 v[48:49], v[48:49], 0, v[152:153]
	v_add_co_u32_e32 v48, vcc, 0x2000, v48
	s_nop 1
	v_addc_co_u32_e32 v49, vcc, 0, v49, vcc
	global_store_dword v[48:49], v50, off
.LBB0_2539:
	s_or_b64 exec, exec, s[0:1]
	v_add_co_u32_e32 v56, vcc, 0x48000, v64
	s_mov_b64 s[0:1], 0x48000
	s_nop 0
	v_addc_co_u32_e32 v57, vcc, 0, v65, vcc
	s_waitcnt lgkmcnt(0)
	s_mov_b32 s98, 0x50000
	s_mov_b32 s99, 0
	v_lshl_add_u64 v[204:205], v[202:203], 0, s[98:99]
	global_load_dwordx4 v[224:227], v[204:205], off offset:256
	v_lshl_add_u64 v[58:59], v[64:65], 0, s[0:1]
	s_mov_b32 s98, 0x58000
	s_mov_b32 s99, 0
	v_lshl_add_u64 v[204:205], v[202:203], 0, s[98:99]
	global_load_dwordx4 v[244:247], v[204:205], off
	s_waitcnt vmcnt(8)
	v_lshlrev_b32_e32 v60, 16, v212
	v_and_b32_e32 v61, 0xffff0000, v212
	v_lshlrev_b32_e32 v48, 16, v213
	v_and_b32_e32 v49, 0xffff0000, v213
	v_lshlrev_b32_e32 v62, 16, v214
	v_and_b32_e32 v63, 0xffff0000, v214
	v_lshlrev_b32_e32 v50, 16, v215
	v_and_b32_e32 v51, 0xffff0000, v215
	s_waitcnt vmcnt(5)
	v_lshlrev_b32_e32 v66, 16, v218
	v_and_b32_e32 v67, 0xffff0000, v218
	v_lshlrev_b32_e32 v54, 16, v219
	v_and_b32_e32 v55, 0xffff0000, v219
	v_pk_fma_f32 v[46:47], v[46:47], v[110:111], v[48:49]
	v_pk_fma_f32 v[44:45], v[44:45], v[108:109], v[60:61]
	v_lshlrev_b32_e32 v64, 16, v216
	v_and_b32_e32 v65, 0xffff0000, v216
	v_lshlrev_b32_e32 v52, 16, v217
	v_and_b32_e32 v53, 0xffff0000, v217
	v_pk_fma_f32 v[42:43], v[42:43], v[106:107], v[50:51]
	v_pk_fma_f32 v[40:41], v[40:41], v[104:105], v[62:63]
	v_pk_fma_f32 v[50:51], v[34:35], v[94:95], v[54:55]
	v_pk_fma_f32 v[32:33], v[32:33], v[92:93], v[66:67]
	v_cvt_pk_bf16_f32 v34, v44, v45
	v_cvt_pk_bf16_f32 v35, v46, v47
	v_pk_fma_f32 v[48:49], v[38:39], v[102:103], v[52:53]
	v_pk_fma_f32 v[38:39], v[36:37], v[100:101], v[64:65]
	v_cvt_pk_bf16_f32 v36, v40, v41
	v_cvt_pk_bf16_f32 v37, v42, v43
	v_cvt_pk_bf16_f32 v40, v32, v33
	v_and_b32_e32 v33, 0xffff0000, v34
	v_and_b32_e32 v43, 0xffff0000, v35
	v_lshlrev_b32_e32 v32, 16, v34
	v_lshlrev_b32_e32 v42, 16, v35
	v_and_b32_e32 v45, 0xffff0000, v36
	v_mul_f32_e32 v33, v33, v33
	v_mul_f32_e32 v43, v43, v43
	v_cvt_pk_bf16_f32 v38, v38, v39
	v_lshlrev_b32_e32 v44, 16, v36
	v_and_b32_e32 v47, 0xffff0000, v37
	v_mul_f32_e32 v45, v45, v45
	v_fmac_f32_e32 v33, v32, v32
	v_fmac_f32_e32 v43, v42, v42
	v_cvt_pk_bf16_f32 v39, v48, v49
	v_lshlrev_b32_e32 v46, 16, v37
	v_and_b32_e32 v49, 0xffff0000, v38
	v_mul_f32_e32 v47, v47, v47
	v_fmac_f32_e32 v45, v44, v44
	v_add_f32_e32 v32, v33, v43
	v_cvt_pk_bf16_f32 v41, v50, v51
	v_lshlrev_b32_e32 v48, 16, v38
	v_and_b32_e32 v51, 0xffff0000, v39
	v_mul_f32_e32 v49, v49, v49
	v_fmac_f32_e32 v47, v46, v46
	v_add_f32_e32 v32, v45, v32
	v_lshlrev_b32_e32 v50, 16, v39
	v_and_b32_e32 v53, 0xffff0000, v40
	v_mul_f32_e32 v51, v51, v51
	v_fmac_f32_e32 v49, v48, v48
	v_add_f32_e32 v32, v47, v32
	v_lshlrev_b32_e32 v52, 16, v40
	v_and_b32_e32 v55, 0xffff0000, v41
	v_mul_f32_e32 v53, v53, v53
	v_fmac_f32_e32 v51, v50, v50
	v_add_f32_e32 v32, v49, v32
	v_lshlrev_b32_e32 v54, 16, v41
	v_mul_f32_e32 v55, v55, v55
	v_fmac_f32_e32 v53, v52, v52
	v_add_f32_e32 v32, v51, v32
	v_add_f32_e32 v32, v53, v32
	v_fmac_f32_e32 v55, v54, v54
	v_add_f32_e32 v32, v55, v32
	ds_bpermute_b32 v33, v183, v32
	global_store_dwordx4 v[56:57], v[34:37], off
	global_store_dwordx4 v[58:59], v[38:41], off offset:256
	s_waitcnt lgkmcnt(0)
	v_add_f32_e32 v32, v32, v33
	ds_bpermute_b32 v33, v182, v32
	s_and_saveexec_b64 s[0:1], s[14:15]
	s_cbranch_execz .LBB0_2541
	s_waitcnt lgkmcnt(0)
	v_add_f32_e32 v34, v32, v33
	v_lshlrev_b64 v[32:33], 6, v[128:129]
	v_lshl_add_u64 v[32:33], s[22:23], 0, v[32:33]
	s_lshl_b32 s20, s2, 2
	v_lshl_add_u64 v[32:33], v[32:33], 0, s[20:21]
	v_lshl_add_u64 v[32:33], v[32:33], 0, v[152:153]
	v_add_co_u32_e32 v32, vcc, 0x2000, v32
	s_nop 1
	v_addc_co_u32_e32 v33, vcc, 0, v33, vcc
	global_store_dword v[32:33], v34, off offset:1024
.LBB0_2541:
	s_or_b64 exec, exec, s[0:1]
	s_waitcnt lgkmcnt(0)
	v_lshlrev_b64 v[32:33], 11, v[160:161]
	v_lshl_add_u64 v[32:33], v[158:159], 0, v[32:33]
	v_add_co_u32_e32 v42, vcc, 0x50000, v32
	s_mov_b64 s[0:1], 0x50000
	s_nop 0
	v_addc_co_u32_e32 v43, vcc, 0, v33, vcc
	s_mov_b32 s98, 0x58000
	s_mov_b32 s99, 0
	v_lshl_add_u64 v[204:205], v[202:203], 0, s[98:99]
	global_load_dwordx4 v[212:215], v[204:205], off offset:256
	v_lshl_add_u64 v[44:45], v[32:33], 0, s[0:1]
	s_waitcnt vmcnt(7)
	v_lshlrev_b32_e32 v46, 16, v220
	v_and_b32_e32 v47, 0xffff0000, v220
	v_lshlrev_b32_e32 v34, 16, v221
	v_and_b32_e32 v35, 0xffff0000, v221
	v_lshlrev_b32_e32 v48, 16, v222
	v_and_b32_e32 v49, 0xffff0000, v222
	v_lshlrev_b32_e32 v36, 16, v223
	v_and_b32_e32 v37, 0xffff0000, v223
	s_waitcnt vmcnt(4)
	v_lshlrev_b32_e32 v52, 16, v226
	v_and_b32_e32 v53, 0xffff0000, v226
	v_lshlrev_b32_e32 v40, 16, v227
	v_and_b32_e32 v41, 0xffff0000, v227
	v_pk_fma_f32 v[30:31], v[30:31], v[110:111], v[34:35]
	v_pk_fma_f32 v[28:29], v[28:29], v[108:109], v[46:47]
	v_lshlrev_b32_e32 v50, 16, v224
	v_and_b32_e32 v51, 0xffff0000, v224
	v_lshlrev_b32_e32 v38, 16, v225
	v_and_b32_e32 v39, 0xffff0000, v225
	v_pk_fma_f32 v[26:27], v[26:27], v[106:107], v[36:37]
	v_pk_fma_f32 v[24:25], v[24:25], v[104:105], v[48:49]
	v_pk_fma_f32 v[36:37], v[18:19], v[94:95], v[40:41]
	v_pk_fma_f32 v[16:17], v[16:17], v[92:93], v[52:53]
	v_cvt_pk_bf16_f32 v18, v28, v29
	v_cvt_pk_bf16_f32 v19, v30, v31
	v_pk_fma_f32 v[34:35], v[22:23], v[102:103], v[38:39]
	v_pk_fma_f32 v[22:23], v[20:21], v[100:101], v[50:51]
	v_cvt_pk_bf16_f32 v20, v24, v25
	v_cvt_pk_bf16_f32 v21, v26, v27
	v_cvt_pk_bf16_f32 v24, v16, v17
	v_and_b32_e32 v17, 0xffff0000, v18
	v_and_b32_e32 v27, 0xffff0000, v19
	v_lshlrev_b32_e32 v16, 16, v18
	v_lshlrev_b32_e32 v26, 16, v19
	v_and_b32_e32 v29, 0xffff0000, v20
	v_mul_f32_e32 v17, v17, v17
	v_mul_f32_e32 v27, v27, v27
	v_cvt_pk_bf16_f32 v22, v22, v23
	v_lshlrev_b32_e32 v28, 16, v20
	v_and_b32_e32 v31, 0xffff0000, v21
	v_mul_f32_e32 v29, v29, v29
	v_fmac_f32_e32 v17, v16, v16
	v_fmac_f32_e32 v27, v26, v26
	v_cvt_pk_bf16_f32 v23, v34, v35
	v_lshlrev_b32_e32 v30, 16, v21
	v_and_b32_e32 v35, 0xffff0000, v22
	v_mul_f32_e32 v31, v31, v31
	v_fmac_f32_e32 v29, v28, v28
	v_add_f32_e32 v16, v17, v27
	v_cvt_pk_bf16_f32 v25, v36, v37
	v_lshlrev_b32_e32 v34, 16, v22
	v_and_b32_e32 v37, 0xffff0000, v23
	v_mul_f32_e32 v35, v35, v35
	v_fmac_f32_e32 v31, v30, v30
	v_add_f32_e32 v16, v29, v16
	v_lshlrev_b32_e32 v36, 16, v23
	v_and_b32_e32 v39, 0xffff0000, v24
	v_mul_f32_e32 v37, v37, v37
	v_fmac_f32_e32 v35, v34, v34
	v_add_f32_e32 v16, v31, v16
	v_lshlrev_b32_e32 v38, 16, v24
	v_and_b32_e32 v41, 0xffff0000, v25
	v_mul_f32_e32 v39, v39, v39
	v_fmac_f32_e32 v37, v36, v36
	v_add_f32_e32 v16, v35, v16
	v_lshlrev_b32_e32 v40, 16, v25
	v_mul_f32_e32 v41, v41, v41
	v_fmac_f32_e32 v39, v38, v38
	v_add_f32_e32 v16, v37, v16
	v_add_f32_e32 v16, v39, v16
	v_fmac_f32_e32 v41, v40, v40
	v_add_f32_e32 v16, v41, v16
	ds_bpermute_b32 v17, v183, v16
	global_store_dwordx4 v[42:43], v[18:21], off
	global_store_dwordx4 v[44:45], v[22:25], off offset:256
	s_waitcnt lgkmcnt(0)
	v_add_f32_e32 v16, v16, v17
	ds_bpermute_b32 v17, v182, v16
	s_and_saveexec_b64 s[0:1], s[14:15]
	s_cbranch_execz .LBB0_2543
	s_waitcnt lgkmcnt(0)
	v_add_f32_e32 v18, v16, v17
	v_lshlrev_b64 v[16:17], 6, v[128:129]
	v_lshl_add_u64 v[16:17], s[22:23], 0, v[16:17]
	s_lshl_b32 s20, s2, 2
	v_lshl_add_u64 v[16:17], v[16:17], 0, s[20:21]
	v_lshl_add_u64 v[16:17], v[16:17], 0, v[152:153]
	v_add_co_u32_e32 v16, vcc, 0x2000, v16
	s_nop 1
	v_addc_co_u32_e32 v17, vcc, 0, v17, vcc
	global_store_dword v[16:17], v18, off offset:2048
.LBB0_2543:
	s_or_b64 exec, exec, s[0:1]
	v_add_co_u32_e32 v24, vcc, 0x58000, v32
	s_mov_b64 s[0:1], 0x58000
	s_nop 0
	v_addc_co_u32_e32 v25, vcc, 0, v33, vcc
	s_waitcnt lgkmcnt(0)
	v_lshl_add_u64 v[26:27], v[32:33], 0, s[0:1]
	s_waitcnt vmcnt(5)
	v_lshlrev_b32_e32 v28, 16, v244
	v_and_b32_e32 v29, 0xffff0000, v244
	v_lshlrev_b32_e32 v16, 16, v245
	v_and_b32_e32 v17, 0xffff0000, v245
	v_lshlrev_b32_e32 v30, 16, v246
	v_and_b32_e32 v31, 0xffff0000, v246
	v_lshlrev_b32_e32 v18, 16, v247
	v_and_b32_e32 v19, 0xffff0000, v247
	s_waitcnt vmcnt(2)
	v_lshlrev_b32_e32 v34, 16, v214
	v_and_b32_e32 v35, 0xffff0000, v214
	v_lshlrev_b32_e32 v22, 16, v215
	v_and_b32_e32 v23, 0xffff0000, v215
	v_pk_fma_f32 v[14:15], v[14:15], v[110:111], v[16:17]
	v_pk_fma_f32 v[12:13], v[12:13], v[108:109], v[28:29]
	v_lshlrev_b32_e32 v32, 16, v212
	v_and_b32_e32 v33, 0xffff0000, v212
	v_lshlrev_b32_e32 v20, 16, v213
	v_and_b32_e32 v21, 0xffff0000, v213
	v_pk_fma_f32 v[10:11], v[10:11], v[106:107], v[18:19]
	v_pk_fma_f32 v[8:9], v[8:9], v[104:105], v[30:31]
	v_pk_fma_f32 v[18:19], v[2:3], v[94:95], v[22:23]
	v_pk_fma_f32 v[0:1], v[0:1], v[92:93], v[34:35]
	v_cvt_pk_bf16_f32 v2, v12, v13
	v_cvt_pk_bf16_f32 v3, v14, v15
	v_pk_fma_f32 v[16:17], v[6:7], v[102:103], v[20:21]
	v_pk_fma_f32 v[6:7], v[4:5], v[100:101], v[32:33]
	v_cvt_pk_bf16_f32 v4, v8, v9
	v_cvt_pk_bf16_f32 v5, v10, v11
	v_cvt_pk_bf16_f32 v8, v0, v1
	v_and_b32_e32 v1, 0xffff0000, v2
	v_and_b32_e32 v11, 0xffff0000, v3
	v_lshlrev_b32_e32 v0, 16, v2
	v_lshlrev_b32_e32 v10, 16, v3
	v_and_b32_e32 v13, 0xffff0000, v4
	v_mul_f32_e32 v1, v1, v1
	v_mul_f32_e32 v11, v11, v11
	v_cvt_pk_bf16_f32 v6, v6, v7
	v_lshlrev_b32_e32 v12, 16, v4
	v_and_b32_e32 v15, 0xffff0000, v5
	v_mul_f32_e32 v13, v13, v13
	v_fmac_f32_e32 v1, v0, v0
	v_fmac_f32_e32 v11, v10, v10
	v_cvt_pk_bf16_f32 v7, v16, v17
	v_lshlrev_b32_e32 v14, 16, v5
	v_and_b32_e32 v17, 0xffff0000, v6
	v_mul_f32_e32 v15, v15, v15
	v_fmac_f32_e32 v13, v12, v12
	v_add_f32_e32 v0, v1, v11
	v_cvt_pk_bf16_f32 v9, v18, v19
	v_lshlrev_b32_e32 v16, 16, v6
	v_and_b32_e32 v19, 0xffff0000, v7
	v_mul_f32_e32 v17, v17, v17
	v_fmac_f32_e32 v15, v14, v14
	v_add_f32_e32 v0, v13, v0
	v_lshlrev_b32_e32 v18, 16, v7
	v_and_b32_e32 v21, 0xffff0000, v8
	v_mul_f32_e32 v19, v19, v19
	v_fmac_f32_e32 v17, v16, v16
	v_add_f32_e32 v0, v15, v0
	v_lshlrev_b32_e32 v20, 16, v8
	v_and_b32_e32 v23, 0xffff0000, v9
	v_mul_f32_e32 v21, v21, v21
	v_fmac_f32_e32 v19, v18, v18
	v_add_f32_e32 v0, v17, v0
	v_lshlrev_b32_e32 v22, 16, v9
	v_mul_f32_e32 v23, v23, v23
	v_fmac_f32_e32 v21, v20, v20
	v_add_f32_e32 v0, v19, v0
	v_add_f32_e32 v0, v21, v0
	v_fmac_f32_e32 v23, v22, v22
	v_add_f32_e32 v0, v23, v0
	ds_bpermute_b32 v1, v183, v0
	global_store_dwordx4 v[24:25], v[2:5], off
	global_store_dwordx4 v[26:27], v[6:9], off offset:256
	s_waitcnt lgkmcnt(0)
	v_add_f32_e32 v0, v0, v1
	ds_bpermute_b32 v1, v182, v0
	s_and_saveexec_b64 s[0:1], s[14:15]
	s_cbranch_execz .LBB0_2522
	s_waitcnt lgkmcnt(0)
	v_add_f32_e32 v2, v0, v1
	v_lshlrev_b64 v[0:1], 6, v[128:129]
	v_lshl_add_u64 v[0:1], s[22:23], 0, v[0:1]
	s_lshl_b32 s20, s2, 2
	v_lshl_add_u64 v[0:1], v[0:1], 0, s[20:21]
	v_lshl_add_u64 v[0:1], v[0:1], 0, v[152:153]
	v_add_co_u32_e32 v0, vcc, 0x2000, v0
	s_nop 1
	v_addc_co_u32_e32 v1, vcc, 0, v1, vcc
	global_store_dword v[0:1], v2, off offset:3072
	s_branch .LBB0_2522

.LBB0_2625:
	s_or_b64 exec, exec, s[0:1]
	v_readlane_b32 s0, v242, 1
	s_waitcnt lgkmcnt(0)
	s_barrier
	s_nop 0
	s_mov_b32 s2, 0
	v_readlane_b32 s1, v242, 2
	s_load_dwordx2 s[8:9], s[0:1], s2 offset:0x108
	s_nop 0
	s_load_dwordx2 s[0:1], s[0:1], s2 offset:0x38
	v_mov_b32_e32 v68, v208
	s_mov_b32 s4, 0x8000
	s_waitcnt lgkmcnt(0)
	s_add_u32 s46, s8, 0x4000
	s_addc_u32 s47, s9, 0
	s_add_u32 s28, s8, 0x35df000
	s_addc_u32 s29, s9, 0
	s_add_u32 s2, s8, 0x2d0f000
	s_addc_u32 s3, s9, 0
	v_ashrrev_i32_e32 v69, 31, v68
	v_add_u32_e32 v32, 0x200, v68
	v_add_u32_e32 v34, 0x400, v68
	v_add_u32_e32 v36, 0x600, v68
	v_lshl_add_u64 v[16:17], v[68:69], 4, s[2:3]
	v_ashrrev_i32_e32 v33, 31, v32
	v_ashrrev_i32_e32 v35, 31, v34
	v_ashrrev_i32_e32 v37, 31, v36
	v_add_u32_e32 v38, 0xa00, v68
	v_lshl_add_u64 v[8:9], v[32:33], 4, s[2:3]
	global_load_dwordx4 v[0:3], v[16:17], off
	global_load_dwordx4 v[4:7], v[8:9], off
	v_lshl_add_u64 v[18:19], v[34:35], 4, s[2:3]
	v_lshl_add_u64 v[20:21], v[36:37], 4, s[2:3]
	v_add_co_u32_e32 v16, vcc, s4, v16
	v_ashrrev_i32_e32 v39, 31, v38
	global_load_dwordx4 v[8:11], v[18:19], off
	global_load_dwordx4 v[12:15], v[20:21], off
	v_addc_co_u32_e32 v17, vcc, 0, v17, vcc
	v_lshl_add_u64 v[20:21], v[38:39], 4, s[2:3]
	v_add_u32_e32 v40, 0xc00, v68
	global_load_dwordx4 v[16:19], v[16:17], off
	s_nop 0
	global_load_dwordx4 v[20:23], v[20:21], off
	v_ashrrev_i32_e32 v41, 31, v40
	v_lshl_add_u64 v[24:25], v[40:41], 4, s[2:3]
	global_load_dwordx4 v[24:27], v[24:25], off
	v_add_u32_e32 v42, 0xe00, v68
	v_ashrrev_i32_e32 v43, 31, v42
	v_lshl_add_u64 v[28:29], v[42:43], 4, s[2:3]
	global_load_dwordx4 v[28:31], v[28:29], off
	s_movk_i32 s3, 0x800
	s_add_i32 s5, 0, 0x8100
	v_mov_b32_e32 v48, s5
	v_cmp_gt_u32_e32 vcc, s3, v68
	s_movk_i32 s4, 0xf7ff
	v_bfe_u32 v44, v34, 7, 4
	v_cndmask_b32_e64 v49, v48, 0, vcc
	v_cmp_gt_u32_e32 vcc, s3, v32
	v_bfe_u32 v39, v68, 7, 4
	v_lshlrev_b32_e32 v41, 4, v68
	v_cndmask_b32_e64 v50, v48, 0, vcc
	v_cmp_gt_u32_e32 vcc, s3, v34
	v_bfe_u32 v45, v36, 7, 4
	v_mul_u32_u24_e32 v39, 0x810, v39
	v_cndmask_b32_e64 v34, v48, 0, vcc
	v_cmp_gt_u32_e32 vcc, s3, v36
	v_and_b32_e32 v41, 0x7f0, v41
	v_bfe_u32 v43, v32, 7, 4
	v_cndmask_b32_e64 v36, v48, 0, vcc
	v_cmp_lt_u32_e32 vcc, s4, v68
	v_bfe_u32 v46, v38, 7, 4
	v_bfe_u32 v47, v40, 7, 4
	v_cndmask_b32_e64 v51, v48, 0, vcc
	v_cmp_gt_u32_e32 vcc, s3, v38
	v_mul_u32_u24_e32 v43, 0x810, v43
	v_mul_u32_u24_e32 v44, 0x810, v44
	v_mul_u32_u24_e32 v45, 0x810, v45
	v_mul_u32_u24_e32 v46, 0x810, v46
	v_cndmask_b32_e64 v38, v48, 0, vcc
	v_cmp_gt_u32_e32 vcc, s3, v40
	v_add3_u32 v49, v49, v39, v41
	v_add3_u32 v43, v50, v43, v41
	v_cndmask_b32_e64 v40, v48, 0, vcc
	v_add3_u32 v34, v34, v44, v41
	v_add3_u32 v36, v36, v45, v41
	v_add3_u32 v39, v51, v39, v41
	v_add3_u32 v38, v38, v46, v41
	v_cmp_gt_u32_e32 vcc, s3, v42
	s_add_u32 s34, s0, 0x2000
	v_readlane_b32 s0, v242, 30
	v_ashrrev_i32_e32 v33, 6, v68
	v_bfe_u32 v37, v68, 4, 2
	v_and_b32_e32 v90, 15, v68
	v_mov_b32_e32 v71, 0
	v_lshlrev_b32_e32 v93, 2, v68
	s_addc_u32 s35, s1, 0
	v_lshlrev_b32_e32 v70, 4, v37
	s_movk_i32 s49, 0x1ff
	s_movk_i32 s2, 0x400
	v_lshrrev_b32_e32 v35, 4, v68
	s_waitcnt vmcnt(7)
	ds_write_b128 v49, v[0:3]
	s_waitcnt vmcnt(6)
	ds_write_b128 v43, v[4:7]
	s_waitcnt vmcnt(5)
	ds_write_b128 v34, v[8:11]
	s_waitcnt vmcnt(4)
	ds_write_b128 v36, v[12:15]
	s_waitcnt vmcnt(3)
	ds_write_b128 v39, v[16:19]
	s_waitcnt vmcnt(2)
	ds_write_b128 v38, v[20:23]
	v_mul_u32_u24_e32 v0, 0x810, v47
	v_add3_u32 v0, v40, v0, v41
	s_waitcnt vmcnt(1)
	ds_write_b128 v0, v[24:27]
	v_bfe_u32 v0, v42, 7, 4
	v_cndmask_b32_e64 v1, v48, 0, vcc
	v_mul_u32_u24_e32 v0, 0x810, v0
	v_add3_u32 v0, v1, v0, v41
	v_mov_b32_e32 v1, s0
	v_readlane_b32 s0, v242, 16
	s_waitcnt vmcnt(0)
	ds_write_b128 v0, v[28:31]
	v_mov_b32_e32 v0, 0x880
	v_cmp_gt_u32_e32 vcc, 64, v68
	v_add_u32_e32 v92, s0, v33
	v_readlane_b32 s0, v242, 32
	v_cndmask_b32_e32 v91, v0, v1, vcc
	v_mul_u32_u24_e32 v0, 0x408, v90
	v_add_u32_e32 v94, s0, v93
	v_readlane_b32 s0, v242, 33
	v_lshlrev_b32_e32 v2, 5, v37
	v_mov_b32_e32 v3, v71
	v_add_u32_e32 v95, s0, v93
	v_lshlrev_b32_e32 v5, 1, v0
	v_lshl_add_u32 v97, v90, 2, s0
	v_mul_u32_u24_e32 v0, 0x22000, v90
	v_mov_b32_e32 v1, v71
	v_lshl_add_u64 v[2:3], s[8:9], 0, v[2:3]
	s_mov_b64 s[0:1], 0x37ff000
	v_lshl_add_u64 v[72:73], v[2:3], 0, s[0:1]
	v_lshl_add_u64 v[2:3], s[8:9], 0, v[70:71]
	s_mov_b64 s[0:1], 0xdbff000
	v_lshl_add_u64 v[0:1], s[8:9], 0, v[0:1]
	v_lshl_add_u64 v[74:75], v[2:3], 0, s[0:1]
	v_lshl_add_u64 v[0:1], v[0:1], 0, v[70:71]
	s_mov_b64 s[0:1], 0x907000
	v_lshl_add_u64 v[76:77], v[0:1], 0, s[0:1]
	v_max_i32_e32 v0, 0x200, v68
	v_sub_u32_e32 v0, v0, v68
	v_add_u32_e32 v0, 0x1ff, v0
	v_lshrrev_b32_e32 v1, 9, v0
	v_add_u32_e32 v2, 1, v1
	v_add_u32_e32 v1, -1, v1
	v_lshrrev_b32_e32 v3, 1, v1
	v_add_u32_e32 v3, 1, v3
	v_lshlrev_b32_e32 v4, 1, v68
	v_cmp_lt_u32_e64 s[16:17], s49, v0
	v_and_b32_e32 v0, 0xfffffe, v2
	v_and_b32_e32 v6, 3, v3
	v_add_u32_e32 v109, 0, v93
	s_movk_i32 s0, 0xffe0
	s_mov_b32 s31, 0
	s_movk_i32 s48, 0x880
	v_cmp_gt_i32_e64 s[10:11], s2, v68
	v_cmp_gt_i32_e64 s[14:15], 16, v68
	v_add_u32_e32 v96, 0, v5
	v_or_b32_e32 v98, 31, v4
	v_or_b32_e32 v99, 8, v70
	v_or_b32_e32 v100, 4, v70
	v_or_b32_e32 v101, 12, v70
	v_lshl_add_u32 v78, v0, 9, v68
	v_mov_b32_e32 v80, v68
	v_mov_b32_e32 v81, v32
	v_cmp_lt_u32_e64 s[18:19], 5, v1
	v_and_b32_e32 v71, -4, v3
	v_cmp_ne_u32_e64 s[20:21], 0, v6
	v_cmp_ne_u32_e64 s[22:23], v2, v0
	v_or_b32_e32 v102, 64, v70
	v_or_b32_e32 v103, 0x80, v70
	v_or_b32_e32 v104, 0xc0, v70
	v_or_b32_e32 v105, 0x100, v70
	v_or_b32_e32 v106, 0x140, v70
	v_or_b32_e32 v107, 0x180, v70
	v_or_b32_e32 v108, 0x1c0, v70
	v_add_u32_e32 v110, 0x10200, v109
	v_lshlrev_b32_e32 v111, 12, v6
	v_lshl_add_u32 v112, v35, 6, v5
	v_and_or_b32 v113, v4, s0, 2
	v_lshlrev_b32_e32 v114, 7, v35
	s_mov_b64 s[0:1], -1
	s_movk_i32 s50, 0x4000
	s_movk_i32 s51, 0x3000
	v_mov_b32_e32 v115, 0x358637bd
	s_mov_b32 s52, 0xf800000
	v_mov_b32_e32 v116, 0x260
	s_mov_b64 s[26:27], -1
	s_branch .LBB0_2629

.LBB0_3524:
	s_lshl_b32 s2, s2, 8
	s_ashr_i32 s3, s2, 31
	s_lshl_b64 s[40:41], s[2:3], 11
	s_lshl_b64 s[6:7], s[6:7], 2
	v_bfe_u32 v152, v80, 6, 2
	v_bfe_u32 v200, v80, 4, 2
	s_add_u32 s6, s14, s6
	v_and_b32_e32 v180, 15, v80
	s_addc_u32 s7, s15, s7
	v_ashrrev_i32_e32 v82, 2, v80
	s_lshl_b32 s1, s0, 8
	v_lshlrev_b32_e32 v80, 5, v152
	v_lshlrev_b32_e32 v81, 3, v200
	v_or3_b32 v80, v80, s1, v81
	s_add_u32 s40, s65, s40
	v_and_or_b32 v160, v82, s77, v180
	v_ashrrev_i32_e32 v81, 31, v80
	s_addc_u32 s41, s66, s41
	v_ashrrev_i32_e32 v161, 31, v160
	v_lshl_add_u64 v[158:159], v[80:81], 1, s[40:41]
	v_lshlrev_b64 v[82:83], 11, v[160:161]
	v_lshl_add_u64 v[80:81], v[80:81], 2, s[6:7]
	v_lshl_add_u64 v[190:191], v[158:159], 0, v[82:83]
	v_add_co_u32_e32 v82, vcc, s76, v80
	v_mov_b32_e32 v202, v190
	v_mov_b32_e32 v203, v191
	global_load_dwordx4 v[204:207], v[202:203], off
	global_load_dwordx4 v[212:215], v[202:203], off offset:256
	s_mov_b32 s98, 0x8000
	s_mov_b32 s99, 0
	v_lshl_add_u64 v[210:211], v[202:203], 0, s[98:99]
	global_load_dwordx4 v[216:219], v[210:211], off
	s_mov_b32 s98, 0x8000
	s_mov_b32 s99, 0
	v_lshl_add_u64 v[210:211], v[202:203], 0, s[98:99]
	global_load_dwordx4 v[220:223], v[210:211], off offset:256
	s_mov_b32 s98, 0x10000
	s_mov_b32 s99, 0
	v_lshl_add_u64 v[210:211], v[202:203], 0, s[98:99]
	global_load_dwordx4 v[244:247], v[210:211], off
	v_addc_co_u32_e32 v83, vcc, 0, v81, vcc
	global_load_dwordx4 v[92:95], v[82:83], off
	v_lshl_add_u64 v[80:81], v[80:81], 0, s[22:23]
	global_load_dwordx4 v[88:91], v[80:81], off offset:16
	global_load_dwordx4 v[84:87], v[80:81], off offset:512
	s_nop 0
	global_load_dwordx4 v[80:83], v[80:81], off offset:528
	v_lshlrev_b32_e32 v192, 6, v200
	v_lshlrev_b32_e32 v180, 2, v180
	v_bitop3_b32 v181, v192, 64, v180 bitop3:0x36
	v_bitop3_b32 v180, v192, s75, v180 bitop3:0x36
	s_lshl_b32 s0, s0, 2
	v_cmp_eq_u32_e64 s[6:7], 0, v200
	v_lshlrev_b32_e32 v152, 2, v152
	s_waitcnt vmcnt(8)
	v_lshlrev_b32_e32 v192, 16, v204
	v_and_b32_e32 v193, 0xffff0000, v204
	v_lshlrev_b32_e32 v182, 16, v205
	v_and_b32_e32 v183, 0xffff0000, v205
	v_lshlrev_b32_e32 v194, 16, v206
	v_and_b32_e32 v195, 0xffff0000, v206
	v_lshlrev_b32_e32 v184, 16, v207
	v_and_b32_e32 v185, 0xffff0000, v207
	s_waitcnt vmcnt(7)
	v_lshlrev_b32_e32 v196, 16, v212
	v_and_b32_e32 v197, 0xffff0000, v212
	v_lshlrev_b32_e32 v198, 16, v214
	v_and_b32_e32 v199, 0xffff0000, v214
	v_lshlrev_b32_e32 v188, 16, v215
	v_and_b32_e32 v189, 0xffff0000, v215
	s_waitcnt vmcnt(3)
	v_pk_fma_f32 v[142:143], v[142:143], v[94:95], v[182:183]
	v_pk_fma_f32 v[140:141], v[140:141], v[92:93], v[192:193]
	v_lshlrev_b32_e32 v186, 16, v213
	v_and_b32_e32 v187, 0xffff0000, v213
	s_waitcnt vmcnt(2)
	v_pk_fma_f32 v[138:139], v[138:139], v[90:91], v[184:185]
	v_pk_fma_f32 v[136:137], v[136:137], v[88:89], v[194:195]
	s_waitcnt vmcnt(1)
	v_pk_fma_f32 v[184:185], v[132:133], v[84:85], v[196:197]
	s_waitcnt vmcnt(0)
	v_pk_fma_f32 v[130:131], v[130:131], v[82:83], v[188:189]
	v_pk_fma_f32 v[128:129], v[128:129], v[80:81], v[198:199]
	v_cvt_pk_bf16_f32 v132, v140, v141
	v_cvt_pk_bf16_f32 v133, v142, v143
	v_pk_fma_f32 v[182:183], v[134:135], v[86:87], v[186:187]
	v_cvt_pk_bf16_f32 v134, v136, v137
	v_cvt_pk_bf16_f32 v135, v138, v139
	v_cvt_pk_bf16_f32 v138, v128, v129
	v_cvt_pk_bf16_f32 v139, v130, v131
	v_and_b32_e32 v129, 0xffff0000, v132
	v_and_b32_e32 v131, 0xffff0000, v133
	v_lshlrev_b32_e32 v128, 16, v132
	v_lshlrev_b32_e32 v130, 16, v133
	v_and_b32_e32 v141, 0xffff0000, v134
	v_mul_f32_e32 v129, v129, v129
	v_mul_f32_e32 v131, v131, v131
	v_cvt_pk_bf16_f32 v136, v184, v185
	v_lshlrev_b32_e32 v140, 16, v134
	v_and_b32_e32 v143, 0xffff0000, v135
	v_mul_f32_e32 v141, v141, v141
	v_fmac_f32_e32 v129, v128, v128
	v_fmac_f32_e32 v131, v130, v130
	v_cvt_pk_bf16_f32 v137, v182, v183
	v_lshlrev_b32_e32 v142, 16, v135
	v_and_b32_e32 v183, 0xffff0000, v136
	v_mul_f32_e32 v143, v143, v143
	v_fmac_f32_e32 v141, v140, v140
	v_add_f32_e32 v128, v129, v131
	v_lshlrev_b32_e32 v182, 16, v136
	v_and_b32_e32 v185, 0xffff0000, v137
	v_mul_f32_e32 v183, v183, v183
	v_fmac_f32_e32 v143, v142, v142
	v_add_f32_e32 v128, v141, v128
	v_lshlrev_b32_e32 v184, 16, v137
	v_mul_f32_e32 v185, v185, v185
	v_fmac_f32_e32 v183, v182, v182
	v_add_f32_e32 v128, v143, v128
	v_and_b32_e32 v129, 0xffff0000, v138
	v_lshlrev_b32_e32 v186, 16, v138
	v_fmac_f32_e32 v185, v184, v184
	v_add_f32_e32 v128, v183, v128
	v_mul_f32_e32 v129, v129, v129
	v_add_f32_e32 v128, v185, v128
	v_fmac_f32_e32 v129, v186, v186
	v_and_b32_e32 v130, 0xffff0000, v139
	v_add_f32_e32 v128, v129, v128
	v_lshlrev_b32_e32 v129, 16, v139
	v_mul_f32_e32 v130, v130, v130
	v_fmac_f32_e32 v130, v129, v129
	v_add_f32_e32 v129, v130, v128
	ds_bpermute_b32 v130, v181, v129
	v_add_u32_e32 v128, s2, v160
	s_and_b32 s2, s0, 12
	global_store_dwordx4 v[190:191], v[132:135], off
	global_store_dwordx4 v[190:191], v[136:139], off offset:256
	s_waitcnt lgkmcnt(0)
	v_add_f32_e32 v130, v129, v130
	ds_bpermute_b32 v131, v180, v130
	v_ashrrev_i32_e32 v129, 31, v128
	s_and_saveexec_b64 s[0:1], s[6:7]
	s_cbranch_execz .LBB0_3526
	s_waitcnt lgkmcnt(0)
	v_add_f32_e32 v132, v130, v131
	v_lshlrev_b64 v[130:131], 6, v[128:129]
	v_lshl_add_u64 v[130:131], s[20:21], 0, v[130:131]
	s_lshl_b32 s16, s2, 2
	v_lshl_add_u64 v[130:131], v[130:131], 0, s[16:17]
	v_lshl_add_u64 v[130:131], v[130:131], 0, v[152:153]
	global_store_dword v[130:131], v132, off
.LBB0_3526:
	s_or_b64 exec, exec, s[0:1]
	v_or_b32_e32 v130, 16, v160
	s_waitcnt lgkmcnt(0)
	v_ashrrev_i32_e32 v131, 31, v130
	v_lshlrev_b64 v[130:131], 11, v[130:131]
	v_lshl_add_u64 v[138:139], v[158:159], 0, v[130:131]
	s_mov_b32 s98, 0x10000
	s_mov_b32 s99, 0
	v_lshl_add_u64 v[210:211], v[202:203], 0, s[98:99]
	global_load_dwordx4 v[204:207], v[210:211], off offset:256
	s_mov_b32 s98, 0x18000
	s_mov_b32 s99, 0
	v_lshl_add_u64 v[210:211], v[202:203], 0, s[98:99]
	global_load_dwordx4 v[212:215], v[210:211], off
	s_waitcnt vmcnt(10)
	v_lshlrev_b32_e32 v140, 16, v216
	v_and_b32_e32 v141, 0xffff0000, v216
	v_lshlrev_b32_e32 v130, 16, v217
	v_and_b32_e32 v131, 0xffff0000, v217
	v_lshlrev_b32_e32 v142, 16, v218
	v_and_b32_e32 v143, 0xffff0000, v218
	v_lshlrev_b32_e32 v132, 16, v219
	v_and_b32_e32 v133, 0xffff0000, v219
	s_waitcnt vmcnt(9)
	v_lshlrev_b32_e32 v184, 16, v222
	v_and_b32_e32 v185, 0xffff0000, v222
	v_lshlrev_b32_e32 v136, 16, v223
	v_and_b32_e32 v137, 0xffff0000, v223
	v_pk_fma_f32 v[126:127], v[126:127], v[94:95], v[130:131]
	v_pk_fma_f32 v[124:125], v[124:125], v[92:93], v[140:141]
	v_lshlrev_b32_e32 v182, 16, v220
	v_and_b32_e32 v183, 0xffff0000, v220
	v_lshlrev_b32_e32 v134, 16, v221
	v_and_b32_e32 v135, 0xffff0000, v221
	v_pk_fma_f32 v[122:123], v[122:123], v[90:91], v[132:133]
	v_pk_fma_f32 v[120:121], v[120:121], v[88:89], v[142:143]
	v_pk_fma_f32 v[132:133], v[114:115], v[82:83], v[136:137]
	v_pk_fma_f32 v[112:113], v[112:113], v[80:81], v[184:185]
	v_cvt_pk_bf16_f32 v114, v124, v125
	v_cvt_pk_bf16_f32 v115, v126, v127
	v_pk_fma_f32 v[130:131], v[118:119], v[86:87], v[134:135]
	v_pk_fma_f32 v[118:119], v[116:117], v[84:85], v[182:183]
	v_cvt_pk_bf16_f32 v116, v120, v121
	v_cvt_pk_bf16_f32 v117, v122, v123
	v_cvt_pk_bf16_f32 v120, v112, v113
	v_and_b32_e32 v113, 0xffff0000, v114
	v_and_b32_e32 v123, 0xffff0000, v115
	v_lshlrev_b32_e32 v112, 16, v114
	v_lshlrev_b32_e32 v122, 16, v115
	v_and_b32_e32 v125, 0xffff0000, v116
	v_mul_f32_e32 v113, v113, v113
	v_mul_f32_e32 v123, v123, v123
	v_cvt_pk_bf16_f32 v118, v118, v119
	v_lshlrev_b32_e32 v124, 16, v116
	v_and_b32_e32 v127, 0xffff0000, v117
	v_mul_f32_e32 v125, v125, v125
	v_fmac_f32_e32 v113, v112, v112
	v_fmac_f32_e32 v123, v122, v122
	v_cvt_pk_bf16_f32 v119, v130, v131
	v_lshlrev_b32_e32 v126, 16, v117
	v_and_b32_e32 v131, 0xffff0000, v118
	v_mul_f32_e32 v127, v127, v127
	v_fmac_f32_e32 v125, v124, v124
	v_add_f32_e32 v112, v113, v123
	v_cvt_pk_bf16_f32 v121, v132, v133
	v_lshlrev_b32_e32 v130, 16, v118
	v_and_b32_e32 v133, 0xffff0000, v119
	v_mul_f32_e32 v131, v131, v131
	v_fmac_f32_e32 v127, v126, v126
	v_add_f32_e32 v112, v125, v112
	v_lshlrev_b32_e32 v132, 16, v119
	v_and_b32_e32 v135, 0xffff0000, v120
	v_mul_f32_e32 v133, v133, v133
	v_fmac_f32_e32 v131, v130, v130
	v_add_f32_e32 v112, v127, v112
	v_lshlrev_b32_e32 v134, 16, v120
	v_and_b32_e32 v137, 0xffff0000, v121
	v_mul_f32_e32 v135, v135, v135
	v_fmac_f32_e32 v133, v132, v132
	v_add_f32_e32 v112, v131, v112
	v_lshlrev_b32_e32 v136, 16, v121
	v_mul_f32_e32 v137, v137, v137
	v_fmac_f32_e32 v135, v134, v134
	v_add_f32_e32 v112, v133, v112
	v_add_f32_e32 v112, v135, v112
	v_fmac_f32_e32 v137, v136, v136
	v_add_f32_e32 v112, v137, v112
	ds_bpermute_b32 v113, v181, v112
	global_store_dwordx4 v[138:139], v[114:117], off
	global_store_dwordx4 v[138:139], v[118:121], off offset:256
	s_waitcnt lgkmcnt(0)
	v_add_f32_e32 v112, v112, v113
	ds_bpermute_b32 v113, v180, v112
	s_and_saveexec_b64 s[0:1], s[6:7]
	s_cbranch_execz .LBB0_3528
	s_waitcnt lgkmcnt(0)
	v_add_f32_e32 v114, v112, v113
	v_or_b32_e32 v112, 16, v128
	v_ashrrev_i32_e32 v113, 31, v112
	v_lshlrev_b64 v[112:113], 6, v[112:113]
	v_lshl_add_u64 v[112:113], s[20:21], 0, v[112:113]
	s_lshl_b32 s16, s2, 2
	v_lshl_add_u64 v[112:113], v[112:113], 0, s[16:17]
	v_lshl_add_u64 v[112:113], v[112:113], 0, v[152:153]
	global_store_dword v[112:113], v114, off
.LBB0_3528:
	s_or_b64 exec, exec, s[0:1]
	v_or_b32_e32 v112, 32, v160
	s_waitcnt lgkmcnt(0)
	v_ashrrev_i32_e32 v113, 31, v112
	v_lshlrev_b64 v[112:113], 11, v[112:113]
	v_lshl_add_u64 v[120:121], v[158:159], 0, v[112:113]
	s_mov_b32 s98, 0x18000
	s_mov_b32 s99, 0
	v_lshl_add_u64 v[210:211], v[202:203], 0, s[98:99]
	global_load_dwordx4 v[216:219], v[210:211], off offset:256
	s_mov_b32 s98, 0x40000
	s_mov_b32 s99, 0
	v_lshl_add_u64 v[210:211], v[202:203], 0, s[98:99]
	global_load_dwordx4 v[220:223], v[210:211], off
	s_waitcnt vmcnt(12)
	v_lshlrev_b32_e32 v122, 16, v244
	v_and_b32_e32 v123, 0xffff0000, v244
	v_lshlrev_b32_e32 v112, 16, v245
	v_and_b32_e32 v113, 0xffff0000, v245
	v_lshlrev_b32_e32 v124, 16, v246
	v_and_b32_e32 v125, 0xffff0000, v246
	v_lshlrev_b32_e32 v114, 16, v247
	v_and_b32_e32 v115, 0xffff0000, v247
	s_waitcnt vmcnt(5)
	v_lshlrev_b32_e32 v130, 16, v206
	v_and_b32_e32 v131, 0xffff0000, v206
	v_lshlrev_b32_e32 v118, 16, v207
	v_and_b32_e32 v119, 0xffff0000, v207
	v_pk_fma_f32 v[110:111], v[110:111], v[94:95], v[112:113]
	v_pk_fma_f32 v[108:109], v[108:109], v[92:93], v[122:123]
	v_lshlrev_b32_e32 v126, 16, v204
	v_and_b32_e32 v127, 0xffff0000, v204
	v_lshlrev_b32_e32 v116, 16, v205
	v_and_b32_e32 v117, 0xffff0000, v205
	v_pk_fma_f32 v[106:107], v[106:107], v[90:91], v[114:115]
	v_pk_fma_f32 v[104:105], v[104:105], v[88:89], v[124:125]
	v_pk_fma_f32 v[114:115], v[98:99], v[82:83], v[118:119]
	v_pk_fma_f32 v[96:97], v[96:97], v[80:81], v[130:131]
	v_cvt_pk_bf16_f32 v98, v108, v109
	v_cvt_pk_bf16_f32 v99, v110, v111
	v_pk_fma_f32 v[112:113], v[102:103], v[86:87], v[116:117]
	v_pk_fma_f32 v[102:103], v[100:101], v[84:85], v[126:127]
	v_cvt_pk_bf16_f32 v100, v104, v105
	v_cvt_pk_bf16_f32 v101, v106, v107
	v_cvt_pk_bf16_f32 v104, v96, v97
	v_and_b32_e32 v97, 0xffff0000, v98
	v_and_b32_e32 v107, 0xffff0000, v99
	v_lshlrev_b32_e32 v96, 16, v98
	v_lshlrev_b32_e32 v106, 16, v99
	v_and_b32_e32 v109, 0xffff0000, v100
	v_mul_f32_e32 v97, v97, v97
	v_mul_f32_e32 v107, v107, v107
	v_cvt_pk_bf16_f32 v102, v102, v103
	v_lshlrev_b32_e32 v108, 16, v100
	v_and_b32_e32 v111, 0xffff0000, v101
	v_mul_f32_e32 v109, v109, v109
	v_fmac_f32_e32 v97, v96, v96
	v_fmac_f32_e32 v107, v106, v106
	v_cvt_pk_bf16_f32 v103, v112, v113
	v_lshlrev_b32_e32 v110, 16, v101
	v_and_b32_e32 v113, 0xffff0000, v102
	v_mul_f32_e32 v111, v111, v111
	v_fmac_f32_e32 v109, v108, v108
	v_add_f32_e32 v96, v97, v107
	v_cvt_pk_bf16_f32 v105, v114, v115
	v_lshlrev_b32_e32 v112, 16, v102
	v_and_b32_e32 v115, 0xffff0000, v103
	v_mul_f32_e32 v113, v113, v113
	v_fmac_f32_e32 v111, v110, v110
	v_add_f32_e32 v96, v109, v96
	v_lshlrev_b32_e32 v114, 16, v103
	v_and_b32_e32 v117, 0xffff0000, v104
	v_mul_f32_e32 v115, v115, v115
	v_fmac_f32_e32 v113, v112, v112
	v_add_f32_e32 v96, v111, v96
	v_lshlrev_b32_e32 v116, 16, v104
	v_and_b32_e32 v119, 0xffff0000, v105
	v_mul_f32_e32 v117, v117, v117
	v_fmac_f32_e32 v115, v114, v114
	v_add_f32_e32 v96, v113, v96
	v_lshlrev_b32_e32 v118, 16, v105
	v_mul_f32_e32 v119, v119, v119
	v_fmac_f32_e32 v117, v116, v116
	v_add_f32_e32 v96, v115, v96
	v_add_f32_e32 v96, v117, v96
	v_fmac_f32_e32 v119, v118, v118
	v_add_f32_e32 v96, v119, v96
	ds_bpermute_b32 v97, v181, v96
	global_store_dwordx4 v[120:121], v[98:101], off
	global_store_dwordx4 v[120:121], v[102:105], off offset:256
	s_waitcnt lgkmcnt(0)
	v_add_f32_e32 v96, v96, v97
	ds_bpermute_b32 v97, v180, v96
	s_and_saveexec_b64 s[0:1], s[6:7]
	s_cbranch_execz .LBB0_3530
	s_waitcnt lgkmcnt(0)
	v_add_f32_e32 v98, v96, v97
	v_or_b32_e32 v96, 32, v128
	v_ashrrev_i32_e32 v97, 31, v96
	v_lshlrev_b64 v[96:97], 6, v[96:97]
	v_lshl_add_u64 v[96:97], s[20:21], 0, v[96:97]
	s_lshl_b32 s16, s2, 2
	v_lshl_add_u64 v[96:97], v[96:97], 0, s[16:17]
	v_lshl_add_u64 v[96:97], v[96:97], 0, v[152:153]
	global_store_dword v[96:97], v98, off
.LBB0_3530:
	s_or_b64 exec, exec, s[0:1]
	v_or_b32_e32 v96, 48, v160
	s_waitcnt lgkmcnt(0)
	v_ashrrev_i32_e32 v97, 31, v96
	v_lshlrev_b64 v[96:97], 11, v[96:97]
	v_lshl_add_u64 v[104:105], v[158:159], 0, v[96:97]
	s_mov_b32 s98, 0x40000
	s_mov_b32 s99, 0
	v_lshl_add_u64 v[210:211], v[202:203], 0, s[98:99]
	global_load_dwordx4 v[244:247], v[210:211], off offset:256
	s_mov_b32 s98, 0x48000
	s_mov_b32 s99, 0
	v_lshl_add_u64 v[210:211], v[202:203], 0, s[98:99]
	global_load_dwordx4 v[204:207], v[210:211], off
	s_waitcnt vmcnt(8)
	v_lshlrev_b32_e32 v106, 16, v212
	v_and_b32_e32 v107, 0xffff0000, v212
	v_lshlrev_b32_e32 v96, 16, v213
	v_and_b32_e32 v97, 0xffff0000, v213
	v_lshlrev_b32_e32 v108, 16, v214
	v_and_b32_e32 v109, 0xffff0000, v214
	v_lshlrev_b32_e32 v98, 16, v215
	v_and_b32_e32 v99, 0xffff0000, v215
	s_waitcnt vmcnt(5)
	v_lshlrev_b32_e32 v112, 16, v218
	v_and_b32_e32 v113, 0xffff0000, v218
	v_lshlrev_b32_e32 v102, 16, v219
	v_and_b32_e32 v103, 0xffff0000, v219
	v_pk_fma_f32 v[78:79], v[78:79], v[94:95], v[96:97]
	v_pk_fma_f32 v[76:77], v[76:77], v[92:93], v[106:107]
	v_lshlrev_b32_e32 v110, 16, v216
	v_and_b32_e32 v111, 0xffff0000, v216
	v_lshlrev_b32_e32 v100, 16, v217
	v_and_b32_e32 v101, 0xffff0000, v217
	v_pk_fma_f32 v[74:75], v[74:75], v[90:91], v[98:99]
	v_pk_fma_f32 v[72:73], v[72:73], v[88:89], v[108:109]
	v_pk_fma_f32 v[98:99], v[66:67], v[82:83], v[102:103]
	v_pk_fma_f32 v[64:65], v[64:65], v[80:81], v[112:113]
	v_cvt_pk_bf16_f32 v66, v76, v77
	v_cvt_pk_bf16_f32 v67, v78, v79
	v_pk_fma_f32 v[96:97], v[70:71], v[86:87], v[100:101]
	v_pk_fma_f32 v[70:71], v[68:69], v[84:85], v[110:111]
	v_cvt_pk_bf16_f32 v68, v72, v73
	v_cvt_pk_bf16_f32 v69, v74, v75
	v_cvt_pk_bf16_f32 v72, v64, v65
	v_and_b32_e32 v65, 0xffff0000, v66
	v_and_b32_e32 v75, 0xffff0000, v67
	v_lshlrev_b32_e32 v64, 16, v66
	v_lshlrev_b32_e32 v74, 16, v67
	v_and_b32_e32 v77, 0xffff0000, v68
	v_mul_f32_e32 v65, v65, v65
	v_mul_f32_e32 v75, v75, v75
	v_cvt_pk_bf16_f32 v70, v70, v71
	v_lshlrev_b32_e32 v76, 16, v68
	v_and_b32_e32 v79, 0xffff0000, v69
	v_mul_f32_e32 v77, v77, v77
	v_fmac_f32_e32 v65, v64, v64
	v_fmac_f32_e32 v75, v74, v74
	v_cvt_pk_bf16_f32 v71, v96, v97
	v_lshlrev_b32_e32 v78, 16, v69
	v_and_b32_e32 v97, 0xffff0000, v70
	v_mul_f32_e32 v79, v79, v79
	v_fmac_f32_e32 v77, v76, v76
	v_add_f32_e32 v64, v65, v75
	v_cvt_pk_bf16_f32 v73, v98, v99
	v_lshlrev_b32_e32 v96, 16, v70
	v_and_b32_e32 v99, 0xffff0000, v71
	v_mul_f32_e32 v97, v97, v97
	v_fmac_f32_e32 v79, v78, v78
	v_add_f32_e32 v64, v77, v64
	v_lshlrev_b32_e32 v98, 16, v71
	v_and_b32_e32 v101, 0xffff0000, v72
	v_mul_f32_e32 v99, v99, v99
	v_fmac_f32_e32 v97, v96, v96
	v_add_f32_e32 v64, v79, v64
	v_lshlrev_b32_e32 v100, 16, v72
	v_and_b32_e32 v103, 0xffff0000, v73
	v_mul_f32_e32 v101, v101, v101
	v_fmac_f32_e32 v99, v98, v98
	v_add_f32_e32 v64, v97, v64
	v_lshlrev_b32_e32 v102, 16, v73
	v_mul_f32_e32 v103, v103, v103
	v_fmac_f32_e32 v101, v100, v100
	v_add_f32_e32 v64, v99, v64
	v_add_f32_e32 v64, v101, v64
	v_fmac_f32_e32 v103, v102, v102
	v_add_f32_e32 v64, v103, v64
	ds_bpermute_b32 v65, v181, v64
	global_store_dwordx4 v[104:105], v[66:69], off
	global_store_dwordx4 v[104:105], v[70:73], off offset:256
	s_waitcnt lgkmcnt(0)
	v_add_f32_e32 v64, v64, v65
	ds_bpermute_b32 v65, v180, v64
	s_and_saveexec_b64 s[0:1], s[6:7]
	s_cbranch_execz .LBB0_3532
	s_waitcnt lgkmcnt(0)
	v_add_f32_e32 v66, v64, v65
	v_or_b32_e32 v64, 48, v128
	v_ashrrev_i32_e32 v65, 31, v64
	v_lshlrev_b64 v[64:65], 6, v[64:65]
	v_lshl_add_u64 v[64:65], s[20:21], 0, v[64:65]
	s_lshl_b32 s16, s2, 2
	v_lshl_add_u64 v[64:65], v[64:65], 0, s[16:17]
	v_lshl_add_u64 v[64:65], v[64:65], 0, v[152:153]
	global_store_dword v[64:65], v66, off
.LBB0_3532:
	s_or_b64 exec, exec, s[0:1]
	s_waitcnt lgkmcnt(0)
	v_lshlrev_b64 v[64:65], 11, v[160:161]
	v_lshl_add_u64 v[64:65], v[158:159], 0, v[64:65]
	v_add_co_u32_e32 v74, vcc, 0x40000, v64
	v_lshl_add_u64 v[76:77], v[64:65], 0, s[18:19]
	s_nop 0
	v_addc_co_u32_e32 v75, vcc, 0, v65, vcc
	s_mov_b32 s98, 0x48000
	s_mov_b32 s99, 0
	v_lshl_add_u64 v[210:211], v[202:203], 0, s[98:99]
	global_load_dwordx4 v[212:215], v[210:211], off offset:256
	s_mov_b32 s98, 0x50000
	s_mov_b32 s99, 0
	v_lshl_add_u64 v[210:211], v[202:203], 0, s[98:99]
	global_load_dwordx4 v[216:219], v[210:211], off
	s_waitcnt vmcnt(8)
	v_lshlrev_b32_e32 v78, 16, v220
	v_and_b32_e32 v79, 0xffff0000, v220
	v_lshlrev_b32_e32 v66, 16, v221
	v_and_b32_e32 v67, 0xffff0000, v221
	v_lshlrev_b32_e32 v96, 16, v222
	v_and_b32_e32 v97, 0xffff0000, v222
	v_lshlrev_b32_e32 v68, 16, v223
	v_and_b32_e32 v69, 0xffff0000, v223
	s_waitcnt vmcnt(5)
	v_lshlrev_b32_e32 v100, 16, v246
	v_and_b32_e32 v101, 0xffff0000, v246
	v_lshlrev_b32_e32 v72, 16, v247
	v_and_b32_e32 v73, 0xffff0000, v247
	v_pk_fma_f32 v[62:63], v[62:63], v[94:95], v[66:67]
	v_pk_fma_f32 v[60:61], v[60:61], v[92:93], v[78:79]
	v_lshlrev_b32_e32 v98, 16, v244
	v_and_b32_e32 v99, 0xffff0000, v244
	v_lshlrev_b32_e32 v70, 16, v245
	v_and_b32_e32 v71, 0xffff0000, v245
	v_pk_fma_f32 v[58:59], v[58:59], v[90:91], v[68:69]
	v_pk_fma_f32 v[56:57], v[56:57], v[88:89], v[96:97]
	v_pk_fma_f32 v[68:69], v[50:51], v[82:83], v[72:73]
	v_pk_fma_f32 v[48:49], v[48:49], v[80:81], v[100:101]
	v_cvt_pk_bf16_f32 v50, v60, v61
	v_cvt_pk_bf16_f32 v51, v62, v63
	v_pk_fma_f32 v[66:67], v[54:55], v[86:87], v[70:71]
	v_pk_fma_f32 v[54:55], v[52:53], v[84:85], v[98:99]
	v_cvt_pk_bf16_f32 v52, v56, v57
	v_cvt_pk_bf16_f32 v53, v58, v59
	v_cvt_pk_bf16_f32 v56, v48, v49
	v_and_b32_e32 v49, 0xffff0000, v50
	v_and_b32_e32 v59, 0xffff0000, v51
	v_lshlrev_b32_e32 v48, 16, v50
	v_lshlrev_b32_e32 v58, 16, v51
	v_and_b32_e32 v61, 0xffff0000, v52
	v_mul_f32_e32 v49, v49, v49
	v_mul_f32_e32 v59, v59, v59
	v_cvt_pk_bf16_f32 v54, v54, v55
	v_lshlrev_b32_e32 v60, 16, v52
	v_and_b32_e32 v63, 0xffff0000, v53
	v_mul_f32_e32 v61, v61, v61
	v_fmac_f32_e32 v49, v48, v48
	v_fmac_f32_e32 v59, v58, v58
	v_cvt_pk_bf16_f32 v55, v66, v67
	v_lshlrev_b32_e32 v62, 16, v53
	v_and_b32_e32 v67, 0xffff0000, v54
	v_mul_f32_e32 v63, v63, v63
	v_fmac_f32_e32 v61, v60, v60
	v_add_f32_e32 v48, v49, v59
	v_cvt_pk_bf16_f32 v57, v68, v69
	v_lshlrev_b32_e32 v66, 16, v54
	v_and_b32_e32 v69, 0xffff0000, v55
	v_mul_f32_e32 v67, v67, v67
	v_fmac_f32_e32 v63, v62, v62
	v_add_f32_e32 v48, v61, v48
	v_lshlrev_b32_e32 v68, 16, v55
	v_and_b32_e32 v71, 0xffff0000, v56
	v_mul_f32_e32 v69, v69, v69
	v_fmac_f32_e32 v67, v66, v66
	v_add_f32_e32 v48, v63, v48
	v_lshlrev_b32_e32 v70, 16, v56
	v_and_b32_e32 v73, 0xffff0000, v57
	v_mul_f32_e32 v71, v71, v71
	v_fmac_f32_e32 v69, v68, v68
	v_add_f32_e32 v48, v67, v48
	v_lshlrev_b32_e32 v72, 16, v57
	v_mul_f32_e32 v73, v73, v73
	v_fmac_f32_e32 v71, v70, v70
	v_add_f32_e32 v48, v69, v48
	v_add_f32_e32 v48, v71, v48
	v_fmac_f32_e32 v73, v72, v72
	v_add_f32_e32 v48, v73, v48
	ds_bpermute_b32 v49, v181, v48
	global_store_dwordx4 v[74:75], v[50:53], off
	global_store_dwordx4 v[76:77], v[54:57], off offset:256
	s_waitcnt lgkmcnt(0)
	v_add_f32_e32 v48, v48, v49
	ds_bpermute_b32 v49, v180, v48
	s_and_saveexec_b64 s[0:1], s[6:7]
	s_cbranch_execz .LBB0_3534
	s_waitcnt lgkmcnt(0)
	v_add_f32_e32 v50, v48, v49
	v_lshlrev_b64 v[48:49], 6, v[128:129]
	v_lshl_add_u64 v[48:49], s[20:21], 0, v[48:49]
	s_lshl_b32 s16, s2, 2
	v_lshl_add_u64 v[48:49], v[48:49], 0, s[16:17]
	v_lshl_add_u64 v[48:49], v[48:49], 0, v[152:153]
	v_add_co_u32_e32 v48, vcc, 0x2000, v48
	s_nop 1
	v_addc_co_u32_e32 v49, vcc, 0, v49, vcc
	global_store_dword v[48:49], v50, off
.LBB0_3534:
	s_or_b64 exec, exec, s[0:1]
	v_add_co_u32_e32 v56, vcc, 0x48000, v64
	v_lshl_add_u64 v[58:59], v[64:65], 0, s[24:25]
	s_nop 0
	v_addc_co_u32_e32 v57, vcc, 0, v65, vcc
	s_waitcnt lgkmcnt(0)
	s_mov_b32 s98, 0x50000
	s_mov_b32 s99, 0
	v_lshl_add_u64 v[210:211], v[202:203], 0, s[98:99]
	global_load_dwordx4 v[220:223], v[210:211], off offset:256
	s_mov_b32 s98, 0x58000
	s_mov_b32 s99, 0
	v_lshl_add_u64 v[210:211], v[202:203], 0, s[98:99]
	global_load_dwordx4 v[244:247], v[210:211], off
	s_waitcnt vmcnt(8)
	v_lshlrev_b32_e32 v60, 16, v204
	v_and_b32_e32 v61, 0xffff0000, v204
	v_lshlrev_b32_e32 v48, 16, v205
	v_and_b32_e32 v49, 0xffff0000, v205
	v_lshlrev_b32_e32 v62, 16, v206
	v_and_b32_e32 v63, 0xffff0000, v206
	v_lshlrev_b32_e32 v50, 16, v207
	v_and_b32_e32 v51, 0xffff0000, v207
	s_waitcnt vmcnt(5)
	v_lshlrev_b32_e32 v66, 16, v214
	v_and_b32_e32 v67, 0xffff0000, v214
	v_lshlrev_b32_e32 v54, 16, v215
	v_and_b32_e32 v55, 0xffff0000, v215
	v_pk_fma_f32 v[46:47], v[46:47], v[94:95], v[48:49]
	v_pk_fma_f32 v[44:45], v[44:45], v[92:93], v[60:61]
	v_lshlrev_b32_e32 v64, 16, v212
	v_and_b32_e32 v65, 0xffff0000, v212
	v_lshlrev_b32_e32 v52, 16, v213
	v_and_b32_e32 v53, 0xffff0000, v213
	v_pk_fma_f32 v[42:43], v[42:43], v[90:91], v[50:51]
	v_pk_fma_f32 v[40:41], v[40:41], v[88:89], v[62:63]
	v_pk_fma_f32 v[50:51], v[34:35], v[82:83], v[54:55]
	v_pk_fma_f32 v[32:33], v[32:33], v[80:81], v[66:67]
	v_cvt_pk_bf16_f32 v34, v44, v45
	v_cvt_pk_bf16_f32 v35, v46, v47
	v_pk_fma_f32 v[48:49], v[38:39], v[86:87], v[52:53]
	v_pk_fma_f32 v[38:39], v[36:37], v[84:85], v[64:65]
	v_cvt_pk_bf16_f32 v36, v40, v41
	v_cvt_pk_bf16_f32 v37, v42, v43
	v_cvt_pk_bf16_f32 v40, v32, v33
	v_and_b32_e32 v33, 0xffff0000, v34
	v_and_b32_e32 v43, 0xffff0000, v35
	v_lshlrev_b32_e32 v32, 16, v34
	v_lshlrev_b32_e32 v42, 16, v35
	v_and_b32_e32 v45, 0xffff0000, v36
	v_mul_f32_e32 v33, v33, v33
	v_mul_f32_e32 v43, v43, v43
	v_cvt_pk_bf16_f32 v38, v38, v39
	v_lshlrev_b32_e32 v44, 16, v36
	v_and_b32_e32 v47, 0xffff0000, v37
	v_mul_f32_e32 v45, v45, v45
	v_fmac_f32_e32 v33, v32, v32
	v_fmac_f32_e32 v43, v42, v42
	v_cvt_pk_bf16_f32 v39, v48, v49
	v_lshlrev_b32_e32 v46, 16, v37
	v_and_b32_e32 v49, 0xffff0000, v38
	v_mul_f32_e32 v47, v47, v47
	v_fmac_f32_e32 v45, v44, v44
	v_add_f32_e32 v32, v33, v43
	v_cvt_pk_bf16_f32 v41, v50, v51
	v_lshlrev_b32_e32 v48, 16, v38
	v_and_b32_e32 v51, 0xffff0000, v39
	v_mul_f32_e32 v49, v49, v49
	v_fmac_f32_e32 v47, v46, v46
	v_add_f32_e32 v32, v45, v32
	v_lshlrev_b32_e32 v50, 16, v39
	v_and_b32_e32 v53, 0xffff0000, v40
	v_mul_f32_e32 v51, v51, v51
	v_fmac_f32_e32 v49, v48, v48
	v_add_f32_e32 v32, v47, v32
	v_lshlrev_b32_e32 v52, 16, v40
	v_and_b32_e32 v55, 0xffff0000, v41
	v_mul_f32_e32 v53, v53, v53
	v_fmac_f32_e32 v51, v50, v50
	v_add_f32_e32 v32, v49, v32
	v_lshlrev_b32_e32 v54, 16, v41
	v_mul_f32_e32 v55, v55, v55
	v_fmac_f32_e32 v53, v52, v52
	v_add_f32_e32 v32, v51, v32
	v_add_f32_e32 v32, v53, v32
	v_fmac_f32_e32 v55, v54, v54
	v_add_f32_e32 v32, v55, v32
	ds_bpermute_b32 v33, v181, v32
	global_store_dwordx4 v[56:57], v[34:37], off
	global_store_dwordx4 v[58:59], v[38:41], off offset:256
	s_waitcnt lgkmcnt(0)
	v_add_f32_e32 v32, v32, v33
	ds_bpermute_b32 v33, v180, v32
	s_and_saveexec_b64 s[0:1], s[6:7]
	s_cbranch_execz .LBB0_3536
	s_waitcnt lgkmcnt(0)
	v_add_f32_e32 v34, v32, v33
	v_lshlrev_b64 v[32:33], 6, v[128:129]
	v_lshl_add_u64 v[32:33], s[20:21], 0, v[32:33]
	s_lshl_b32 s16, s2, 2
	v_lshl_add_u64 v[32:33], v[32:33], 0, s[16:17]
	v_lshl_add_u64 v[32:33], v[32:33], 0, v[152:153]
	v_add_co_u32_e32 v32, vcc, 0x2000, v32
	s_nop 1
	v_addc_co_u32_e32 v33, vcc, 0, v33, vcc
	global_store_dword v[32:33], v34, off offset:1024
.LBB0_3536:
	s_or_b64 exec, exec, s[0:1]
	s_waitcnt lgkmcnt(0)
	v_lshlrev_b64 v[32:33], 11, v[160:161]
	v_lshl_add_u64 v[32:33], v[158:159], 0, v[32:33]
	v_add_co_u32_e32 v42, vcc, 0x50000, v32
	v_lshl_add_u64 v[44:45], v[32:33], 0, s[26:27]
	s_nop 0
	v_addc_co_u32_e32 v43, vcc, 0, v33, vcc
	s_mov_b32 s98, 0x58000
	s_mov_b32 s99, 0
	v_lshl_add_u64 v[210:211], v[202:203], 0, s[98:99]
	global_load_dwordx4 v[204:207], v[210:211], off offset:256
	s_waitcnt vmcnt(7)
	v_lshlrev_b32_e32 v46, 16, v216
	v_and_b32_e32 v47, 0xffff0000, v216
	v_lshlrev_b32_e32 v34, 16, v217
	v_and_b32_e32 v35, 0xffff0000, v217
	v_lshlrev_b32_e32 v48, 16, v218
	v_and_b32_e32 v49, 0xffff0000, v218
	v_lshlrev_b32_e32 v36, 16, v219
	v_and_b32_e32 v37, 0xffff0000, v219
	s_waitcnt vmcnt(4)
	v_lshlrev_b32_e32 v52, 16, v222
	v_and_b32_e32 v53, 0xffff0000, v222
	v_lshlrev_b32_e32 v40, 16, v223
	v_and_b32_e32 v41, 0xffff0000, v223
	v_pk_fma_f32 v[30:31], v[30:31], v[94:95], v[34:35]
	v_pk_fma_f32 v[28:29], v[28:29], v[92:93], v[46:47]
	v_lshlrev_b32_e32 v50, 16, v220
	v_and_b32_e32 v51, 0xffff0000, v220
	v_lshlrev_b32_e32 v38, 16, v221
	v_and_b32_e32 v39, 0xffff0000, v221
	v_pk_fma_f32 v[26:27], v[26:27], v[90:91], v[36:37]
	v_pk_fma_f32 v[24:25], v[24:25], v[88:89], v[48:49]
	v_pk_fma_f32 v[36:37], v[18:19], v[82:83], v[40:41]
	v_pk_fma_f32 v[16:17], v[16:17], v[80:81], v[52:53]
	v_cvt_pk_bf16_f32 v18, v28, v29
	v_cvt_pk_bf16_f32 v19, v30, v31
	v_pk_fma_f32 v[34:35], v[22:23], v[86:87], v[38:39]
	v_pk_fma_f32 v[22:23], v[20:21], v[84:85], v[50:51]
	v_cvt_pk_bf16_f32 v20, v24, v25
	v_cvt_pk_bf16_f32 v21, v26, v27
	v_cvt_pk_bf16_f32 v24, v16, v17
	v_and_b32_e32 v17, 0xffff0000, v18
	v_and_b32_e32 v27, 0xffff0000, v19
	v_lshlrev_b32_e32 v16, 16, v18
	v_lshlrev_b32_e32 v26, 16, v19
	v_and_b32_e32 v29, 0xffff0000, v20
	v_mul_f32_e32 v17, v17, v17
	v_mul_f32_e32 v27, v27, v27
	v_cvt_pk_bf16_f32 v22, v22, v23
	v_lshlrev_b32_e32 v28, 16, v20
	v_and_b32_e32 v31, 0xffff0000, v21
	v_mul_f32_e32 v29, v29, v29
	v_fmac_f32_e32 v17, v16, v16
	v_fmac_f32_e32 v27, v26, v26
	v_cvt_pk_bf16_f32 v23, v34, v35
	v_lshlrev_b32_e32 v30, 16, v21
	v_and_b32_e32 v35, 0xffff0000, v22
	v_mul_f32_e32 v31, v31, v31
	v_fmac_f32_e32 v29, v28, v28
	v_add_f32_e32 v16, v17, v27
	v_cvt_pk_bf16_f32 v25, v36, v37
	v_lshlrev_b32_e32 v34, 16, v22
	v_and_b32_e32 v37, 0xffff0000, v23
	v_mul_f32_e32 v35, v35, v35
	v_fmac_f32_e32 v31, v30, v30
	v_add_f32_e32 v16, v29, v16
	v_lshlrev_b32_e32 v36, 16, v23
	v_and_b32_e32 v39, 0xffff0000, v24
	v_mul_f32_e32 v37, v37, v37
	v_fmac_f32_e32 v35, v34, v34
	v_add_f32_e32 v16, v31, v16
	v_lshlrev_b32_e32 v38, 16, v24
	v_and_b32_e32 v41, 0xffff0000, v25
	v_mul_f32_e32 v39, v39, v39
	v_fmac_f32_e32 v37, v36, v36
	v_add_f32_e32 v16, v35, v16
	v_lshlrev_b32_e32 v40, 16, v25
	v_mul_f32_e32 v41, v41, v41
	v_fmac_f32_e32 v39, v38, v38
	v_add_f32_e32 v16, v37, v16
	v_add_f32_e32 v16, v39, v16
	v_fmac_f32_e32 v41, v40, v40
	v_add_f32_e32 v16, v41, v16
	ds_bpermute_b32 v17, v181, v16
	global_store_dwordx4 v[42:43], v[18:21], off
	global_store_dwordx4 v[44:45], v[22:25], off offset:256
	s_waitcnt lgkmcnt(0)
	v_add_f32_e32 v16, v16, v17
	ds_bpermute_b32 v17, v180, v16
	s_and_saveexec_b64 s[0:1], s[6:7]
	s_cbranch_execz .LBB0_3538
	s_waitcnt lgkmcnt(0)
	v_add_f32_e32 v18, v16, v17
	v_lshlrev_b64 v[16:17], 6, v[128:129]
	v_lshl_add_u64 v[16:17], s[20:21], 0, v[16:17]
	s_lshl_b32 s16, s2, 2
	v_lshl_add_u64 v[16:17], v[16:17], 0, s[16:17]
	v_lshl_add_u64 v[16:17], v[16:17], 0, v[152:153]
	v_add_co_u32_e32 v16, vcc, 0x2000, v16
	s_nop 1
	v_addc_co_u32_e32 v17, vcc, 0, v17, vcc
	global_store_dword v[16:17], v18, off offset:2048
.LBB0_3538:
	s_or_b64 exec, exec, s[0:1]
	v_add_co_u32_e32 v24, vcc, 0x58000, v32
	v_lshl_add_u64 v[26:27], v[32:33], 0, s[28:29]
	s_nop 0
	v_addc_co_u32_e32 v25, vcc, 0, v33, vcc
	s_waitcnt lgkmcnt(0)
	s_waitcnt vmcnt(5)
	v_lshlrev_b32_e32 v28, 16, v244
	v_and_b32_e32 v29, 0xffff0000, v244
	v_lshlrev_b32_e32 v16, 16, v245
	v_and_b32_e32 v17, 0xffff0000, v245
	v_lshlrev_b32_e32 v30, 16, v246
	v_and_b32_e32 v31, 0xffff0000, v246
	v_lshlrev_b32_e32 v18, 16, v247
	v_and_b32_e32 v19, 0xffff0000, v247
	s_waitcnt vmcnt(2)
	v_lshlrev_b32_e32 v34, 16, v206
	v_and_b32_e32 v35, 0xffff0000, v206
	v_lshlrev_b32_e32 v22, 16, v207
	v_and_b32_e32 v23, 0xffff0000, v207
	v_pk_fma_f32 v[14:15], v[14:15], v[94:95], v[16:17]
	v_pk_fma_f32 v[12:13], v[12:13], v[92:93], v[28:29]
	v_lshlrev_b32_e32 v32, 16, v204
	v_and_b32_e32 v33, 0xffff0000, v204
	v_lshlrev_b32_e32 v20, 16, v205
	v_and_b32_e32 v21, 0xffff0000, v205
	v_pk_fma_f32 v[10:11], v[10:11], v[90:91], v[18:19]
	v_pk_fma_f32 v[8:9], v[8:9], v[88:89], v[30:31]
	v_pk_fma_f32 v[18:19], v[2:3], v[82:83], v[22:23]
	v_pk_fma_f32 v[0:1], v[0:1], v[80:81], v[34:35]
	v_cvt_pk_bf16_f32 v2, v12, v13
	v_cvt_pk_bf16_f32 v3, v14, v15
	v_pk_fma_f32 v[16:17], v[6:7], v[86:87], v[20:21]
	v_pk_fma_f32 v[6:7], v[4:5], v[84:85], v[32:33]
	v_cvt_pk_bf16_f32 v4, v8, v9
	v_cvt_pk_bf16_f32 v5, v10, v11
	v_cvt_pk_bf16_f32 v8, v0, v1
	v_and_b32_e32 v1, 0xffff0000, v2
	v_and_b32_e32 v11, 0xffff0000, v3
	v_lshlrev_b32_e32 v0, 16, v2
	v_lshlrev_b32_e32 v10, 16, v3
	v_and_b32_e32 v13, 0xffff0000, v4
	v_mul_f32_e32 v1, v1, v1
	v_mul_f32_e32 v11, v11, v11
	v_cvt_pk_bf16_f32 v6, v6, v7
	v_lshlrev_b32_e32 v12, 16, v4
	v_and_b32_e32 v15, 0xffff0000, v5
	v_mul_f32_e32 v13, v13, v13
	v_fmac_f32_e32 v1, v0, v0
	v_fmac_f32_e32 v11, v10, v10
	v_cvt_pk_bf16_f32 v7, v16, v17
	v_lshlrev_b32_e32 v14, 16, v5
	v_and_b32_e32 v17, 0xffff0000, v6
	v_mul_f32_e32 v15, v15, v15
	v_fmac_f32_e32 v13, v12, v12
	v_add_f32_e32 v0, v1, v11
	v_cvt_pk_bf16_f32 v9, v18, v19
	v_lshlrev_b32_e32 v16, 16, v6
	v_and_b32_e32 v19, 0xffff0000, v7
	v_mul_f32_e32 v17, v17, v17
	v_fmac_f32_e32 v15, v14, v14
	v_add_f32_e32 v0, v13, v0
	v_lshlrev_b32_e32 v18, 16, v7
	v_and_b32_e32 v21, 0xffff0000, v8
	v_mul_f32_e32 v19, v19, v19
	v_fmac_f32_e32 v17, v16, v16
	v_add_f32_e32 v0, v15, v0
	v_lshlrev_b32_e32 v20, 16, v8
	v_and_b32_e32 v23, 0xffff0000, v9
	v_mul_f32_e32 v21, v21, v21
	v_fmac_f32_e32 v19, v18, v18
	v_add_f32_e32 v0, v17, v0
	v_lshlrev_b32_e32 v22, 16, v9
	v_mul_f32_e32 v23, v23, v23
	v_fmac_f32_e32 v21, v20, v20
	v_add_f32_e32 v0, v19, v0
	v_add_f32_e32 v0, v21, v0
	v_fmac_f32_e32 v23, v22, v22
	v_add_f32_e32 v0, v23, v0
	ds_bpermute_b32 v1, v181, v0
	global_store_dwordx4 v[24:25], v[2:5], off
	global_store_dwordx4 v[26:27], v[6:9], off offset:256
	s_waitcnt lgkmcnt(0)
	v_add_f32_e32 v0, v0, v1
	ds_bpermute_b32 v1, v180, v0
	s_and_saveexec_b64 s[0:1], s[6:7]
	s_cbranch_execz .LBB0_3517
	s_waitcnt lgkmcnt(0)
	v_add_f32_e32 v2, v0, v1
	v_lshlrev_b64 v[0:1], 6, v[128:129]
	v_lshl_add_u64 v[0:1], s[20:21], 0, v[0:1]
	s_lshl_b32 s16, s2, 2
	v_lshl_add_u64 v[0:1], v[0:1], 0, s[16:17]
	v_lshl_add_u64 v[0:1], v[0:1], 0, v[152:153]
	v_add_co_u32_e32 v0, vcc, 0x2000, v0
	s_nop 1
	v_addc_co_u32_e32 v1, vcc, 0, v1, vcc
	global_store_dword v[0:1], v2, off offset:3072
	s_branch .LBB0_3517

.LBB0_3620:
	s_or_b64 exec, exec, s[0:1]
	v_readlane_b32 s0, v242, 1
	s_waitcnt lgkmcnt(0)
	s_barrier
	s_nop 0
	s_mov_b32 s2, 0
	v_readlane_b32 s1, v242, 2
	s_load_dwordx2 s[20:21], s[0:1], s2 offset:0x108
	s_nop 0
	s_load_dwordx2 s[0:1], s[0:1], s2 offset:0x38
	v_mov_b32_e32 v68, v208
	s_mov_b32 s4, 0x8000
	s_waitcnt lgkmcnt(0)
	s_add_u32 s48, s20, 0x4000
	s_addc_u32 s49, s21, 0
	s_add_u32 s22, s20, 0x35df000
	s_addc_u32 s23, s21, 0
	s_add_u32 s2, s20, 0x2d1f000
	s_addc_u32 s3, s21, 0
	v_ashrrev_i32_e32 v69, 31, v68
	v_lshl_add_u64 v[16:17], v[68:69], 4, s[2:3]
	v_add_u32_e32 v32, 0x200, v68
	v_add_u32_e32 v34, 0x400, v68
	v_add_u32_e32 v36, 0x600, v68
	v_ashrrev_i32_e32 v33, 31, v32
	v_ashrrev_i32_e32 v35, 31, v34
	v_ashrrev_i32_e32 v37, 31, v36
	v_add_co_u32_e32 v24, vcc, s4, v16
	v_add_u32_e32 v38, 0xa00, v68
	v_lshl_add_u64 v[8:9], v[32:33], 4, s[2:3]
	v_lshl_add_u64 v[18:19], v[34:35], 4, s[2:3]
	v_lshl_add_u64 v[20:21], v[36:37], 4, s[2:3]
	v_addc_co_u32_e32 v25, vcc, 0, v17, vcc
	v_ashrrev_i32_e32 v39, 31, v38
	v_add_u32_e32 v40, 0xc00, v68
	global_load_dwordx4 v[0:3], v[16:17], off
	global_load_dwordx4 v[4:7], v[8:9], off
	s_nop 0
	global_load_dwordx4 v[8:11], v[18:19], off
	global_load_dwordx4 v[12:15], v[20:21], off
	v_lshl_add_u64 v[26:27], v[38:39], 4, s[2:3]
	global_load_dwordx4 v[16:19], v[24:25], off
	global_load_dwordx4 v[20:23], v[26:27], off
	v_ashrrev_i32_e32 v41, 31, v40
	v_lshl_add_u64 v[24:25], v[40:41], 4, s[2:3]
	global_load_dwordx4 v[24:27], v[24:25], off
	v_add_u32_e32 v42, 0xe00, v68
	v_ashrrev_i32_e32 v43, 31, v42
	v_lshl_add_u64 v[28:29], v[42:43], 4, s[2:3]
	global_load_dwordx4 v[28:31], v[28:29], off
	s_movk_i32 s50, 0x800
	s_add_i32 s4, 0, 0x8100
	v_mov_b32_e32 v48, s4
	v_cmp_gt_u32_e32 vcc, s50, v68
	s_movk_i32 s3, 0xf7ff
	v_bfe_u32 v44, v34, 7, 4
	v_cndmask_b32_e64 v49, v48, 0, vcc
	v_cmp_gt_u32_e32 vcc, s50, v32
	v_bfe_u32 v39, v68, 7, 4
	v_lshlrev_b32_e32 v41, 4, v68
	v_cndmask_b32_e64 v50, v48, 0, vcc
	v_cmp_gt_u32_e32 vcc, s50, v34
	v_bfe_u32 v45, v36, 7, 4
	v_mul_u32_u24_e32 v39, 0x810, v39
	v_cndmask_b32_e64 v34, v48, 0, vcc
	v_cmp_gt_u32_e32 vcc, s50, v36
	v_and_b32_e32 v41, 0x7f0, v41
	v_bfe_u32 v43, v32, 7, 4
	v_cndmask_b32_e64 v36, v48, 0, vcc
	v_cmp_lt_u32_e32 vcc, s3, v68
	v_bfe_u32 v46, v38, 7, 4
	v_bfe_u32 v47, v40, 7, 4
	v_cndmask_b32_e64 v51, v48, 0, vcc
	v_cmp_gt_u32_e32 vcc, s50, v38
	v_mul_u32_u24_e32 v43, 0x810, v43
	v_mul_u32_u24_e32 v44, 0x810, v44
	v_mul_u32_u24_e32 v45, 0x810, v45
	v_mul_u32_u24_e32 v46, 0x810, v46
	v_cndmask_b32_e64 v38, v48, 0, vcc
	v_cmp_gt_u32_e32 vcc, s50, v40
	v_add3_u32 v49, v49, v39, v41
	v_add3_u32 v43, v50, v43, v41
	v_cndmask_b32_e64 v40, v48, 0, vcc
	v_add3_u32 v34, v34, v44, v41
	v_add3_u32 v36, v36, v45, v41
	v_add3_u32 v39, v51, v39, v41
	v_add3_u32 v38, v38, v46, v41
	s_add_u32 s26, s0, 0x3000
	v_cmp_gt_u32_e32 vcc, s50, v42
	s_addc_u32 s27, s1, 0
	s_sub_i32 s0, 0x800, s79
	v_readlane_b32 s1, v242, 0
	s_cmp_lt_i32 s1, s0
	v_readlane_b32 s0, v242, 30
	v_ashrrev_i32_e32 v33, 6, v68
	v_bfe_u32 v37, v68, 4, 2
	v_and_b32_e32 v90, 15, v68
	v_mov_b32_e32 v71, 0
	v_lshlrev_b32_e32 v93, 2, v68
	v_lshlrev_b32_e32 v70, 4, v37
	s_waitcnt vmcnt(7)
	ds_write_b128 v49, v[0:3]
	s_waitcnt vmcnt(6)
	ds_write_b128 v43, v[4:7]
	s_waitcnt vmcnt(5)
	ds_write_b128 v34, v[8:11]
	s_waitcnt vmcnt(4)
	ds_write_b128 v36, v[12:15]
	s_waitcnt vmcnt(3)
	ds_write_b128 v39, v[16:19]
	s_waitcnt vmcnt(2)
	ds_write_b128 v38, v[20:23]
	v_mul_u32_u24_e32 v0, 0x810, v47
	v_add3_u32 v0, v40, v0, v41
	s_waitcnt vmcnt(1)
	ds_write_b128 v0, v[24:27]
	v_bfe_u32 v0, v42, 7, 4
	v_cndmask_b32_e64 v1, v48, 0, vcc
	v_mul_u32_u24_e32 v0, 0x810, v0
	v_add3_u32 v0, v1, v0, v41
	v_mov_b32_e32 v1, s0
	v_readlane_b32 s0, v242, 16
	s_waitcnt vmcnt(0)
	ds_write_b128 v0, v[28:31]
	v_mov_b32_e32 v0, 0x800
	v_cmp_gt_u32_e32 vcc, 64, v68
	v_add_u32_e32 v92, s0, v33
	v_readlane_b32 s0, v242, 32
	v_cndmask_b32_e32 v91, v0, v1, vcc
	v_mul_u32_u24_e32 v0, 0x408, v90
	v_add_u32_e32 v94, s0, v93
	v_readlane_b32 s0, v242, 33
	v_lshlrev_b32_e32 v2, 5, v37
	v_mov_b32_e32 v3, v71
	v_add_u32_e32 v95, s0, v93
	v_lshlrev_b32_e32 v5, 1, v0
	v_lshl_add_u32 v97, v90, 2, s0
	v_mul_u32_u24_e32 v0, 0x22000, v90
	v_mov_b32_e32 v1, v71
	v_lshl_add_u64 v[2:3], s[20:21], 0, v[2:3]
	s_mov_b64 s[0:1], 0x37ff000
	v_lshl_add_u64 v[72:73], v[2:3], 0, s[0:1]
	v_lshl_add_u64 v[2:3], s[20:21], 0, v[70:71]
	s_mov_b64 s[0:1], 0xdbff000
	v_lshl_add_u64 v[0:1], s[20:21], 0, v[0:1]
	v_lshl_add_u64 v[74:75], v[2:3], 0, s[0:1]
	v_lshl_add_u64 v[0:1], v[0:1], 0, v[70:71]
	s_mov_b64 s[0:1], 0x907000
	v_lshl_add_u64 v[76:77], v[0:1], 0, s[0:1]
	v_max_i32_e32 v0, 0x200, v68
	v_sub_u32_e32 v0, v0, v68
	v_add_u32_e32 v0, 0x1ff, v0
	v_lshrrev_b32_e32 v1, 9, v0
	v_add_u32_e32 v2, 1, v1
	v_add_u32_e32 v1, -1, v1
	v_lshrrev_b32_e32 v3, 1, v1
	s_movk_i32 s51, 0x1ff
	v_add_u32_e32 v3, 1, v3
	s_movk_i32 s2, 0x400
	v_lshrrev_b32_e32 v35, 4, v68
	v_lshlrev_b32_e32 v4, 1, v68
	v_cmp_lt_u32_e64 s[8:9], s51, v0
	v_and_b32_e32 v0, 0xfffffe, v2
	v_and_b32_e32 v6, 3, v3
	v_add_u32_e32 v109, 0, v93
	s_movk_i32 s0, 0xffe0
	s_mov_b32 s25, 0
	s_cselect_b64 s[28:29], -1, 0
	v_cmp_gt_i32_e64 s[4:5], s2, v68
	v_cmp_gt_i32_e64 s[6:7], 16, v68
	v_add_u32_e32 v96, 0, v5
	v_or_b32_e32 v98, 31, v4
	v_or_b32_e32 v99, 8, v70
	v_or_b32_e32 v100, 4, v70
	v_or_b32_e32 v101, 12, v70
	v_lshl_add_u32 v78, v0, 9, v68
	v_mov_b32_e32 v80, v68
	v_mov_b32_e32 v81, v32
	v_cmp_lt_u32_e64 s[10:11], 5, v1
	v_and_b32_e32 v71, -4, v3
	v_cmp_ne_u32_e64 s[12:13], 0, v6
	v_cmp_ne_u32_e64 s[14:15], v2, v0
	v_or_b32_e32 v102, 64, v70
	v_or_b32_e32 v103, 0x80, v70
	v_or_b32_e32 v104, 0xc0, v70
	v_or_b32_e32 v105, 0x100, v70
	v_or_b32_e32 v106, 0x140, v70
	v_or_b32_e32 v107, 0x180, v70
	v_or_b32_e32 v108, 0x1c0, v70
	v_add_u32_e32 v110, 0x10200, v109
	v_lshlrev_b32_e32 v111, 12, v6
	v_lshl_add_u32 v112, v35, 6, v5
	v_and_or_b32 v113, v4, s0, 2
	v_lshlrev_b32_e32 v114, 7, v35
	s_mov_b64 s[0:1], -1
	s_movk_i32 s52, 0x4000
	s_movk_i32 s53, 0x3000
	v_mov_b32_e32 v115, 0x358637bd
	s_mov_b32 s54, 0xf800000
	v_mov_b32_e32 v116, 0x260
	s_mov_b64 s[18:19], -1
	s_branch .LBB0_3624

	.amdhsa_kernel _Z5k_all5KArgs
		.amdhsa_group_segment_fixed_size 0
		.amdhsa_private_segment_fixed_size 0
		.amdhsa_kernarg_size 528
		.amdhsa_user_sgpr_count 2
		.amdhsa_user_sgpr_dispatch_ptr 0
		.amdhsa_user_sgpr_queue_ptr 0
		.amdhsa_user_sgpr_kernarg_segment_ptr 1
		.amdhsa_user_sgpr_dispatch_id 0
		.amdhsa_user_sgpr_kernarg_preload_length 0
		.amdhsa_user_sgpr_kernarg_preload_offset 0
		.amdhsa_user_sgpr_private_segment_size 0
		.amdhsa_uses_dynamic_stack 0
		.amdhsa_enable_private_segment 0
		.amdhsa_system_sgpr_workgroup_id_x 1
		.amdhsa_system_sgpr_workgroup_id_y 0
		.amdhsa_system_sgpr_workgroup_id_z 0
		.amdhsa_system_sgpr_workgroup_info 0
		.amdhsa_system_vgpr_workitem_id 0
		.amdhsa_next_free_vgpr 248
		.amdhsa_next_free_sgpr 102
		.amdhsa_accum_offset 248
		.amdhsa_reserve_vcc 1
		.amdhsa_float_round_mode_32 0
		.amdhsa_float_round_mode_16_64 0
		.amdhsa_float_denorm_mode_32 3
		.amdhsa_float_denorm_mode_16_64 3
		.amdhsa_dx10_clamp 1
		.amdhsa_ieee_mode 1
		.amdhsa_fp16_overflow 0
		.amdhsa_tg_split 0
		.amdhsa_exception_fp_ieee_invalid_op 0
		.amdhsa_exception_fp_denorm_src 0
		.amdhsa_exception_fp_ieee_div_zero 0
		.amdhsa_exception_fp_ieee_overflow 0
		.amdhsa_exception_fp_ieee_underflow 0
		.amdhsa_exception_fp_ieee_inexact 0
		.amdhsa_exception_int_div_zero 0
	.end_amdhsa_kernel

amdhsa.kernels:
  - .agpr_count:     0
    .args:
      - .offset:         0
        .size:           272
        .value_kind:     by_value
      - .offset:         272
        .size:           4
        .value_kind:     hidden_block_count_x
      - .offset:         276
        .size:           4
        .value_kind:     hidden_block_count_y
      - .offset:         280
        .size:           4
        .value_kind:     hidden_block_count_z
      - .offset:         284
        .size:           2
        .value_kind:     hidden_group_size_x
      - .offset:         286
        .size:           2
        .value_kind:     hidden_group_size_y
      - .offset:         288
        .size:           2
        .value_kind:     hidden_group_size_z
      - .offset:         290
        .size:           2
        .value_kind:     hidden_remainder_x
      - .offset:         292
        .size:           2
        .value_kind:     hidden_remainder_y
      - .offset:         294
        .size:           2
        .value_kind:     hidden_remainder_z
      - .offset:         312
        .size:           8
        .value_kind:     hidden_global_offset_x
      - .offset:         320
        .size:           8
        .value_kind:     hidden_global_offset_y
      - .offset:         328
        .size:           8
        .value_kind:     hidden_global_offset_z
      - .offset:         336
        .size:           2
        .value_kind:     hidden_grid_dims
      - .offset:         392
        .size:           4
        .value_kind:     hidden_dynamic_lds_size
    .group_segment_fixed_size: 0
    .kernarg_segment_align: 8
    .kernarg_segment_size: 528
    .language:       OpenCL C
    .language_version:
      - 2
      - 0
    .max_flat_workgroup_size: 512
    .name:           _Z5k_all5KArgs
    .private_segment_fixed_size: 0
    .sgpr_count:     108
    .sgpr_spill_count: 115
    .symbol:         _Z5k_all5KArgs.kd
    .uniform_work_group_size: 1
    .uses_dynamic_stack: false
    .vgpr_count:     248
    .vgpr_spill_count: 0
    .wavefront_size: 64
